# remove redundant setprio 0/1 pairs and post-barrier lgkmcnt(0) in GEMM K-loops
# speedup vs baseline: 1.0020x; 1.0020x over previous
; #define PG8_STAGE(bufoff, gbase, voff) do { _Pragma("unroll") for (int _i = 0; _i < 2; ++_i) \
;         __builtin_amdgcn_global_load_lds((const unsigned*)((const char*)(gbase) + (voff)[_i]), (PG8_LAS unsigned*)(lds + (bufoff) + ldsw + _i * 8192), 16, 0, 0); } while (0)
; #define PG8_LDA(dst, b, h) do { _Pragma("unroll") for (int m = 0; m < 4; ++m) _Pragma("unroll") for (int k = 0; k < 2; ++k) dst[m][k] = *(const PG8_LAS bf16x8*)(lds + PG8_SA(b, h) + aoff + m * 2048 + k * 1024); } while (0)
; #define PG8_LDB(dst, b, h) do { _Pragma("unroll") for (int n = 0; n < 2; ++n) _Pragma("unroll") for (int k = 0; k < 2; ++k) dst[n][k] = *(const PG8_LAS bf16x8*)(lds + PG8_SB(b, h) + boff + n * 2048 + k * 1024); } while (0)
; #define PG8_MMA(ai, bj, At, Bt) do { __builtin_amdgcn_s_setprio(1); _Pragma("unroll") for (int m = 0; m < 4; ++m) _Pragma("unroll") for (int n = 0; n < 2; ++n) _Pragma("unroll") for (int k = 0; k < 2; ++k) \
;         acc[ai][bj][m][n] = __builtin_amdgcn_mfma_f32_16x16x32_bf16(Bt[n][k], At[m][k], acc[ai][bj][m][n], 0, 0, 0); __builtin_amdgcn_s_setprio(0); } while (0)
; #define PG8_WAIT_V(n) asm volatile("s_waitcnt vmcnt(" #n ")" ::: "memory")
; #define PG8_WAIT_L(n) asm volatile("s_waitcnt lgkmcnt(" #n ")" ::: "memory")
; #define PG8_BAR __builtin_amdgcn_s_barrier()
; #define PG8_SCHED __builtin_amdgcn_sched_barrier(0)
; template <class Epi, class Sched, bool ALIGN_EPI = false>
; __device__ __forceinline__ void gemm_phase(PG8_LAS unsigned char* lds, const Gemm g, const Sched& S, const Epi& E) {
;     ...
;             PG8_LDB(B0, 0, 0); PG8_LDB(B1, 0, 1); PG8_SCHED; PG8_LDA(At, 0, 0); PG8_STAGE(PG8_SA(1, 1), a1 + hstepA, vc1);
;             PG8_WAIT_V(8); PG8_WAIT_L(0); PG8_BAR; PG8_MMA(0, 0, At, B0); PG8_MMA(0, 1, At, B1); PG8_BAR; PG8_SCHED;
;             PG8_LDA(At, 0, 1); PG8_STAGE(PG8_SB(0, 0), b2, voffB); PG8_STAGE(PG8_SB(0, 1), b2 + hstep, voffB); PG8_STAGE(PG8_SA(0, 0), a2, w0);
;             PG8_WAIT_V(8); PG8_WAIT_L(0); PG8_BAR; PG8_MMA(1, 0, At, B0); PG8_MMA(1, 1, At, B1); PG8_BAR; PG8_SCHED;
.LBB0_247:
	ds_read_b128 v[132:135], v191
	ds_read_b128 v[136:139], v191 offset:1024
	ds_read_b128 v[140:143], v191 offset:2048
	ds_read_b128 v[144:147], v191 offset:3072
	ds_read_b128 v[148:151], v193
	ds_read_b128 v[152:155], v193 offset:1024
	ds_read_b128 v[156:159], v193 offset:2048
	ds_read_b128 v[196:199], v193 offset:3072
	s_add_u32 s52, s50, 0xfff80080
	s_addc_u32 s53, s51, -1
	s_cmp_eq_u32 s80, 28
	s_cselect_b32 s55, s9, s53
	s_cselect_b32 s54, s76, s52
	s_cselect_b32 s53, s45, s79
	s_cselect_b32 s52, s77, s78
	v_lshl_add_u64 v[160:161], s[50:51], 0, v[172:173]
	s_add_i32 m0, s59, 0xc000
	ds_read_b128 v[204:207], v195
	ds_read_b128 v[210:213], v195 offset:1024
	ds_read_b128 v[214:217], v195 offset:2048
	ds_read_b128 v[218:221], v195 offset:3072
	ds_read_b128 v[222:225], v195 offset:4096
	ds_read_b128 v[226:229], v195 offset:5120
	ds_read_b128 v[230:233], v195 offset:6144
	ds_read_b128 v[234:237], v195 offset:7168
	global_load_lds_dwordx4 v[160:161], off
	v_lshl_add_u64 v[160:161], s[50:51], 0, v[174:175]
	s_add_i32 m0, s59, 0xe000
	s_nop 0
	global_load_lds_dwordx4 v[160:161], off
	s_waitcnt vmcnt(8)
	s_waitcnt lgkmcnt(0)
	s_barrier
	s_setprio 1
	v_mfma_f32_16x16x32_bf16 v[126:129], v[132:135], v[204:207], v[126:129]
	v_mfma_f32_16x16x32_bf16 v[122:125], v[140:143], v[204:207], v[122:125]
	v_mfma_f32_16x16x32_bf16 v[110:113], v[132:135], v[214:217], v[110:113]
	v_mfma_f32_16x16x32_bf16 v[106:109], v[140:143], v[214:217], v[106:109]
	v_mfma_f32_16x16x32_bf16 v[94:97], v[132:135], v[222:225], v[94:97]
	v_mfma_f32_16x16x32_bf16 v[90:93], v[140:143], v[222:225], v[90:93]
	v_mfma_f32_16x16x32_bf16 v[78:81], v[132:135], v[230:233], v[78:81]
	v_mfma_f32_16x16x32_bf16 v[74:77], v[140:143], v[230:233], v[74:77]
	v_mfma_f32_16x16x32_bf16 v[126:129], v[136:139], v[210:213], v[126:129]
	v_mfma_f32_16x16x32_bf16 v[122:125], v[144:147], v[210:213], v[122:125]
	v_mfma_f32_16x16x32_bf16 v[110:113], v[136:139], v[218:221], v[110:113]
	v_mfma_f32_16x16x32_bf16 v[106:109], v[144:147], v[218:221], v[106:109]
	v_mfma_f32_16x16x32_bf16 v[94:97], v[136:139], v[226:229], v[94:97]
	v_mfma_f32_16x16x32_bf16 v[90:93], v[144:147], v[226:229], v[90:93]
	v_mfma_f32_16x16x32_bf16 v[78:81], v[136:139], v[234:237], v[78:81]
	v_mfma_f32_16x16x32_bf16 v[74:77], v[144:147], v[234:237], v[74:77]
	v_mfma_f32_16x16x32_bf16 v[118:121], v[148:151], v[204:207], v[118:121]
	v_mfma_f32_16x16x32_bf16 v[114:117], v[156:159], v[204:207], v[114:117]
	v_mfma_f32_16x16x32_bf16 v[102:105], v[148:151], v[214:217], v[102:105]
	v_mfma_f32_16x16x32_bf16 v[98:101], v[156:159], v[214:217], v[98:101]
	v_mfma_f32_16x16x32_bf16 v[86:89], v[148:151], v[222:225], v[86:89]
	v_mfma_f32_16x16x32_bf16 v[82:85], v[156:159], v[222:225], v[82:85]
	v_mfma_f32_16x16x32_bf16 v[70:73], v[148:151], v[230:233], v[70:73]
	v_mfma_f32_16x16x32_bf16 v[66:69], v[156:159], v[230:233], v[66:69]
	v_mfma_f32_16x16x32_bf16 v[118:121], v[152:155], v[210:213], v[118:121]
	v_mfma_f32_16x16x32_bf16 v[114:117], v[196:199], v[210:213], v[114:117]
	v_mfma_f32_16x16x32_bf16 v[102:105], v[152:155], v[218:221], v[102:105]
	v_mfma_f32_16x16x32_bf16 v[98:101], v[196:199], v[218:221], v[98:101]
	v_mfma_f32_16x16x32_bf16 v[86:89], v[152:155], v[226:229], v[86:89]
	v_mfma_f32_16x16x32_bf16 v[82:85], v[196:199], v[226:229], v[82:85]
	v_mfma_f32_16x16x32_bf16 v[70:73], v[152:155], v[234:237], v[70:73]
	v_mfma_f32_16x16x32_bf16 v[66:69], v[196:199], v[234:237], v[66:69]
	s_setprio 0
	s_barrier
	s_add_i32 s81, s67, s57
	v_lshl_add_u64 v[160:161], s[52:53], 0, v[164:165]
	s_mov_b32 m0, s81
	ds_read_b128 v[204:207], v195 offset:16384
	ds_read_b128 v[210:213], v195 offset:17408
	ds_read_b128 v[214:217], v195 offset:18432
	ds_read_b128 v[218:221], v195 offset:19456
	ds_read_b128 v[222:225], v195 offset:20480
	ds_read_b128 v[226:229], v195 offset:21504
	ds_read_b128 v[230:233], v195 offset:22528
	ds_read_b128 v[234:237], v195 offset:23552
	global_load_lds_dwordx4 v[160:161], off
	s_add_i32 m0, s81, 0x2000
	s_add_u32 s82, s52, 0x80000
	v_lshl_add_u64 v[200:201], s[52:53], 0, v[168:169]
	s_addc_u32 s83, s53, 0
	s_add_i32 s81, s68, s57
	global_load_lds_dwordx4 v[200:201], off
	v_lshl_add_u64 v[238:239], s[82:83], 0, v[164:165]
	s_mov_b32 m0, s81
	v_lshl_add_u64 v[240:241], s[54:55], 0, v[166:167]
	global_load_lds_dwordx4 v[238:239], off
	v_lshl_add_u64 v[238:239], s[82:83], 0, v[168:169]
	s_add_i32 m0, s81, 0x2000
	s_nop 0
	global_load_lds_dwordx4 v[238:239], off
	v_lshl_add_u64 v[238:239], s[54:55], 0, v[162:163]
	s_mov_b32 m0, s59
	s_nop 0
	global_load_lds_dwordx4 v[238:239], off
	s_mov_b32 m0, s60
	s_nop 0
	global_load_lds_dwordx4 v[240:241], off
	s_waitcnt vmcnt(8)
	s_waitcnt lgkmcnt(0)
	s_barrier
; #define PG8_STAGE(bufoff, gbase, voff) do { _Pragma("unroll") for (int _i = 0; _i < 2; ++_i) \
;         __builtin_amdgcn_global_load_lds((const unsigned*)((const char*)(gbase) + (voff)[_i]), (PG8_LAS unsigned*)(lds + (bufoff) + ldsw + _i * 8192), 16, 0, 0); } while (0)
; #define PG8_LDA(dst, b, h) do { _Pragma("unroll") for (int m = 0; m < 4; ++m) _Pragma("unroll") for (int k = 0; k < 2; ++k) dst[m][k] = *(const PG8_LAS bf16x8*)(lds + PG8_SA(b, h) + aoff + m * 2048 + k * 1024); } while (0)
; #define PG8_LDB(dst, b, h) do { _Pragma("unroll") for (int n = 0; n < 2; ++n) _Pragma("unroll") for (int k = 0; k < 2; ++k) dst[n][k] = *(const PG8_LAS bf16x8*)(lds + PG8_SB(b, h) + boff + n * 2048 + k * 1024); } while (0)
; #define PG8_MMA(ai, bj, At, Bt) do { __builtin_amdgcn_s_setprio(1); _Pragma("unroll") for (int m = 0; m < 4; ++m) _Pragma("unroll") for (int n = 0; n < 2; ++n) _Pragma("unroll") for (int k = 0; k < 2; ++k) \
;         acc[ai][bj][m][n] = __builtin_amdgcn_mfma_f32_16x16x32_bf16(Bt[n][k], At[m][k], acc[ai][bj][m][n], 0, 0, 0); __builtin_amdgcn_s_setprio(0); } while (0)
; #define PG8_WAIT_V(n) asm volatile("s_waitcnt vmcnt(" #n ")" ::: "memory")
; #define PG8_WAIT_L(n) asm volatile("s_waitcnt lgkmcnt(" #n ")" ::: "memory")
; #define PG8_BAR __builtin_amdgcn_s_barrier()
; #define PG8_SCHED __builtin_amdgcn_sched_barrier(0)
; template <class Epi, class Sched, bool ALIGN_EPI = false>
; __device__ __forceinline__ void gemm_phase(PG8_LAS unsigned char* lds, const Gemm g, const Sched& S, const Epi& E) {
;     ...
;             PG8_WAIT_V(8); PG8_WAIT_L(0); PG8_BAR; PG8_MMA(0, 0, At, B0); PG8_MMA(0, 1, At, B1); PG8_BAR; PG8_SCHED;
;             PG8_LDA(At, 0, 1); PG8_STAGE(PG8_SB(0, 0), b2, voffB); PG8_STAGE(PG8_SB(0, 1), b2 + hstep, voffB); PG8_STAGE(PG8_SA(0, 0), a2, w0);
;             PG8_WAIT_V(8); PG8_WAIT_L(0); PG8_BAR; PG8_MMA(1, 0, At, B0); PG8_MMA(1, 1, At, B1); PG8_BAR; PG8_SCHED;
;             PG8_LDB(B0, 1, 0); PG8_LDB(B1, 1, 1); PG8_SCHED; PG8_LDA(At, 1, 0); PG8_STAGE(PG8_SA(0, 1), a2 + hstepA, w1);
;             PG8_WAIT_V(8); PG8_WAIT_L(0); PG8_BAR; PG8_MMA(0, 0, At, B0); PG8_MMA(0, 1, At, B1); PG8_BAR; PG8_SCHED;
	s_setprio 1
	v_mfma_f32_16x16x32_bf16 v[54:57], v[132:135], v[204:207], v[54:57]
	v_mfma_f32_16x16x32_bf16 v[50:53], v[140:143], v[204:207], v[50:53]
	v_mfma_f32_16x16x32_bf16 v[38:41], v[132:135], v[214:217], v[38:41]
	v_mfma_f32_16x16x32_bf16 v[34:37], v[140:143], v[214:217], v[34:37]
	v_mfma_f32_16x16x32_bf16 v[22:25], v[132:135], v[222:225], v[22:25]
	v_mfma_f32_16x16x32_bf16 v[18:21], v[140:143], v[222:225], v[18:21]
	v_mfma_f32_16x16x32_bf16 v[6:9], v[132:135], v[230:233], v[6:9]
	v_mfma_f32_16x16x32_bf16 v[2:5], v[140:143], v[230:233], v[2:5]
	v_mfma_f32_16x16x32_bf16 v[54:57], v[136:139], v[210:213], v[54:57]
	v_mfma_f32_16x16x32_bf16 v[50:53], v[144:147], v[210:213], v[50:53]
	v_mfma_f32_16x16x32_bf16 v[38:41], v[136:139], v[218:221], v[38:41]
	v_mfma_f32_16x16x32_bf16 v[34:37], v[144:147], v[218:221], v[34:37]
	v_mfma_f32_16x16x32_bf16 v[22:25], v[136:139], v[226:229], v[22:25]
	v_mfma_f32_16x16x32_bf16 v[18:21], v[144:147], v[226:229], v[18:21]
	v_mfma_f32_16x16x32_bf16 v[6:9], v[136:139], v[234:237], v[6:9]
	v_mfma_f32_16x16x32_bf16 v[2:5], v[144:147], v[234:237], v[2:5]
	v_mfma_f32_16x16x32_bf16 v[58:61], v[148:151], v[204:207], v[58:61]
	v_mfma_f32_16x16x32_bf16 v[62:65], v[156:159], v[204:207], v[62:65]
	v_mfma_f32_16x16x32_bf16 v[42:45], v[148:151], v[214:217], v[42:45]
	v_mfma_f32_16x16x32_bf16 v[46:49], v[156:159], v[214:217], v[46:49]
	v_mfma_f32_16x16x32_bf16 v[26:29], v[148:151], v[222:225], v[26:29]
	v_mfma_f32_16x16x32_bf16 v[30:33], v[156:159], v[222:225], v[30:33]
	v_mfma_f32_16x16x32_bf16 v[10:13], v[148:151], v[230:233], v[10:13]
	v_mfma_f32_16x16x32_bf16 v[14:17], v[156:159], v[230:233], v[14:17]
	v_mfma_f32_16x16x32_bf16 v[58:61], v[152:155], v[210:213], v[58:61]
	v_mfma_f32_16x16x32_bf16 v[62:65], v[196:199], v[210:213], v[62:65]
	v_mfma_f32_16x16x32_bf16 v[42:45], v[152:155], v[218:221], v[42:45]
	v_mfma_f32_16x16x32_bf16 v[46:49], v[196:199], v[218:221], v[46:49]
	v_mfma_f32_16x16x32_bf16 v[26:29], v[152:155], v[226:229], v[26:29]
	v_mfma_f32_16x16x32_bf16 v[30:33], v[196:199], v[226:229], v[30:33]
	v_mfma_f32_16x16x32_bf16 v[10:13], v[152:155], v[234:237], v[10:13]
	v_mfma_f32_16x16x32_bf16 v[14:17], v[196:199], v[234:237], v[14:17]
	s_setprio 0
	s_barrier
	s_add_i32 s81, 0, 0x18000
	v_add_u32_e32 v131, s81, v181
	s_add_i32 s82, 0, 0x1c000
	ds_read_b128 v[132:135], v131
	ds_read_b128 v[136:139], v131 offset:1024
	ds_read_b128 v[140:143], v131 offset:2048
	ds_read_b128 v[144:147], v131 offset:3072
	v_add_u32_e32 v131, s82, v181
	ds_read_b128 v[148:151], v131
	ds_read_b128 v[152:155], v131 offset:1024
	ds_read_b128 v[156:159], v131 offset:2048
	ds_read_b128 v[196:199], v131 offset:3072
	s_add_u32 s54, s54, 0x80000
	s_addc_u32 s55, s55, 0
	s_mov_b32 m0, s61
	v_lshl_add_u64 v[242:243], s[54:55], 0, v[162:163]
	ds_read_b128 v[204:207], v195 offset:32768
	ds_read_b128 v[210:213], v195 offset:33792
	ds_read_b128 v[214:217], v195 offset:34816
	ds_read_b128 v[218:221], v195 offset:35840
	ds_read_b128 v[222:225], v195 offset:36864
	ds_read_b128 v[226:229], v195 offset:37888
	ds_read_b128 v[230:233], v195 offset:38912
	ds_read_b128 v[234:237], v195 offset:39936
	global_load_lds_dwordx4 v[242:243], off
	v_lshl_add_u64 v[242:243], s[54:55], 0, v[166:167]
	s_mov_b32 m0, s62
	s_nop 0
	global_load_lds_dwordx4 v[242:243], off
	s_waitcnt vmcnt(8)
	s_waitcnt lgkmcnt(0)
	s_barrier
	s_setprio 1
	v_mfma_f32_16x16x32_bf16 v[126:129], v[132:135], v[204:207], v[126:129]
	v_mfma_f32_16x16x32_bf16 v[122:125], v[140:143], v[204:207], v[122:125]
	v_mfma_f32_16x16x32_bf16 v[110:113], v[132:135], v[214:217], v[110:113]
	v_mfma_f32_16x16x32_bf16 v[106:109], v[140:143], v[214:217], v[106:109]
	v_mfma_f32_16x16x32_bf16 v[94:97], v[132:135], v[222:225], v[94:97]
	v_mfma_f32_16x16x32_bf16 v[90:93], v[140:143], v[222:225], v[90:93]
	v_mfma_f32_16x16x32_bf16 v[78:81], v[132:135], v[230:233], v[78:81]
	v_mfma_f32_16x16x32_bf16 v[74:77], v[140:143], v[230:233], v[74:77]
	v_mfma_f32_16x16x32_bf16 v[126:129], v[136:139], v[210:213], v[126:129]
	v_mfma_f32_16x16x32_bf16 v[122:125], v[144:147], v[210:213], v[122:125]
	v_mfma_f32_16x16x32_bf16 v[110:113], v[136:139], v[218:221], v[110:113]
	v_mfma_f32_16x16x32_bf16 v[106:109], v[144:147], v[218:221], v[106:109]
	v_mfma_f32_16x16x32_bf16 v[94:97], v[136:139], v[226:229], v[94:97]
	v_mfma_f32_16x16x32_bf16 v[90:93], v[144:147], v[226:229], v[90:93]
	v_mfma_f32_16x16x32_bf16 v[78:81], v[136:139], v[234:237], v[78:81]
	v_mfma_f32_16x16x32_bf16 v[74:77], v[144:147], v[234:237], v[74:77]
	v_mfma_f32_16x16x32_bf16 v[118:121], v[148:151], v[204:207], v[118:121]
	v_mfma_f32_16x16x32_bf16 v[114:117], v[156:159], v[204:207], v[114:117]
	v_mfma_f32_16x16x32_bf16 v[102:105], v[148:151], v[214:217], v[102:105]
	v_mfma_f32_16x16x32_bf16 v[98:101], v[156:159], v[214:217], v[98:101]
	v_mfma_f32_16x16x32_bf16 v[86:89], v[148:151], v[222:225], v[86:89]
	v_mfma_f32_16x16x32_bf16 v[82:85], v[156:159], v[222:225], v[82:85]
	v_mfma_f32_16x16x32_bf16 v[70:73], v[148:151], v[230:233], v[70:73]
	v_mfma_f32_16x16x32_bf16 v[66:69], v[156:159], v[230:233], v[66:69]
	v_mfma_f32_16x16x32_bf16 v[118:121], v[152:155], v[210:213], v[118:121]
	v_mfma_f32_16x16x32_bf16 v[114:117], v[196:199], v[210:213], v[114:117]
	v_mfma_f32_16x16x32_bf16 v[102:105], v[152:155], v[218:221], v[102:105]
	v_mfma_f32_16x16x32_bf16 v[98:101], v[196:199], v[218:221], v[98:101]
	v_mfma_f32_16x16x32_bf16 v[86:89], v[152:155], v[226:229], v[86:89]
	v_mfma_f32_16x16x32_bf16 v[82:85], v[196:199], v[226:229], v[82:85]
	v_mfma_f32_16x16x32_bf16 v[70:73], v[152:155], v[234:237], v[70:73]
	v_mfma_f32_16x16x32_bf16 v[66:69], v[196:199], v[234:237], v[66:69]
	s_setprio 0
	s_barrier
; #define PG8_STAGE(bufoff, gbase, voff) do { _Pragma("unroll") for (int _i = 0; _i < 2; ++_i) \
;         __builtin_amdgcn_global_load_lds((const unsigned*)((const char*)(gbase) + (voff)[_i]), (PG8_LAS unsigned*)(lds + (bufoff) + ldsw + _i * 8192), 16, 0, 0); } while (0)
; #define PG8_LDA(dst, b, h) do { _Pragma("unroll") for (int m = 0; m < 4; ++m) _Pragma("unroll") for (int k = 0; k < 2; ++k) dst[m][k] = *(const PG8_LAS bf16x8*)(lds + PG8_SA(b, h) + aoff + m * 2048 + k * 1024); } while (0)
; #define PG8_MMA(ai, bj, At, Bt) do { __builtin_amdgcn_s_setprio(1); _Pragma("unroll") for (int m = 0; m < 4; ++m) _Pragma("unroll") for (int n = 0; n < 2; ++n) _Pragma("unroll") for (int k = 0; k < 2; ++k) \
;         acc[ai][bj][m][n] = __builtin_amdgcn_mfma_f32_16x16x32_bf16(Bt[n][k], At[m][k], acc[ai][bj][m][n], 0, 0, 0); __builtin_amdgcn_s_setprio(0); } while (0)
; #define PG8_WAIT_V(n) asm volatile("s_waitcnt vmcnt(" #n ")" ::: "memory")
; #define PG8_WAIT_L(n) asm volatile("s_waitcnt lgkmcnt(" #n ")" ::: "memory")
; #define PG8_BAR __builtin_amdgcn_s_barrier()
; #define PG8_SCHED __builtin_amdgcn_sched_barrier(0)
; template <class Epi, class Sched, bool ALIGN_EPI = false>
; __device__ __forceinline__ void gemm_phase(PG8_LAS unsigned char* lds, const Gemm g, const Sched& S, const Epi& E) {
;     ...
;         for (int t = 0; t < nt; t += 2) {
;     ...
;             PG8_LDA(At, 1, 1); PG8_STAGE(PG8_SB(1, 0), b3, voffB); PG8_STAGE(PG8_SB(1, 1), b3 + hstep, voffB); PG8_STAGE(PG8_SA(1, 0), a3, w0);
;             PG8_WAIT_V(8); PG8_WAIT_L(0); PG8_BAR; PG8_MMA(1, 0, At, B0); PG8_MMA(1, 1, At, B1); PG8_BAR; PG8_SCHED;
;             if constexpr (Epi::KSCALE) { if (((t + 2) & 7) == 0 && t + 2 < nt) { E.kscale(acc, pf, ((t + 2) >> 3) - 1, wr, fr); PG8_SCHED; } }
;         }
	s_add_i32 s54, s81, s57
	v_lshl_add_u64 v[160:161], v[160:161], 0, s[20:21]
	s_mov_b32 m0, s54
	ds_read_b128 v[204:207], v195 offset:49152
	ds_read_b128 v[210:213], v195 offset:50176
	ds_read_b128 v[214:217], v195 offset:51200
	ds_read_b128 v[218:221], v195 offset:52224
	ds_read_b128 v[222:225], v195 offset:53248
	ds_read_b128 v[226:229], v195 offset:54272
	ds_read_b128 v[230:233], v195 offset:55296
	ds_read_b128 v[234:237], v195 offset:56320
	global_load_lds_dwordx4 v[160:161], off
	s_add_i32 m0, s54, 0x2000
	s_add_u32 s52, s52, 0x80080
	v_lshl_add_u64 v[160:161], v[200:201], 0, s[20:21]
	s_addc_u32 s53, s53, 0
	s_add_i32 s54, s82, s57
	global_load_lds_dwordx4 v[160:161], off
	v_lshl_add_u64 v[160:161], s[52:53], 0, v[164:165]
	s_mov_b32 m0, s54
	s_nop 0
	global_load_lds_dwordx4 v[160:161], off
	v_lshl_add_u64 v[160:161], s[52:53], 0, v[168:169]
	s_add_i32 m0, s54, 0x2000
	s_nop 0
	global_load_lds_dwordx4 v[160:161], off
	v_lshl_add_u64 v[160:161], v[238:239], 0, s[20:21]
	s_mov_b32 m0, s65
	s_nop 0
	global_load_lds_dwordx4 v[160:161], off
	v_lshl_add_u64 v[160:161], v[240:241], 0, s[20:21]
	s_mov_b32 m0, s66
	s_nop 0
	global_load_lds_dwordx4 v[160:161], off
	s_waitcnt vmcnt(8)
	s_waitcnt lgkmcnt(0)
	s_barrier
	s_setprio 1
	v_mfma_f32_16x16x32_bf16 v[54:57], v[132:135], v[204:207], v[54:57]
	v_mfma_f32_16x16x32_bf16 v[50:53], v[140:143], v[204:207], v[50:53]
	v_mfma_f32_16x16x32_bf16 v[38:41], v[132:135], v[214:217], v[38:41]
	v_mfma_f32_16x16x32_bf16 v[34:37], v[140:143], v[214:217], v[34:37]
	v_mfma_f32_16x16x32_bf16 v[22:25], v[132:135], v[222:225], v[22:25]
	v_mfma_f32_16x16x32_bf16 v[18:21], v[140:143], v[222:225], v[18:21]
	v_mfma_f32_16x16x32_bf16 v[6:9], v[132:135], v[230:233], v[6:9]
	v_mfma_f32_16x16x32_bf16 v[2:5], v[140:143], v[230:233], v[2:5]
	v_mfma_f32_16x16x32_bf16 v[54:57], v[136:139], v[210:213], v[54:57]
	v_mfma_f32_16x16x32_bf16 v[50:53], v[144:147], v[210:213], v[50:53]
	v_mfma_f32_16x16x32_bf16 v[38:41], v[136:139], v[218:221], v[38:41]
	v_mfma_f32_16x16x32_bf16 v[34:37], v[144:147], v[218:221], v[34:37]
	v_mfma_f32_16x16x32_bf16 v[22:25], v[136:139], v[226:229], v[22:25]
	v_mfma_f32_16x16x32_bf16 v[18:21], v[144:147], v[226:229], v[18:21]
	v_mfma_f32_16x16x32_bf16 v[6:9], v[136:139], v[234:237], v[6:9]
	v_mfma_f32_16x16x32_bf16 v[2:5], v[144:147], v[234:237], v[2:5]
	v_mfma_f32_16x16x32_bf16 v[58:61], v[148:151], v[204:207], v[58:61]
	v_mfma_f32_16x16x32_bf16 v[62:65], v[156:159], v[204:207], v[62:65]
	v_mfma_f32_16x16x32_bf16 v[42:45], v[148:151], v[214:217], v[42:45]
	v_mfma_f32_16x16x32_bf16 v[46:49], v[156:159], v[214:217], v[46:49]
	v_mfma_f32_16x16x32_bf16 v[26:29], v[148:151], v[222:225], v[26:29]
	v_mfma_f32_16x16x32_bf16 v[30:33], v[156:159], v[222:225], v[30:33]
	v_mfma_f32_16x16x32_bf16 v[10:13], v[148:151], v[230:233], v[10:13]
	v_mfma_f32_16x16x32_bf16 v[14:17], v[156:159], v[230:233], v[14:17]
	v_mfma_f32_16x16x32_bf16 v[58:61], v[152:155], v[210:213], v[58:61]
	v_mfma_f32_16x16x32_bf16 v[62:65], v[196:199], v[210:213], v[62:65]
	v_mfma_f32_16x16x32_bf16 v[42:45], v[152:155], v[218:221], v[42:45]
	v_mfma_f32_16x16x32_bf16 v[46:49], v[196:199], v[218:221], v[46:49]
	v_mfma_f32_16x16x32_bf16 v[26:29], v[152:155], v[226:229], v[26:29]
	v_mfma_f32_16x16x32_bf16 v[30:33], v[196:199], v[226:229], v[30:33]
	v_mfma_f32_16x16x32_bf16 v[10:13], v[152:155], v[234:237], v[10:13]
	v_mfma_f32_16x16x32_bf16 v[14:17], v[196:199], v[234:237], v[14:17]
	s_setprio 0
	s_barrier
	s_add_i32 s80, s80, 2
	s_add_u32 s50, s50, 0x100
	s_addc_u32 s51, s51, 0
	s_add_u32 s78, s78, 0x100
	s_addc_u32 s79, s79, 0
	s_cmp_gt_u32 s80, 29
	s_cbranch_scc0 .LBB0_247
	s_and_b64 vcc, exec, s[22:23]
	s_cbranch_vccz .LBB0_250
	s_barrier

; #define PG8_STAGE(bufoff, gbase, voff) do { _Pragma("unroll") for (int _i = 0; _i < 2; ++_i) \
;         __builtin_amdgcn_global_load_lds((const unsigned*)((const char*)(gbase) + (voff)[_i]), (PG8_LAS unsigned*)(lds + (bufoff) + ldsw + _i * 8192), 16, 0, 0); } while (0)
; #define PG8_LDA(dst, b, h) do { _Pragma("unroll") for (int m = 0; m < 4; ++m) _Pragma("unroll") for (int k = 0; k < 2; ++k) dst[m][k] = *(const PG8_LAS bf16x8*)(lds + PG8_SA(b, h) + aoff + m * 2048 + k * 1024); } while (0)
; #define PG8_LDB(dst, b, h) do { _Pragma("unroll") for (int n = 0; n < 2; ++n) _Pragma("unroll") for (int k = 0; k < 2; ++k) dst[n][k] = *(const PG8_LAS bf16x8*)(lds + PG8_SB(b, h) + boff + n * 2048 + k * 1024); } while (0)
; #define PG8_MMA(ai, bj, At, Bt) do { __builtin_amdgcn_s_setprio(1); _Pragma("unroll") for (int m = 0; m < 4; ++m) _Pragma("unroll") for (int n = 0; n < 2; ++n) _Pragma("unroll") for (int k = 0; k < 2; ++k) \
;         acc[ai][bj][m][n] = __builtin_amdgcn_mfma_f32_16x16x32_bf16(Bt[n][k], At[m][k], acc[ai][bj][m][n], 0, 0, 0); __builtin_amdgcn_s_setprio(0); } while (0)
; #define PG8_WAIT_V(n) asm volatile("s_waitcnt vmcnt(" #n ")" ::: "memory")
; #define PG8_WAIT_L(n) asm volatile("s_waitcnt lgkmcnt(" #n ")" ::: "memory")
; #define PG8_BAR __builtin_amdgcn_s_barrier()
; #define PG8_SCHED __builtin_amdgcn_sched_barrier(0)
; template <class Epi, class Sched, bool ALIGN_EPI = false>
; __device__ __forceinline__ void gemm_phase(PG8_LAS unsigned char* lds, const Gemm g, const Sched& S, const Epi& E) {
;     ...
;             PG8_LDB(B0, 0, 0); PG8_LDB(B1, 0, 1); PG8_SCHED; PG8_LDA(At, 0, 0); PG8_STAGE(PG8_SA(1, 1), a1 + hstepA, vc1);
;             PG8_WAIT_V(8); PG8_WAIT_L(0); PG8_BAR; PG8_MMA(0, 0, At, B0); PG8_MMA(0, 1, At, B1); PG8_BAR; PG8_SCHED;
;             PG8_LDA(At, 0, 1); PG8_STAGE(PG8_SB(0, 0), b2, voffB); PG8_STAGE(PG8_SB(0, 1), b2 + hstep, voffB); PG8_STAGE(PG8_SA(0, 0), a2, w0);
;             PG8_WAIT_V(8); PG8_WAIT_L(0); PG8_BAR; PG8_MMA(1, 0, At, B0); PG8_MMA(1, 1, At, B1); PG8_BAR; PG8_SCHED;
.LBB0_504:
	v_add_u32_e32 v3, s74, v178
	s_add_u32 s54, s50, s52
	ds_read_b128 v[138:141], v3
	ds_read_b128 v[162:165], v3 offset:1024
	ds_read_b128 v[166:169], v3 offset:2048
	ds_read_b128 v[170:173], v3 offset:3072
	v_add_u32_e32 v3, s75, v178
	s_addc_u32 s55, s51, s53
	ds_read_b128 v[186:189], v3
	s_waitcnt lgkmcnt(0)
	ds_read_b128 v[190:193], v3 offset:1024
	ds_read_b128 v[194:197], v3 offset:2048
	ds_read_b128 v[198:201], v3 offset:3072
	s_add_u32 s54, s54, 0x100
	s_addc_u32 s55, s55, 0
	s_add_u32 s82, s79, s52
	s_addc_u32 s83, s80, s53
	s_cmpk_eq_i32 s52, 0xf00
	s_cselect_b32 s57, s47, s55
	s_cselect_b32 s56, s49, s54
	s_cselect_b32 s55, s45, s83
	s_cselect_b32 s54, s78, s82
	v_lshl_add_u64 v[142:143], v[132:133], 0, s[52:53]
	s_add_i32 m0, s62, 0xc000
	ds_read_b128 v[202:205], v184
	ds_read_b128 v[206:209], v184 offset:1024
	ds_read_b128 v[210:213], v184 offset:2048
	ds_read_b128 v[214:217], v184 offset:3072
	ds_read_b128 v[218:221], v184 offset:4096
	ds_read_b128 v[222:225], v184 offset:5120
	ds_read_b128 v[226:229], v184 offset:6144
	ds_read_b128 v[230:233], v184 offset:7168
	global_load_lds_dwordx4 v[142:143], off
	v_lshl_add_u64 v[142:143], v[134:135], 0, s[52:53]
	s_add_i32 m0, s62, 0xe000
	s_nop 0
	global_load_lds_dwordx4 v[142:143], off
	s_waitcnt vmcnt(8)
	s_waitcnt lgkmcnt(0)
	s_barrier
	s_setprio 1
	v_mfma_f32_16x16x32_bf16 v[128:131], v[138:141], v[202:205], v[128:131]
	v_mfma_f32_16x16x32_bf16 v[124:127], v[166:169], v[202:205], v[124:127]
	v_mfma_f32_16x16x32_bf16 v[120:123], v[138:141], v[210:213], v[120:123]
	v_mfma_f32_16x16x32_bf16 v[112:115], v[166:169], v[210:213], v[112:115]
	v_mfma_f32_16x16x32_bf16 v[96:99], v[138:141], v[218:221], v[96:99]
	v_mfma_f32_16x16x32_bf16 v[92:95], v[166:169], v[218:221], v[92:95]
	v_mfma_f32_16x16x32_bf16 v[80:83], v[138:141], v[226:229], v[80:83]
	v_mfma_f32_16x16x32_bf16 v[76:79], v[166:169], v[226:229], v[76:79]
	v_mfma_f32_16x16x32_bf16 v[128:131], v[162:165], v[206:209], v[128:131]
	v_mfma_f32_16x16x32_bf16 v[124:127], v[170:173], v[206:209], v[124:127]
	v_mfma_f32_16x16x32_bf16 v[120:123], v[162:165], v[214:217], v[120:123]
	v_mfma_f32_16x16x32_bf16 v[112:115], v[170:173], v[214:217], v[112:115]
	v_mfma_f32_16x16x32_bf16 v[96:99], v[162:165], v[222:225], v[96:99]
	v_mfma_f32_16x16x32_bf16 v[92:95], v[170:173], v[222:225], v[92:95]
	v_mfma_f32_16x16x32_bf16 v[80:83], v[162:165], v[230:233], v[80:83]
	v_mfma_f32_16x16x32_bf16 v[76:79], v[170:173], v[230:233], v[76:79]
	v_mfma_f32_16x16x32_bf16 v[116:119], v[186:189], v[202:205], v[116:119]
	v_mfma_f32_16x16x32_bf16 v[108:111], v[194:197], v[202:205], v[108:111]
	v_mfma_f32_16x16x32_bf16 v[104:107], v[186:189], v[210:213], v[104:107]
	v_mfma_f32_16x16x32_bf16 v[100:103], v[194:197], v[210:213], v[100:103]
	v_mfma_f32_16x16x32_bf16 v[88:91], v[186:189], v[218:221], v[88:91]
	v_mfma_f32_16x16x32_bf16 v[84:87], v[194:197], v[218:221], v[84:87]
	v_mfma_f32_16x16x32_bf16 v[72:75], v[186:189], v[226:229], v[72:75]
	v_mfma_f32_16x16x32_bf16 v[68:71], v[194:197], v[226:229], v[68:71]
	v_mfma_f32_16x16x32_bf16 v[116:119], v[190:193], v[206:209], v[116:119]
	v_mfma_f32_16x16x32_bf16 v[108:111], v[198:201], v[206:209], v[108:111]
	v_mfma_f32_16x16x32_bf16 v[104:107], v[190:193], v[214:217], v[104:107]
	v_mfma_f32_16x16x32_bf16 v[100:103], v[198:201], v[214:217], v[100:103]
	v_mfma_f32_16x16x32_bf16 v[88:91], v[190:193], v[222:225], v[88:91]
	v_mfma_f32_16x16x32_bf16 v[84:87], v[198:201], v[222:225], v[84:87]
	v_mfma_f32_16x16x32_bf16 v[72:75], v[190:193], v[230:233], v[72:75]
	v_mfma_f32_16x16x32_bf16 v[68:71], v[198:201], v[230:233], v[68:71]
	s_setprio 0
	s_barrier
	s_add_i32 s82, s74, s61
	v_lshl_add_u64 v[142:143], s[54:55], 0, v[146:147]
	s_mov_b32 m0, s82
	ds_read_b128 v[202:205], v184 offset:16384
	ds_read_b128 v[206:209], v184 offset:17408
	ds_read_b128 v[210:213], v184 offset:18432
	ds_read_b128 v[214:217], v184 offset:19456
	ds_read_b128 v[218:221], v184 offset:20480
	ds_read_b128 v[222:225], v184 offset:21504
	ds_read_b128 v[226:229], v184 offset:22528
	ds_read_b128 v[230:233], v184 offset:23552
	global_load_lds_dwordx4 v[142:143], off
	s_add_i32 m0, s82, 0x2000
	s_add_u32 s82, s54, 0x80000
	v_lshl_add_u64 v[174:175], s[54:55], 0, v[150:151]
	s_addc_u32 s83, s55, 0
	s_add_i32 s84, s75, s61
	global_load_lds_dwordx4 v[174:175], off
	v_lshl_add_u64 v[234:235], s[82:83], 0, v[146:147]
	s_mov_b32 m0, s84
	v_lshl_add_u64 v[236:237], s[56:57], 0, v[148:149]
	global_load_lds_dwordx4 v[234:235], off
	v_lshl_add_u64 v[234:235], s[82:83], 0, v[150:151]
	s_add_i32 m0, s84, 0x2000
	s_nop 0
	global_load_lds_dwordx4 v[234:235], off
	v_lshl_add_u64 v[234:235], s[56:57], 0, v[144:145]
	s_mov_b32 m0, s62
	s_nop 0
	global_load_lds_dwordx4 v[234:235], off
	s_mov_b32 m0, s63
	s_nop 0
	global_load_lds_dwordx4 v[236:237], off
	s_waitcnt vmcnt(8)
	s_waitcnt lgkmcnt(0)
	s_barrier
; #define PG8_STAGE(bufoff, gbase, voff) do { _Pragma("unroll") for (int _i = 0; _i < 2; ++_i) \
;         __builtin_amdgcn_global_load_lds((const unsigned*)((const char*)(gbase) + (voff)[_i]), (PG8_LAS unsigned*)(lds + (bufoff) + ldsw + _i * 8192), 16, 0, 0); } while (0)
; #define PG8_LDA(dst, b, h) do { _Pragma("unroll") for (int m = 0; m < 4; ++m) _Pragma("unroll") for (int k = 0; k < 2; ++k) dst[m][k] = *(const PG8_LAS bf16x8*)(lds + PG8_SA(b, h) + aoff + m * 2048 + k * 1024); } while (0)
; #define PG8_LDB(dst, b, h) do { _Pragma("unroll") for (int n = 0; n < 2; ++n) _Pragma("unroll") for (int k = 0; k < 2; ++k) dst[n][k] = *(const PG8_LAS bf16x8*)(lds + PG8_SB(b, h) + boff + n * 2048 + k * 1024); } while (0)
; #define PG8_MMA(ai, bj, At, Bt) do { __builtin_amdgcn_s_setprio(1); _Pragma("unroll") for (int m = 0; m < 4; ++m) _Pragma("unroll") for (int n = 0; n < 2; ++n) _Pragma("unroll") for (int k = 0; k < 2; ++k) \
;         acc[ai][bj][m][n] = __builtin_amdgcn_mfma_f32_16x16x32_bf16(Bt[n][k], At[m][k], acc[ai][bj][m][n], 0, 0, 0); __builtin_amdgcn_s_setprio(0); } while (0)
; #define PG8_WAIT_V(n) asm volatile("s_waitcnt vmcnt(" #n ")" ::: "memory")
; #define PG8_WAIT_L(n) asm volatile("s_waitcnt lgkmcnt(" #n ")" ::: "memory")
; #define PG8_BAR __builtin_amdgcn_s_barrier()
; #define PG8_SCHED __builtin_amdgcn_sched_barrier(0)
; template <class Epi, class Sched, bool ALIGN_EPI = false>
; __device__ __forceinline__ void gemm_phase(PG8_LAS unsigned char* lds, const Gemm g, const Sched& S, const Epi& E) {
;     ...
;             PG8_WAIT_V(8); PG8_WAIT_L(0); PG8_BAR; PG8_MMA(1, 0, At, B0); PG8_MMA(1, 1, At, B1); PG8_BAR; PG8_SCHED;
;             PG8_LDB(B0, 1, 0); PG8_LDB(B1, 1, 1); PG8_SCHED; PG8_LDA(At, 1, 0); PG8_STAGE(PG8_SA(0, 1), a2 + hstepA, w1);
;             PG8_WAIT_V(8); PG8_WAIT_L(0); PG8_BAR; PG8_MMA(0, 0, At, B0); PG8_MMA(0, 1, At, B1); PG8_BAR; PG8_SCHED;
	s_setprio 1
	v_mfma_f32_16x16x32_bf16 v[64:67], v[138:141], v[202:205], v[64:67]
	v_mfma_f32_16x16x32_bf16 v[60:63], v[166:169], v[202:205], v[60:63]
	v_mfma_f32_16x16x32_bf16 v[48:51], v[138:141], v[210:213], v[48:51]
	v_mfma_f32_16x16x32_bf16 v[44:47], v[166:169], v[210:213], v[44:47]
	v_mfma_f32_16x16x32_bf16 v[32:35], v[138:141], v[218:221], v[32:35]
	v_mfma_f32_16x16x32_bf16 v[28:31], v[166:169], v[218:221], v[28:31]
	v_mfma_f32_16x16x32_bf16 v[16:19], v[138:141], v[226:229], v[16:19]
	v_mfma_f32_16x16x32_bf16 v[12:15], v[166:169], v[226:229], v[12:15]
	v_mfma_f32_16x16x32_bf16 v[64:67], v[162:165], v[206:209], v[64:67]
	v_mfma_f32_16x16x32_bf16 v[60:63], v[170:173], v[206:209], v[60:63]
	v_mfma_f32_16x16x32_bf16 v[48:51], v[162:165], v[214:217], v[48:51]
	v_mfma_f32_16x16x32_bf16 v[44:47], v[170:173], v[214:217], v[44:47]
	v_mfma_f32_16x16x32_bf16 v[32:35], v[162:165], v[222:225], v[32:35]
	v_mfma_f32_16x16x32_bf16 v[28:31], v[170:173], v[222:225], v[28:31]
	v_mfma_f32_16x16x32_bf16 v[16:19], v[162:165], v[230:233], v[16:19]
	v_mfma_f32_16x16x32_bf16 v[12:15], v[170:173], v[230:233], v[12:15]
	v_mfma_f32_16x16x32_bf16 v[56:59], v[186:189], v[202:205], v[56:59]
	v_mfma_f32_16x16x32_bf16 v[52:55], v[194:197], v[202:205], v[52:55]
	v_mfma_f32_16x16x32_bf16 v[40:43], v[186:189], v[210:213], v[40:43]
	v_mfma_f32_16x16x32_bf16 v[36:39], v[194:197], v[210:213], v[36:39]
	v_mfma_f32_16x16x32_bf16 v[24:27], v[186:189], v[218:221], v[24:27]
	v_mfma_f32_16x16x32_bf16 v[20:23], v[194:197], v[218:221], v[20:23]
	v_mfma_f32_16x16x32_bf16 v[8:11], v[186:189], v[226:229], v[8:11]
	v_mfma_f32_16x16x32_bf16 v[4:7], v[194:197], v[226:229], v[4:7]
	v_mfma_f32_16x16x32_bf16 v[56:59], v[190:193], v[206:209], v[56:59]
	v_mfma_f32_16x16x32_bf16 v[52:55], v[198:201], v[206:209], v[52:55]
	v_mfma_f32_16x16x32_bf16 v[40:43], v[190:193], v[214:217], v[40:43]
	v_mfma_f32_16x16x32_bf16 v[36:39], v[198:201], v[214:217], v[36:39]
	v_mfma_f32_16x16x32_bf16 v[24:27], v[190:193], v[222:225], v[24:27]
	v_mfma_f32_16x16x32_bf16 v[20:23], v[198:201], v[222:225], v[20:23]
	v_mfma_f32_16x16x32_bf16 v[8:11], v[190:193], v[230:233], v[8:11]
	v_mfma_f32_16x16x32_bf16 v[4:7], v[198:201], v[230:233], v[4:7]
	s_setprio 0
	s_barrier
	s_add_i32 s82, 0, 0x18000
	v_add_u32_e32 v3, s82, v178
	s_add_i32 s83, 0, 0x1c000
	ds_read_b128 v[138:141], v3
	ds_read_b128 v[162:165], v3 offset:1024
	ds_read_b128 v[166:169], v3 offset:2048
	ds_read_b128 v[170:173], v3 offset:3072
	v_add_u32_e32 v3, s83, v178
	ds_read_b128 v[186:189], v3
	ds_read_b128 v[190:193], v3 offset:1024
	ds_read_b128 v[194:197], v3 offset:2048
	ds_read_b128 v[198:201], v3 offset:3072
	s_add_u32 s56, s56, 0x80000
	s_addc_u32 s57, s57, 0
	s_mov_b32 m0, s64
	v_lshl_add_u64 v[238:239], s[56:57], 0, v[144:145]
	ds_read_b128 v[202:205], v184 offset:32768
	ds_read_b128 v[206:209], v184 offset:33792
	ds_read_b128 v[210:213], v184 offset:34816
	ds_read_b128 v[214:217], v184 offset:35840
	ds_read_b128 v[218:221], v184 offset:36864
	ds_read_b128 v[222:225], v184 offset:37888
	ds_read_b128 v[226:229], v184 offset:38912
	ds_read_b128 v[230:233], v184 offset:39936
	global_load_lds_dwordx4 v[238:239], off
	v_lshl_add_u64 v[238:239], s[56:57], 0, v[148:149]
	s_mov_b32 m0, s65
	s_nop 0
	global_load_lds_dwordx4 v[238:239], off
	s_waitcnt vmcnt(8)
	s_waitcnt lgkmcnt(0)
	s_barrier
	s_setprio 1
	v_mfma_f32_16x16x32_bf16 v[128:131], v[138:141], v[202:205], v[128:131]
	v_mfma_f32_16x16x32_bf16 v[124:127], v[166:169], v[202:205], v[124:127]
	v_mfma_f32_16x16x32_bf16 v[120:123], v[138:141], v[210:213], v[120:123]
	v_mfma_f32_16x16x32_bf16 v[112:115], v[166:169], v[210:213], v[112:115]
	v_mfma_f32_16x16x32_bf16 v[96:99], v[138:141], v[218:221], v[96:99]
	v_mfma_f32_16x16x32_bf16 v[92:95], v[166:169], v[218:221], v[92:95]
	v_mfma_f32_16x16x32_bf16 v[80:83], v[138:141], v[226:229], v[80:83]
	v_mfma_f32_16x16x32_bf16 v[76:79], v[166:169], v[226:229], v[76:79]
	v_mfma_f32_16x16x32_bf16 v[128:131], v[162:165], v[206:209], v[128:131]
	v_mfma_f32_16x16x32_bf16 v[124:127], v[170:173], v[206:209], v[124:127]
	v_mfma_f32_16x16x32_bf16 v[120:123], v[162:165], v[214:217], v[120:123]
	v_mfma_f32_16x16x32_bf16 v[112:115], v[170:173], v[214:217], v[112:115]
	v_mfma_f32_16x16x32_bf16 v[96:99], v[162:165], v[222:225], v[96:99]
	v_mfma_f32_16x16x32_bf16 v[92:95], v[170:173], v[222:225], v[92:95]
	v_mfma_f32_16x16x32_bf16 v[80:83], v[162:165], v[230:233], v[80:83]
	v_mfma_f32_16x16x32_bf16 v[76:79], v[170:173], v[230:233], v[76:79]
	v_mfma_f32_16x16x32_bf16 v[116:119], v[186:189], v[202:205], v[116:119]
	v_mfma_f32_16x16x32_bf16 v[108:111], v[194:197], v[202:205], v[108:111]
	v_mfma_f32_16x16x32_bf16 v[104:107], v[186:189], v[210:213], v[104:107]
	v_mfma_f32_16x16x32_bf16 v[100:103], v[194:197], v[210:213], v[100:103]
	v_mfma_f32_16x16x32_bf16 v[88:91], v[186:189], v[218:221], v[88:91]
	v_mfma_f32_16x16x32_bf16 v[84:87], v[194:197], v[218:221], v[84:87]
	v_mfma_f32_16x16x32_bf16 v[72:75], v[186:189], v[226:229], v[72:75]
	v_mfma_f32_16x16x32_bf16 v[68:71], v[194:197], v[226:229], v[68:71]
	v_mfma_f32_16x16x32_bf16 v[116:119], v[190:193], v[206:209], v[116:119]
	v_mfma_f32_16x16x32_bf16 v[108:111], v[198:201], v[206:209], v[108:111]
	v_mfma_f32_16x16x32_bf16 v[104:107], v[190:193], v[214:217], v[104:107]
	v_mfma_f32_16x16x32_bf16 v[100:103], v[198:201], v[214:217], v[100:103]
	v_mfma_f32_16x16x32_bf16 v[88:91], v[190:193], v[222:225], v[88:91]
	v_mfma_f32_16x16x32_bf16 v[84:87], v[198:201], v[222:225], v[84:87]
	v_mfma_f32_16x16x32_bf16 v[72:75], v[190:193], v[230:233], v[72:75]
	v_mfma_f32_16x16x32_bf16 v[68:71], v[198:201], v[230:233], v[68:71]
	s_setprio 0
	s_barrier
; #define PG8_STAGE(bufoff, gbase, voff) do { _Pragma("unroll") for (int _i = 0; _i < 2; ++_i) \
;         __builtin_amdgcn_global_load_lds((const unsigned*)((const char*)(gbase) + (voff)[_i]), (PG8_LAS unsigned*)(lds + (bufoff) + ldsw + _i * 8192), 16, 0, 0); } while (0)
; #define PG8_LDA(dst, b, h) do { _Pragma("unroll") for (int m = 0; m < 4; ++m) _Pragma("unroll") for (int k = 0; k < 2; ++k) dst[m][k] = *(const PG8_LAS bf16x8*)(lds + PG8_SA(b, h) + aoff + m * 2048 + k * 1024); } while (0)
; #define PG8_MMA(ai, bj, At, Bt) do { __builtin_amdgcn_s_setprio(1); _Pragma("unroll") for (int m = 0; m < 4; ++m) _Pragma("unroll") for (int n = 0; n < 2; ++n) _Pragma("unroll") for (int k = 0; k < 2; ++k) \
;         acc[ai][bj][m][n] = __builtin_amdgcn_mfma_f32_16x16x32_bf16(Bt[n][k], At[m][k], acc[ai][bj][m][n], 0, 0, 0); __builtin_amdgcn_s_setprio(0); } while (0)
; #define PG8_WAIT_V(n) asm volatile("s_waitcnt vmcnt(" #n ")" ::: "memory")
; #define PG8_WAIT_L(n) asm volatile("s_waitcnt lgkmcnt(" #n ")" ::: "memory")
; #define PG8_BAR __builtin_amdgcn_s_barrier()
; #define PG8_SCHED __builtin_amdgcn_sched_barrier(0)
; template <class Epi, class Sched, bool ALIGN_EPI = false>
; __device__ __forceinline__ void gemm_phase(PG8_LAS unsigned char* lds, const Gemm g, const Sched& S, const Epi& E) {
;     ...
;             PG8_LDA(At, 1, 1); PG8_STAGE(PG8_SB(1, 0), b3, voffB); PG8_STAGE(PG8_SB(1, 1), b3 + hstep, voffB); PG8_STAGE(PG8_SA(1, 0), a3, w0);
;             PG8_WAIT_V(8); PG8_WAIT_L(0); PG8_BAR; PG8_MMA(1, 0, At, B0); PG8_MMA(1, 1, At, B1); PG8_BAR; PG8_SCHED;
;             if constexpr (Epi::KSCALE) { if (((t + 2) & 7) == 0 && t + 2 < nt) { E.kscale(acc, pf, ((t + 2) >> 3) - 1, wr, fr); PG8_SCHED; } }
	s_add_i32 s56, s82, s61
	v_lshl_add_u64 v[142:143], v[142:143], 0, s[18:19]
	s_mov_b32 m0, s56
	ds_read_b128 v[202:205], v184 offset:49152
	ds_read_b128 v[206:209], v184 offset:50176
	ds_read_b128 v[210:213], v184 offset:51200
	ds_read_b128 v[214:217], v184 offset:52224
	ds_read_b128 v[218:221], v184 offset:53248
	ds_read_b128 v[222:225], v184 offset:54272
	ds_read_b128 v[226:229], v184 offset:55296
	ds_read_b128 v[230:233], v184 offset:56320
	global_load_lds_dwordx4 v[142:143], off
	s_add_i32 m0, s56, 0x2000
	s_add_u32 s54, s54, 0x80080
	v_lshl_add_u64 v[142:143], v[174:175], 0, s[18:19]
	s_addc_u32 s55, s55, 0
	s_add_i32 s56, s83, s61
	global_load_lds_dwordx4 v[142:143], off
	v_lshl_add_u64 v[142:143], s[54:55], 0, v[146:147]
	s_mov_b32 m0, s56
	s_nop 0
	global_load_lds_dwordx4 v[142:143], off
	v_lshl_add_u64 v[142:143], s[54:55], 0, v[150:151]
	s_add_i32 m0, s56, 0x2000
	s_nop 0
	global_load_lds_dwordx4 v[142:143], off
	v_lshl_add_u64 v[142:143], v[234:235], 0, s[18:19]
	s_mov_b32 m0, s68
	s_nop 0
	global_load_lds_dwordx4 v[142:143], off
	v_lshl_add_u64 v[142:143], v[236:237], 0, s[18:19]
	s_mov_b32 m0, s69
	s_nop 0
	global_load_lds_dwordx4 v[142:143], off
	s_waitcnt vmcnt(8)
	s_waitcnt lgkmcnt(0)
	s_barrier
	s_setprio 1
	v_mfma_f32_16x16x32_bf16 v[64:67], v[138:141], v[202:205], v[64:67]
	v_mfma_f32_16x16x32_bf16 v[60:63], v[166:169], v[202:205], v[60:63]
	v_mfma_f32_16x16x32_bf16 v[48:51], v[138:141], v[210:213], v[48:51]
	v_mfma_f32_16x16x32_bf16 v[44:47], v[166:169], v[210:213], v[44:47]
	v_mfma_f32_16x16x32_bf16 v[32:35], v[138:141], v[218:221], v[32:35]
	v_mfma_f32_16x16x32_bf16 v[28:31], v[166:169], v[218:221], v[28:31]
	v_mfma_f32_16x16x32_bf16 v[16:19], v[138:141], v[226:229], v[16:19]
	v_mfma_f32_16x16x32_bf16 v[12:15], v[166:169], v[226:229], v[12:15]
	v_mfma_f32_16x16x32_bf16 v[64:67], v[162:165], v[206:209], v[64:67]
	v_mfma_f32_16x16x32_bf16 v[60:63], v[170:173], v[206:209], v[60:63]
	v_mfma_f32_16x16x32_bf16 v[48:51], v[162:165], v[214:217], v[48:51]
	v_mfma_f32_16x16x32_bf16 v[44:47], v[170:173], v[214:217], v[44:47]
	v_mfma_f32_16x16x32_bf16 v[32:35], v[162:165], v[222:225], v[32:35]
	v_mfma_f32_16x16x32_bf16 v[28:31], v[170:173], v[222:225], v[28:31]
	v_mfma_f32_16x16x32_bf16 v[16:19], v[162:165], v[230:233], v[16:19]
	v_mfma_f32_16x16x32_bf16 v[12:15], v[170:173], v[230:233], v[12:15]
	v_mfma_f32_16x16x32_bf16 v[56:59], v[186:189], v[202:205], v[56:59]
	v_mfma_f32_16x16x32_bf16 v[52:55], v[194:197], v[202:205], v[52:55]
	v_mfma_f32_16x16x32_bf16 v[40:43], v[186:189], v[210:213], v[40:43]
	v_mfma_f32_16x16x32_bf16 v[36:39], v[194:197], v[210:213], v[36:39]
	v_mfma_f32_16x16x32_bf16 v[24:27], v[186:189], v[218:221], v[24:27]
	v_mfma_f32_16x16x32_bf16 v[20:23], v[194:197], v[218:221], v[20:23]
	v_mfma_f32_16x16x32_bf16 v[8:11], v[186:189], v[226:229], v[8:11]
	v_mfma_f32_16x16x32_bf16 v[4:7], v[194:197], v[226:229], v[4:7]
	v_mfma_f32_16x16x32_bf16 v[56:59], v[190:193], v[206:209], v[56:59]
	v_mfma_f32_16x16x32_bf16 v[52:55], v[198:201], v[206:209], v[52:55]
	v_mfma_f32_16x16x32_bf16 v[40:43], v[190:193], v[214:217], v[40:43]
	v_mfma_f32_16x16x32_bf16 v[36:39], v[198:201], v[214:217], v[36:39]
	v_mfma_f32_16x16x32_bf16 v[24:27], v[190:193], v[222:225], v[24:27]
	v_mfma_f32_16x16x32_bf16 v[20:23], v[198:201], v[222:225], v[20:23]
	v_mfma_f32_16x16x32_bf16 v[8:11], v[190:193], v[230:233], v[8:11]
	v_mfma_f32_16x16x32_bf16 v[4:7], v[198:201], v[230:233], v[4:7]
	s_setprio 0
	s_barrier
	s_mov_b32 s82, s81
	s_add_i32 s81, s81, 2
	s_and_b32 s54, s81, 6
	s_cmp_eq_u32 s54, 0
	s_cselect_b64 s[56:57], -1, 0
	s_cmp_gt_u32 s82, 29
	s_cselect_b64 s[54:55], -1, 0
	s_cmp_lt_u32 s82, 30
	s_cselect_b64 s[82:83], -1, 0
	s_and_b64 s[56:57], s[56:57], s[82:83]
	s_andn2_b64 vcc, exec, s[56:57]
	s_cbranch_vccnz .LBB0_503
; #define PG8_SCHED __builtin_amdgcn_sched_barrier(0)
;     __device__ __forceinline__ void kscale(f32x4 (&acc)[2][2][4][2], const Pre& pf, int b, int wr, int fr) const {
; #pragma unroll
;         for (int ai = 0; ai < 2; ++ai)
; #pragma unroll
;             for (int m = 0; m < 4; ++m) { const float f = pf.tab[(ai * HALF + wr * 64 + m * 16 + fr) * 4 + b];
; #pragma unroll
;                 for (int bj = 0; bj < 2; ++bj)
; #pragma unroll
;                     for (int n = 0; n < 2; ++n) acc[ai][bj][m][n] = acc[ai][bj][m][n] * f; }
;     }
; template <class Epi, class Sched, bool ALIGN_EPI = false>
; __device__ __forceinline__ void gemm_phase(PG8_LAS unsigned char* lds, const Gemm g, const Sched& S, const Epi& E) {
;     ...
;             if constexpr (Epi::KSCALE) { if (((t + 2) & 7) == 0 && t + 2 < nt) { E.kscale(acc, pf, ((t + 2) >> 3) - 1, wr, fr); PG8_SCHED; } }
	s_lshr_b32 s56, s81, 1
	v_add_u32_e32 v3, s56, v137
	v_add_u32_e32 v136, -4, v3
	ds_read_b32 v136, v136
	ds_read_b32 v138, v3 offset:2812
	ds_read2_b32 v[140:141], v3 offset0:63 offset1:127
	v_add_u32_e32 v3, 0xfc, v3
	s_waitcnt lgkmcnt(0)
	v_pk_mul_f32 v[130:131], v[130:131], v[136:137] op_sel_hi:[1,0]
	v_pk_mul_f32 v[128:129], v[128:129], v[136:137] op_sel_hi:[1,0]
	v_pk_mul_f32 v[126:127], v[126:127], v[136:137] op_sel_hi:[1,0]
	v_pk_mul_f32 v[124:125], v[124:125], v[136:137] op_sel_hi:[1,0]
	v_pk_mul_f32 v[118:119], v[118:119], v[136:137] op_sel_hi:[1,0]
	v_pk_mul_f32 v[116:117], v[116:117], v[136:137] op_sel_hi:[1,0]
	v_pk_mul_f32 v[110:111], v[110:111], v[136:137] op_sel_hi:[1,0]
	v_pk_mul_f32 v[108:109], v[108:109], v[136:137] op_sel_hi:[1,0]
	v_pk_mul_f32 v[122:123], v[122:123], v[140:141] op_sel_hi:[1,0]
	v_pk_mul_f32 v[120:121], v[120:121], v[140:141] op_sel_hi:[1,0]
	v_pk_mul_f32 v[114:115], v[114:115], v[140:141] op_sel_hi:[1,0]
	v_pk_mul_f32 v[112:113], v[112:113], v[140:141] op_sel_hi:[1,0]
	v_pk_mul_f32 v[106:107], v[106:107], v[140:141] op_sel_hi:[1,0]
	v_pk_mul_f32 v[104:105], v[104:105], v[140:141] op_sel_hi:[1,0]
	v_pk_mul_f32 v[102:103], v[102:103], v[140:141] op_sel_hi:[1,0]
	v_pk_mul_f32 v[100:101], v[100:101], v[140:141] op_sel_hi:[1,0]
	v_mov_b32_e32 v136, v141
	ds_read2st64_b32 v[140:141], v3 offset0:2 offset1:7
	v_pk_mul_f32 v[98:99], v[98:99], v[136:137] op_sel_hi:[1,0]
	v_pk_mul_f32 v[96:97], v[96:97], v[136:137] op_sel_hi:[1,0]
	v_pk_mul_f32 v[94:95], v[94:95], v[136:137] op_sel_hi:[1,0]
	v_pk_mul_f32 v[92:93], v[92:93], v[136:137] op_sel_hi:[1,0]
	v_pk_mul_f32 v[90:91], v[90:91], v[136:137] op_sel_hi:[1,0]
	v_pk_mul_f32 v[88:89], v[88:89], v[136:137] op_sel_hi:[1,0]
	v_pk_mul_f32 v[86:87], v[86:87], v[136:137] op_sel_hi:[1,0]
	v_pk_mul_f32 v[84:85], v[84:85], v[136:137] op_sel_hi:[1,0]
	s_waitcnt lgkmcnt(0)
	v_pk_mul_f32 v[82:83], v[82:83], v[140:141] op_sel_hi:[1,0]
	v_pk_mul_f32 v[80:81], v[80:81], v[140:141] op_sel_hi:[1,0]
	v_pk_mul_f32 v[78:79], v[78:79], v[140:141] op_sel_hi:[1,0]
	v_pk_mul_f32 v[76:77], v[76:77], v[140:141] op_sel_hi:[1,0]
	v_pk_mul_f32 v[74:75], v[74:75], v[140:141] op_sel_hi:[1,0]
	v_pk_mul_f32 v[72:73], v[72:73], v[140:141] op_sel_hi:[1,0]
	v_pk_mul_f32 v[70:71], v[70:71], v[140:141] op_sel_hi:[1,0]
	v_pk_mul_f32 v[68:69], v[68:69], v[140:141] op_sel_hi:[1,0]
	v_mov_b32_e32 v136, v141
	ds_read2st64_b32 v[140:141], v3 offset0:8 offset1:9
	v_pk_mul_f32 v[66:67], v[66:67], v[136:137] op_sel_hi:[1,0]
	v_pk_mul_f32 v[64:65], v[64:65], v[136:137] op_sel_hi:[1,0]
	v_pk_mul_f32 v[62:63], v[62:63], v[136:137] op_sel_hi:[1,0]
	v_pk_mul_f32 v[60:61], v[60:61], v[136:137] op_sel_hi:[1,0]
	v_pk_mul_f32 v[58:59], v[58:59], v[136:137] op_sel_hi:[1,0]
	v_pk_mul_f32 v[56:57], v[56:57], v[136:137] op_sel_hi:[1,0]
	v_pk_mul_f32 v[54:55], v[54:55], v[136:137] op_sel_hi:[1,0]
	v_pk_mul_f32 v[52:53], v[52:53], v[136:137] op_sel_hi:[1,0]
	s_waitcnt lgkmcnt(0)
	v_mov_b32_e32 v136, v141
	v_pk_mul_f32 v[50:51], v[50:51], v[140:141] op_sel_hi:[1,0]
	v_pk_mul_f32 v[48:49], v[48:49], v[140:141] op_sel_hi:[1,0]
	v_pk_mul_f32 v[46:47], v[46:47], v[140:141] op_sel_hi:[1,0]
	v_pk_mul_f32 v[44:45], v[44:45], v[140:141] op_sel_hi:[1,0]
	v_pk_mul_f32 v[42:43], v[42:43], v[140:141] op_sel_hi:[1,0]
	v_pk_mul_f32 v[40:41], v[40:41], v[140:141] op_sel_hi:[1,0]
	v_pk_mul_f32 v[38:39], v[38:39], v[140:141] op_sel_hi:[1,0]
	v_pk_mul_f32 v[36:37], v[36:37], v[140:141] op_sel_hi:[1,0]
	v_pk_mul_f32 v[34:35], v[34:35], v[136:137] op_sel_hi:[1,0]
	v_pk_mul_f32 v[32:33], v[32:33], v[136:137] op_sel_hi:[1,0]
	v_pk_mul_f32 v[30:31], v[30:31], v[136:137] op_sel_hi:[1,0]
	v_pk_mul_f32 v[28:29], v[28:29], v[136:137] op_sel_hi:[1,0]
	v_pk_mul_f32 v[26:27], v[26:27], v[136:137] op_sel_hi:[1,0]
	v_pk_mul_f32 v[24:25], v[24:25], v[136:137] op_sel_hi:[1,0]
	v_pk_mul_f32 v[22:23], v[22:23], v[136:137] op_sel_hi:[1,0]
	v_pk_mul_f32 v[20:21], v[20:21], v[136:137] op_sel_hi:[1,0]
	v_pk_mul_f32 v[18:19], v[18:19], v[138:139] op_sel_hi:[1,0]
	v_pk_mul_f32 v[16:17], v[16:17], v[138:139] op_sel_hi:[1,0]
	v_pk_mul_f32 v[14:15], v[14:15], v[138:139] op_sel_hi:[1,0]
	v_pk_mul_f32 v[12:13], v[12:13], v[138:139] op_sel_hi:[1,0]
	v_pk_mul_f32 v[10:11], v[10:11], v[138:139] op_sel_hi:[1,0]
	v_pk_mul_f32 v[8:9], v[8:9], v[138:139] op_sel_hi:[1,0]
	v_pk_mul_f32 v[6:7], v[6:7], v[138:139] op_sel_hi:[1,0]
	v_pk_mul_f32 v[4:5], v[4:5], v[138:139] op_sel_hi:[1,0]
	s_branch .LBB0_503

;     __device__ __forceinline__ int arow(const Unit& u, int r) const { if (!GATHER_) return u.pm * BM + r; int slot = u.s0 + r; slot = slot < u.cnt ? slot : u.cnt - 1; return list[u.e * 16384 + slot] >> 1; }
; #define PG8_STAGE(bufoff, gbase, voff) do { _Pragma("unroll") for (int _i = 0; _i < 2; ++_i) \
;         __builtin_amdgcn_global_load_lds((const unsigned*)((const char*)(gbase) + (voff)[_i]), (PG8_LAS unsigned*)(lds + (bufoff) + ldsw + _i * 8192), 16, 0, 0); } while (0)
; #define PG8_LDA(dst, b, h) do { _Pragma("unroll") for (int m = 0; m < 4; ++m) _Pragma("unroll") for (int k = 0; k < 2; ++k) dst[m][k] = *(const PG8_LAS bf16x8*)(lds + PG8_SA(b, h) + aoff + m * 2048 + k * 1024); } while (0)
; #define PG8_LDB(dst, b, h) do { _Pragma("unroll") for (int n = 0; n < 2; ++n) _Pragma("unroll") for (int k = 0; k < 2; ++k) dst[n][k] = *(const PG8_LAS bf16x8*)(lds + PG8_SB(b, h) + boff + n * 2048 + k * 1024); } while (0)
; #define PG8_WAIT_V(n) asm volatile("s_waitcnt vmcnt(" #n ")" ::: "memory")
; #define PG8_WAIT_L(n) asm volatile("s_waitcnt lgkmcnt(" #n ")" ::: "memory")
; #define PG8_BAR __builtin_amdgcn_s_barrier()
; template <class Epi, class Sched, bool ALIGN_EPI = false>
; __device__ __forceinline__ void gemm_phase(PG8_LAS unsigned char* lds, const Gemm g, const Sched& S, const Epi& E) {
;     ...
;         for (int i = 0; i < 2; ++i) { vc0[i] = (unsigned)(S.arow(cur, RA[i]) * K + CA[i]) * 2u; vc1[i] = (unsigned)(S.arow(cur, RA[i] + HALF) * K + CA[i]) * 2u; vn0[i] = vc0[i]; vn1[i] = vc1[i]; }
;     ...
;             const char* a2 = last ? nA : cA + (size_t)(t + 2) * kstep; const char* b2 = last ? nB : cB + (size_t)(t + 2) * kstep;
;             const char* a3 = a2 + kstep; const char* b3 = b2 + kstep;
;             unsigned w0[2], w1[2];
; #pragma unroll
;             for (int i = 0; i < 2; ++i) { w0[i] = (Sched::GATHER && last) ? vn0[i] : vc0[i]; w1[i] = (Sched::GATHER && last) ? vn1[i] : vc1[i]; }
;             if (last && has_next) S.a_ready(nxt);
;             PG8_LDB(B0, 0, 0); PG8_LDB(B1, 0, 1); PG8_SCHED; PG8_LDA(At, 0, 0); PG8_STAGE(PG8_SA(1, 1), a1 + hstepA, vc1);
;             PG8_WAIT_V(8); PG8_WAIT_L(0); PG8_BAR; PG8_MMA(0, 0, At, B0); PG8_MMA(0, 1, At, B1); PG8_BAR; PG8_SCHED;
;             PG8_LDA(At, 0, 1); PG8_STAGE(PG8_SB(0, 0), b2, voffB); PG8_STAGE(PG8_SB(0, 1), b2 + hstep, voffB); PG8_STAGE(PG8_SA(0, 0), a2, w0);
.LBB0_721:
	s_add_u32 s58, s36, s56
	v_add_u32_e32 v155, s82, v143
	s_addc_u32 s59, s37, s57
	ds_read_b128 v[164:167], v155
	ds_read_b128 v[168:171], v155 offset:1024
	ds_read_b128 v[172:175], v155 offset:2048
	ds_read_b128 v[176:179], v155 offset:3072
	v_add_u32_e32 v155, s83, v143
	s_add_u32 s60, s58, 0x3c800100
	ds_read_b128 v[180:183], v155
	ds_read_b128 v[184:187], v155 offset:1024
	ds_read_b128 v[188:191], v155 offset:2048
	ds_read_b128 v[192:195], v155 offset:3072
	s_addc_u32 s61, s59, 0
	s_add_u32 s91, s49, s56
	s_addc_u32 s92, s89, s57
	s_cmpk_eq_i32 s56, 0xf00
	s_cselect_b64 vcc, -1, 0
	s_and_b64 s[58:59], vcc, exec
	v_cndmask_b32_e32 v134, v151, v149, vcc
	s_cselect_b32 s61, s21, s61
	s_cselect_b32 s60, s20, s60
	v_cndmask_b32_e32 v153, v152, v157, vcc
	v_cndmask_b32_e32 v228, v150, v162, vcc
	v_cndmask_b32_e32 v155, v154, v163, vcc
	s_cselect_b32 s59, s53, s92
	s_cselect_b32 s58, s52, s91
	v_lshl_add_u64 v[230:231], v[160:161], 0, s[56:57]
	s_add_i32 m0, s55, 0xc000
	ds_read_b128 v[196:199], v147
	ds_read_b128 v[200:203], v147 offset:1024
	ds_read_b128 v[204:207], v147 offset:2048
	ds_read_b128 v[208:211], v147 offset:3072
	ds_read_b128 v[212:215], v147 offset:4096
	ds_read_b128 v[216:219], v147 offset:5120
	ds_read_b128 v[220:223], v147 offset:6144
	ds_read_b128 v[224:227], v147 offset:7168
	global_load_lds_dwordx4 v[230:231], off
	v_lshl_add_u64 v[230:231], v[158:159], 0, s[56:57]
	s_add_i32 m0, s55, 0xe000
	s_nop 0
	global_load_lds_dwordx4 v[230:231], off
	s_waitcnt vmcnt(8)
	s_waitcnt lgkmcnt(0)
	s_barrier
	s_setprio 1
	v_mfma_f32_16x16x32_bf16 v[126:129], v[164:167], v[196:199], v[126:129]
	v_mfma_f32_16x16x32_bf16 v[122:125], v[172:175], v[196:199], v[122:125]
	v_mfma_f32_16x16x32_bf16 v[110:113], v[164:167], v[204:207], v[110:113]
	v_mfma_f32_16x16x32_bf16 v[106:109], v[172:175], v[204:207], v[106:109]
	v_mfma_f32_16x16x32_bf16 v[94:97], v[164:167], v[212:215], v[94:97]
	v_mfma_f32_16x16x32_bf16 v[90:93], v[172:175], v[212:215], v[90:93]
	v_mfma_f32_16x16x32_bf16 v[78:81], v[164:167], v[220:223], v[78:81]
	v_mfma_f32_16x16x32_bf16 v[74:77], v[172:175], v[220:223], v[74:77]
	v_mfma_f32_16x16x32_bf16 v[126:129], v[168:171], v[200:203], v[126:129]
	v_mfma_f32_16x16x32_bf16 v[122:125], v[176:179], v[200:203], v[122:125]
	v_mfma_f32_16x16x32_bf16 v[110:113], v[168:171], v[208:211], v[110:113]
	v_mfma_f32_16x16x32_bf16 v[106:109], v[176:179], v[208:211], v[106:109]
	v_mfma_f32_16x16x32_bf16 v[94:97], v[168:171], v[216:219], v[94:97]
	v_mfma_f32_16x16x32_bf16 v[90:93], v[176:179], v[216:219], v[90:93]
	v_mfma_f32_16x16x32_bf16 v[78:81], v[168:171], v[224:227], v[78:81]
	v_mfma_f32_16x16x32_bf16 v[74:77], v[176:179], v[224:227], v[74:77]
	v_mfma_f32_16x16x32_bf16 v[118:121], v[180:183], v[196:199], v[118:121]
	v_mfma_f32_16x16x32_bf16 v[114:117], v[188:191], v[196:199], v[114:117]
	v_mfma_f32_16x16x32_bf16 v[102:105], v[180:183], v[204:207], v[102:105]
	v_mfma_f32_16x16x32_bf16 v[98:101], v[188:191], v[204:207], v[98:101]
	v_mfma_f32_16x16x32_bf16 v[86:89], v[180:183], v[212:215], v[86:89]
	v_mfma_f32_16x16x32_bf16 v[82:85], v[188:191], v[212:215], v[82:85]
	v_mfma_f32_16x16x32_bf16 v[70:73], v[180:183], v[220:223], v[70:73]
	v_mfma_f32_16x16x32_bf16 v[66:69], v[188:191], v[220:223], v[66:69]
	v_mfma_f32_16x16x32_bf16 v[118:121], v[184:187], v[200:203], v[118:121]
	v_mfma_f32_16x16x32_bf16 v[114:117], v[192:195], v[200:203], v[114:117]
	v_mfma_f32_16x16x32_bf16 v[102:105], v[184:187], v[208:211], v[102:105]
	v_mfma_f32_16x16x32_bf16 v[98:101], v[192:195], v[208:211], v[98:101]
	v_mfma_f32_16x16x32_bf16 v[86:89], v[184:187], v[216:219], v[86:89]
	v_mfma_f32_16x16x32_bf16 v[82:85], v[192:195], v[216:219], v[82:85]
	v_mfma_f32_16x16x32_bf16 v[70:73], v[184:187], v[224:227], v[70:73]
	v_mfma_f32_16x16x32_bf16 v[66:69], v[192:195], v[224:227], v[66:69]
	s_setprio 0
	s_barrier
	s_add_i32 s91, s82, s74
	v_lshl_add_u64 v[230:231], s[58:59], 0, v[130:131]
	s_mov_b32 m0, s91
	ds_read_b128 v[196:199], v147 offset:16384
	ds_read_b128 v[200:203], v147 offset:17408
	ds_read_b128 v[204:207], v147 offset:18432
	ds_read_b128 v[208:211], v147 offset:19456
	ds_read_b128 v[212:215], v147 offset:20480
	ds_read_b128 v[216:219], v147 offset:21504
	ds_read_b128 v[220:223], v147 offset:22528
	ds_read_b128 v[224:227], v147 offset:23552
	global_load_lds_dwordx4 v[230:231], off
	s_add_i32 m0, s91, 0x2000
	s_add_u32 s92, s58, 0x80000
	v_lshl_add_u64 v[232:233], s[58:59], 0, v[132:133]
	s_addc_u32 s93, s59, 0
	s_add_i32 s91, s83, s74
	global_load_lds_dwordx4 v[232:233], off
	v_lshl_add_u64 v[234:235], s[92:93], 0, v[130:131]
	s_mov_b32 m0, s91
	v_mov_b32_e32 v229, v135
	global_load_lds_dwordx4 v[234:235], off
	v_lshl_add_u64 v[234:235], s[92:93], 0, v[132:133]
	s_add_i32 m0, s91, 0x2000
	s_nop 0
	global_load_lds_dwordx4 v[234:235], off
	s_mov_b32 m0, s55
	v_lshl_add_u64 v[234:235], s[60:61], 0, v[134:135]
	global_load_lds_dwordx4 v134, s[60:61]
	s_mov_b32 m0, s75
	s_nop 0
	global_load_lds_dwordx4 v228, s[60:61]
	s_waitcnt vmcnt(8)
	s_waitcnt lgkmcnt(0)
	v_lshl_add_u64 v[228:229], s[60:61], 0, v[228:229]
	s_barrier
; #define PG8_STAGE(bufoff, gbase, voff) do { _Pragma("unroll") for (int _i = 0; _i < 2; ++_i) \
;         __builtin_amdgcn_global_load_lds((const unsigned*)((const char*)(gbase) + (voff)[_i]), (PG8_LAS unsigned*)(lds + (bufoff) + ldsw + _i * 8192), 16, 0, 0); } while (0)
; #define PG8_LDA(dst, b, h) do { _Pragma("unroll") for (int m = 0; m < 4; ++m) _Pragma("unroll") for (int k = 0; k < 2; ++k) dst[m][k] = *(const PG8_LAS bf16x8*)(lds + PG8_SA(b, h) + aoff + m * 2048 + k * 1024); } while (0)
; #define PG8_LDB(dst, b, h) do { _Pragma("unroll") for (int n = 0; n < 2; ++n) _Pragma("unroll") for (int k = 0; k < 2; ++k) dst[n][k] = *(const PG8_LAS bf16x8*)(lds + PG8_SB(b, h) + boff + n * 2048 + k * 1024); } while (0)
; #define PG8_MMA(ai, bj, At, Bt) do { __builtin_amdgcn_s_setprio(1); _Pragma("unroll") for (int m = 0; m < 4; ++m) _Pragma("unroll") for (int n = 0; n < 2; ++n) _Pragma("unroll") for (int k = 0; k < 2; ++k) \
;         acc[ai][bj][m][n] = __builtin_amdgcn_mfma_f32_16x16x32_bf16(Bt[n][k], At[m][k], acc[ai][bj][m][n], 0, 0, 0); __builtin_amdgcn_s_setprio(0); } while (0)
; #define PG8_WAIT_V(n) asm volatile("s_waitcnt vmcnt(" #n ")" ::: "memory")
; #define PG8_WAIT_L(n) asm volatile("s_waitcnt lgkmcnt(" #n ")" ::: "memory")
; #define PG8_BAR __builtin_amdgcn_s_barrier()
; #define PG8_SCHED __builtin_amdgcn_sched_barrier(0)
; template <class Epi, class Sched, bool ALIGN_EPI = false>
; __device__ __forceinline__ void gemm_phase(PG8_LAS unsigned char* lds, const Gemm g, const Sched& S, const Epi& E) {
;     ...
;             PG8_WAIT_V(8); PG8_WAIT_L(0); PG8_BAR; PG8_MMA(1, 0, At, B0); PG8_MMA(1, 1, At, B1); PG8_BAR; PG8_SCHED;
;             PG8_LDB(B0, 1, 0); PG8_LDB(B1, 1, 1); PG8_SCHED; PG8_LDA(At, 1, 0); PG8_STAGE(PG8_SA(0, 1), a2 + hstepA, w1);
;             PG8_WAIT_V(8); PG8_WAIT_L(0); PG8_BAR; PG8_MMA(0, 0, At, B0); PG8_MMA(0, 1, At, B1); PG8_BAR; PG8_SCHED;
	s_setprio 1
	v_mfma_f32_16x16x32_bf16 v[62:65], v[164:167], v[196:199], v[62:65]
	v_mfma_f32_16x16x32_bf16 v[58:61], v[172:175], v[196:199], v[58:61]
	v_mfma_f32_16x16x32_bf16 v[50:53], v[164:167], v[204:207], v[50:53]
	v_mfma_f32_16x16x32_bf16 v[42:45], v[172:175], v[204:207], v[42:45]
	v_mfma_f32_16x16x32_bf16 v[34:37], v[164:167], v[212:215], v[34:37]
	v_mfma_f32_16x16x32_bf16 v[30:33], v[172:175], v[212:215], v[30:33]
	v_mfma_f32_16x16x32_bf16 v[14:17], v[164:167], v[220:223], v[14:17]
	v_mfma_f32_16x16x32_bf16 v[2:5], v[172:175], v[220:223], v[2:5]
	v_mfma_f32_16x16x32_bf16 v[62:65], v[168:171], v[200:203], v[62:65]
	v_mfma_f32_16x16x32_bf16 v[58:61], v[176:179], v[200:203], v[58:61]
	v_mfma_f32_16x16x32_bf16 v[50:53], v[168:171], v[208:211], v[50:53]
	v_mfma_f32_16x16x32_bf16 v[42:45], v[176:179], v[208:211], v[42:45]
	v_mfma_f32_16x16x32_bf16 v[34:37], v[168:171], v[216:219], v[34:37]
	v_mfma_f32_16x16x32_bf16 v[30:33], v[176:179], v[216:219], v[30:33]
	v_mfma_f32_16x16x32_bf16 v[14:17], v[168:171], v[224:227], v[14:17]
	v_mfma_f32_16x16x32_bf16 v[2:5], v[176:179], v[224:227], v[2:5]
	v_mfma_f32_16x16x32_bf16 v[54:57], v[180:183], v[196:199], v[54:57]
	v_mfma_f32_16x16x32_bf16 v[46:49], v[188:191], v[196:199], v[46:49]
	v_mfma_f32_16x16x32_bf16 v[38:41], v[180:183], v[204:207], v[38:41]
	v_mfma_f32_16x16x32_bf16 v[26:29], v[188:191], v[204:207], v[26:29]
	v_mfma_f32_16x16x32_bf16 v[22:25], v[180:183], v[212:215], v[22:25]
	v_mfma_f32_16x16x32_bf16 v[18:21], v[188:191], v[212:215], v[18:21]
	v_mfma_f32_16x16x32_bf16 v[10:13], v[180:183], v[220:223], v[10:13]
	v_mfma_f32_16x16x32_bf16 v[6:9], v[188:191], v[220:223], v[6:9]
	v_mfma_f32_16x16x32_bf16 v[54:57], v[184:187], v[200:203], v[54:57]
	v_mfma_f32_16x16x32_bf16 v[46:49], v[192:195], v[200:203], v[46:49]
	v_mfma_f32_16x16x32_bf16 v[38:41], v[184:187], v[208:211], v[38:41]
	v_mfma_f32_16x16x32_bf16 v[26:29], v[192:195], v[208:211], v[26:29]
	v_mfma_f32_16x16x32_bf16 v[22:25], v[184:187], v[216:219], v[22:25]
	v_mfma_f32_16x16x32_bf16 v[18:21], v[192:195], v[216:219], v[18:21]
	v_mfma_f32_16x16x32_bf16 v[10:13], v[184:187], v[224:227], v[10:13]
	v_mfma_f32_16x16x32_bf16 v[6:9], v[192:195], v[224:227], v[6:9]
	s_setprio 0
	s_barrier
	s_add_i32 s91, 0, 0x18000
	v_add_u32_e32 v134, s91, v143
	s_add_i32 s92, 0, 0x1c000
	ds_read_b128 v[164:167], v134
	ds_read_b128 v[168:171], v134 offset:1024
	ds_read_b128 v[172:175], v134 offset:2048
	ds_read_b128 v[176:179], v134 offset:3072
	v_add_u32_e32 v134, s92, v143
	ds_read_b128 v[180:183], v134
	ds_read_b128 v[184:187], v134 offset:1024
	ds_read_b128 v[188:191], v134 offset:2048
	ds_read_b128 v[192:195], v134 offset:3072
	s_mov_b32 m0, s76
	ds_read_b128 v[196:199], v147 offset:32768
	ds_read_b128 v[200:203], v147 offset:33792
	ds_read_b128 v[204:207], v147 offset:34816
	ds_read_b128 v[208:211], v147 offset:35840
	ds_read_b128 v[212:215], v147 offset:36864
	ds_read_b128 v[216:219], v147 offset:37888
	ds_read_b128 v[220:223], v147 offset:38912
	ds_read_b128 v[224:227], v147 offset:39936
	global_load_lds_dwordx4 v153, s[60:61]
	s_mov_b32 m0, s77
	s_nop 0
	global_load_lds_dwordx4 v155, s[60:61]
	s_waitcnt vmcnt(8)
	s_waitcnt lgkmcnt(0)
	s_barrier
	s_setprio 1
	v_mfma_f32_16x16x32_bf16 v[126:129], v[164:167], v[196:199], v[126:129]
	v_mfma_f32_16x16x32_bf16 v[122:125], v[172:175], v[196:199], v[122:125]
	v_mfma_f32_16x16x32_bf16 v[110:113], v[164:167], v[204:207], v[110:113]
	v_mfma_f32_16x16x32_bf16 v[106:109], v[172:175], v[204:207], v[106:109]
	v_mfma_f32_16x16x32_bf16 v[94:97], v[164:167], v[212:215], v[94:97]
	v_mfma_f32_16x16x32_bf16 v[90:93], v[172:175], v[212:215], v[90:93]
	v_mfma_f32_16x16x32_bf16 v[78:81], v[164:167], v[220:223], v[78:81]
	v_mfma_f32_16x16x32_bf16 v[74:77], v[172:175], v[220:223], v[74:77]
	v_mfma_f32_16x16x32_bf16 v[126:129], v[168:171], v[200:203], v[126:129]
	v_mfma_f32_16x16x32_bf16 v[122:125], v[176:179], v[200:203], v[122:125]
	v_mfma_f32_16x16x32_bf16 v[110:113], v[168:171], v[208:211], v[110:113]
	v_mfma_f32_16x16x32_bf16 v[106:109], v[176:179], v[208:211], v[106:109]
	v_mfma_f32_16x16x32_bf16 v[94:97], v[168:171], v[216:219], v[94:97]
	v_mfma_f32_16x16x32_bf16 v[90:93], v[176:179], v[216:219], v[90:93]
	v_mfma_f32_16x16x32_bf16 v[78:81], v[168:171], v[224:227], v[78:81]
	v_mfma_f32_16x16x32_bf16 v[74:77], v[176:179], v[224:227], v[74:77]
	v_mfma_f32_16x16x32_bf16 v[118:121], v[180:183], v[196:199], v[118:121]
	v_mfma_f32_16x16x32_bf16 v[114:117], v[188:191], v[196:199], v[114:117]
	v_mfma_f32_16x16x32_bf16 v[102:105], v[180:183], v[204:207], v[102:105]
	v_mfma_f32_16x16x32_bf16 v[98:101], v[188:191], v[204:207], v[98:101]
	v_mfma_f32_16x16x32_bf16 v[86:89], v[180:183], v[212:215], v[86:89]
	v_mfma_f32_16x16x32_bf16 v[82:85], v[188:191], v[212:215], v[82:85]
	v_mfma_f32_16x16x32_bf16 v[70:73], v[180:183], v[220:223], v[70:73]
	v_mfma_f32_16x16x32_bf16 v[66:69], v[188:191], v[220:223], v[66:69]
	v_mfma_f32_16x16x32_bf16 v[118:121], v[184:187], v[200:203], v[118:121]
	v_mfma_f32_16x16x32_bf16 v[114:117], v[192:195], v[200:203], v[114:117]
	v_mfma_f32_16x16x32_bf16 v[102:105], v[184:187], v[208:211], v[102:105]
	v_mfma_f32_16x16x32_bf16 v[98:101], v[192:195], v[208:211], v[98:101]
	v_mfma_f32_16x16x32_bf16 v[86:89], v[184:187], v[216:219], v[86:89]
	v_mfma_f32_16x16x32_bf16 v[82:85], v[192:195], v[216:219], v[82:85]
	v_mfma_f32_16x16x32_bf16 v[70:73], v[184:187], v[224:227], v[70:73]
	v_mfma_f32_16x16x32_bf16 v[66:69], v[192:195], v[224:227], v[66:69]
	s_setprio 0
	s_barrier
; #define PG8_STAGE(bufoff, gbase, voff) do { _Pragma("unroll") for (int _i = 0; _i < 2; ++_i) \
;         __builtin_amdgcn_global_load_lds((const unsigned*)((const char*)(gbase) + (voff)[_i]), (PG8_LAS unsigned*)(lds + (bufoff) + ldsw + _i * 8192), 16, 0, 0); } while (0)
; #define PG8_LDA(dst, b, h) do { _Pragma("unroll") for (int m = 0; m < 4; ++m) _Pragma("unroll") for (int k = 0; k < 2; ++k) dst[m][k] = *(const PG8_LAS bf16x8*)(lds + PG8_SA(b, h) + aoff + m * 2048 + k * 1024); } while (0)
; #define PG8_MMA(ai, bj, At, Bt) do { __builtin_amdgcn_s_setprio(1); _Pragma("unroll") for (int m = 0; m < 4; ++m) _Pragma("unroll") for (int n = 0; n < 2; ++n) _Pragma("unroll") for (int k = 0; k < 2; ++k) \
;         acc[ai][bj][m][n] = __builtin_amdgcn_mfma_f32_16x16x32_bf16(Bt[n][k], At[m][k], acc[ai][bj][m][n], 0, 0, 0); __builtin_amdgcn_s_setprio(0); } while (0)
; #define PG8_WAIT_V(n) asm volatile("s_waitcnt vmcnt(" #n ")" ::: "memory")
; #define PG8_WAIT_L(n) asm volatile("s_waitcnt lgkmcnt(" #n ")" ::: "memory")
; #define PG8_BAR __builtin_amdgcn_s_barrier()
; #define PG8_SCHED __builtin_amdgcn_sched_barrier(0)
; template <class Epi, class Sched, bool ALIGN_EPI = false>
; __device__ __forceinline__ void gemm_phase(PG8_LAS unsigned char* lds, const Gemm g, const Sched& S, const Epi& E) {
;     ...
;         for (int t = 0; t < nt; t += 2) {
;     ...
;             PG8_LDA(At, 1, 1); PG8_STAGE(PG8_SB(1, 0), b3, voffB); PG8_STAGE(PG8_SB(1, 1), b3 + hstep, voffB); PG8_STAGE(PG8_SA(1, 0), a3, w0);
;             PG8_WAIT_V(8); PG8_WAIT_L(0); PG8_BAR; PG8_MMA(1, 0, At, B0); PG8_MMA(1, 1, At, B1); PG8_BAR; PG8_SCHED;
;             if constexpr (Epi::KSCALE) { if (((t + 2) & 7) == 0 && t + 2 < nt) { E.kscale(acc, pf, ((t + 2) >> 3) - 1, wr, fr); PG8_SCHED; } }
;         }
	s_add_i32 s60, s91, s74
	v_lshl_add_u64 v[230:231], v[230:231], 0, s[44:45]
	s_mov_b32 m0, s60
	ds_read_b128 v[196:199], v147 offset:49152
	ds_read_b128 v[200:203], v147 offset:50176
	ds_read_b128 v[204:207], v147 offset:51200
	ds_read_b128 v[208:211], v147 offset:52224
	ds_read_b128 v[212:215], v147 offset:53248
	ds_read_b128 v[216:219], v147 offset:54272
	ds_read_b128 v[220:223], v147 offset:55296
	ds_read_b128 v[224:227], v147 offset:56320
	global_load_lds_dwordx4 v[230:231], off
	s_add_i32 m0, s60, 0x2000
	s_add_u32 s58, s58, 0x80080
	v_lshl_add_u64 v[230:231], v[232:233], 0, s[44:45]
	s_addc_u32 s59, s59, 0
	s_add_i32 s60, s92, s74
	global_load_lds_dwordx4 v[230:231], off
	v_lshl_add_u64 v[230:231], s[58:59], 0, v[130:131]
	s_mov_b32 m0, s60
	v_lshl_add_u64 v[228:229], v[228:229], 0, s[44:45]
	global_load_lds_dwordx4 v[230:231], off
	v_lshl_add_u64 v[230:231], s[58:59], 0, v[132:133]
	s_add_i32 m0, s60, 0x2000
	s_nop 0
	global_load_lds_dwordx4 v[230:231], off
	v_lshl_add_u64 v[230:231], v[234:235], 0, s[44:45]
	s_mov_b32 m0, s80
	s_nop 0
	global_load_lds_dwordx4 v[230:231], off
	s_mov_b32 m0, s81
	s_nop 0
	global_load_lds_dwordx4 v[228:229], off
	s_waitcnt vmcnt(8)
	s_waitcnt lgkmcnt(0)
	s_barrier
	s_setprio 1
	v_mfma_f32_16x16x32_bf16 v[62:65], v[164:167], v[196:199], v[62:65]
	v_mfma_f32_16x16x32_bf16 v[58:61], v[172:175], v[196:199], v[58:61]
	v_mfma_f32_16x16x32_bf16 v[50:53], v[164:167], v[204:207], v[50:53]
	v_mfma_f32_16x16x32_bf16 v[42:45], v[172:175], v[204:207], v[42:45]
	v_mfma_f32_16x16x32_bf16 v[34:37], v[164:167], v[212:215], v[34:37]
	v_mfma_f32_16x16x32_bf16 v[30:33], v[172:175], v[212:215], v[30:33]
	v_mfma_f32_16x16x32_bf16 v[14:17], v[164:167], v[220:223], v[14:17]
	v_mfma_f32_16x16x32_bf16 v[2:5], v[172:175], v[220:223], v[2:5]
	v_mfma_f32_16x16x32_bf16 v[62:65], v[168:171], v[200:203], v[62:65]
	v_mfma_f32_16x16x32_bf16 v[58:61], v[176:179], v[200:203], v[58:61]
	v_mfma_f32_16x16x32_bf16 v[50:53], v[168:171], v[208:211], v[50:53]
	v_mfma_f32_16x16x32_bf16 v[42:45], v[176:179], v[208:211], v[42:45]
	v_mfma_f32_16x16x32_bf16 v[34:37], v[168:171], v[216:219], v[34:37]
	v_mfma_f32_16x16x32_bf16 v[30:33], v[176:179], v[216:219], v[30:33]
	v_mfma_f32_16x16x32_bf16 v[14:17], v[168:171], v[224:227], v[14:17]
	v_mfma_f32_16x16x32_bf16 v[2:5], v[176:179], v[224:227], v[2:5]
	v_mfma_f32_16x16x32_bf16 v[54:57], v[180:183], v[196:199], v[54:57]
	v_mfma_f32_16x16x32_bf16 v[46:49], v[188:191], v[196:199], v[46:49]
	v_mfma_f32_16x16x32_bf16 v[38:41], v[180:183], v[204:207], v[38:41]
	v_mfma_f32_16x16x32_bf16 v[26:29], v[188:191], v[204:207], v[26:29]
	v_mfma_f32_16x16x32_bf16 v[22:25], v[180:183], v[212:215], v[22:25]
	v_mfma_f32_16x16x32_bf16 v[18:21], v[188:191], v[212:215], v[18:21]
	v_mfma_f32_16x16x32_bf16 v[10:13], v[180:183], v[220:223], v[10:13]
	v_mfma_f32_16x16x32_bf16 v[6:9], v[188:191], v[220:223], v[6:9]
	v_mfma_f32_16x16x32_bf16 v[54:57], v[184:187], v[200:203], v[54:57]
	v_mfma_f32_16x16x32_bf16 v[46:49], v[192:195], v[200:203], v[46:49]
	v_mfma_f32_16x16x32_bf16 v[38:41], v[184:187], v[208:211], v[38:41]
	v_mfma_f32_16x16x32_bf16 v[26:29], v[192:195], v[208:211], v[26:29]
	v_mfma_f32_16x16x32_bf16 v[22:25], v[184:187], v[216:219], v[22:25]
	v_mfma_f32_16x16x32_bf16 v[18:21], v[192:195], v[216:219], v[18:21]
	v_mfma_f32_16x16x32_bf16 v[10:13], v[184:187], v[224:227], v[10:13]
	v_mfma_f32_16x16x32_bf16 v[6:9], v[192:195], v[224:227], v[6:9]
	s_setprio 0
	s_barrier
	s_add_i32 s90, s90, 2
	s_add_u32 s56, s56, 0x100
	s_addc_u32 s57, s57, 0
	s_cmp_gt_u32 s90, 29
	s_cbranch_scc0 .LBB0_721
	s_and_b64 vcc, exec, s[46:47]
	s_cbranch_vccz .LBB0_724
	s_barrier

; #define PG8_STAGE(bufoff, gbase, voff) do { _Pragma("unroll") for (int _i = 0; _i < 2; ++_i) \
;         __builtin_amdgcn_global_load_lds((const unsigned*)((const char*)(gbase) + (voff)[_i]), (PG8_LAS unsigned*)(lds + (bufoff) + ldsw + _i * 8192), 16, 0, 0); } while (0)
; #define PG8_LDA(dst, b, h) do { _Pragma("unroll") for (int m = 0; m < 4; ++m) _Pragma("unroll") for (int k = 0; k < 2; ++k) dst[m][k] = *(const PG8_LAS bf16x8*)(lds + PG8_SA(b, h) + aoff + m * 2048 + k * 1024); } while (0)
; #define PG8_LDB(dst, b, h) do { _Pragma("unroll") for (int n = 0; n < 2; ++n) _Pragma("unroll") for (int k = 0; k < 2; ++k) dst[n][k] = *(const PG8_LAS bf16x8*)(lds + PG8_SB(b, h) + boff + n * 2048 + k * 1024); } while (0)
; #define PG8_MMA(ai, bj, At, Bt) do { __builtin_amdgcn_s_setprio(1); _Pragma("unroll") for (int m = 0; m < 4; ++m) _Pragma("unroll") for (int n = 0; n < 2; ++n) _Pragma("unroll") for (int k = 0; k < 2; ++k) \
;         acc[ai][bj][m][n] = __builtin_amdgcn_mfma_f32_16x16x32_bf16(Bt[n][k], At[m][k], acc[ai][bj][m][n], 0, 0, 0); __builtin_amdgcn_s_setprio(0); } while (0)
; #define PG8_WAIT_V(n) asm volatile("s_waitcnt vmcnt(" #n ")" ::: "memory")
; #define PG8_WAIT_L(n) asm volatile("s_waitcnt lgkmcnt(" #n ")" ::: "memory")
; #define PG8_BAR __builtin_amdgcn_s_barrier()
; #define PG8_SCHED __builtin_amdgcn_sched_barrier(0)
; template <class Epi, class Sched, bool ALIGN_EPI = false>
; __device__ __forceinline__ void gemm_phase(PG8_LAS unsigned char* lds, const Gemm g, const Sched& S, const Epi& E) {
;     ...
;             PG8_LDB(B0, 0, 0); PG8_LDB(B1, 0, 1); PG8_SCHED; PG8_LDA(At, 0, 0); PG8_STAGE(PG8_SA(1, 1), a1 + hstepA, vc1);
;             PG8_WAIT_V(8); PG8_WAIT_L(0); PG8_BAR; PG8_MMA(0, 0, At, B0); PG8_MMA(0, 1, At, B1); PG8_BAR; PG8_SCHED;
;             PG8_LDA(At, 0, 1); PG8_STAGE(PG8_SB(0, 0), b2, voffB); PG8_STAGE(PG8_SB(0, 1), b2 + hstep, voffB); PG8_STAGE(PG8_SA(0, 0), a2, w0);
;             PG8_WAIT_V(8); PG8_WAIT_L(0); PG8_BAR; PG8_MMA(1, 0, At, B0); PG8_MMA(1, 1, At, B1); PG8_BAR; PG8_SCHED;
.LBB0_787:
	ds_read_b128 v[172:175], v167
	ds_read_b128 v[176:179], v167 offset:1024
	ds_read_b128 v[180:183], v167 offset:2048
	ds_read_b128 v[184:187], v167 offset:3072
	ds_read_b128 v[188:191], v168
	ds_read_b128 v[192:195], v168 offset:1024
	ds_read_b128 v[196:199], v168 offset:2048
	ds_read_b128 v[200:203], v168 offset:3072
	s_add_u32 s18, s16, 0x3c800100
	s_addc_u32 s19, s17, 0
	s_add_u32 s58, s16, s45
	s_addc_u32 s59, s17, s46
	s_cmp_eq_u32 s47, 28
	s_cselect_b32 s23, s21, s19
	s_cselect_b32 s22, s20, s18
	s_cselect_b32 s19, s13, s59
	s_cselect_b32 s18, s12, s58
	s_mov_b32 m0, s48
	v_lshl_add_u64 v[236:237], s[16:17], 0, v[160:161]
	ds_read_b128 v[204:207], v169
	ds_read_b128 v[208:211], v169 offset:1024
	ds_read_b128 v[212:215], v169 offset:2048
	ds_read_b128 v[216:219], v169 offset:3072
	ds_read_b128 v[220:223], v169 offset:4096
	ds_read_b128 v[224:227], v169 offset:5120
	ds_read_b128 v[228:231], v169 offset:6144
	ds_read_b128 v[232:235], v169 offset:7168
	global_load_lds_dwordx4 v[236:237], off
	v_lshl_add_u64 v[236:237], s[16:17], 0, v[158:159]
	s_mov_b32 m0, s49
	s_nop 0
	global_load_lds_dwordx4 v[236:237], off
	s_waitcnt vmcnt(8)
	s_waitcnt lgkmcnt(0)
	s_barrier
	s_setprio 1
	v_mfma_f32_16x16x32_bf16 v[126:129], v[172:175], v[204:207], v[126:129]
	v_mfma_f32_16x16x32_bf16 v[122:125], v[180:183], v[204:207], v[122:125]
	v_mfma_f32_16x16x32_bf16 v[110:113], v[172:175], v[212:215], v[110:113]
	v_mfma_f32_16x16x32_bf16 v[106:109], v[180:183], v[212:215], v[106:109]
	v_mfma_f32_16x16x32_bf16 v[94:97], v[172:175], v[220:223], v[94:97]
	v_mfma_f32_16x16x32_bf16 v[90:93], v[180:183], v[220:223], v[90:93]
	v_mfma_f32_16x16x32_bf16 v[78:81], v[172:175], v[228:231], v[78:81]
	v_mfma_f32_16x16x32_bf16 v[74:77], v[180:183], v[228:231], v[74:77]
	v_mfma_f32_16x16x32_bf16 v[126:129], v[176:179], v[208:211], v[126:129]
	v_mfma_f32_16x16x32_bf16 v[122:125], v[184:187], v[208:211], v[122:125]
	v_mfma_f32_16x16x32_bf16 v[110:113], v[176:179], v[216:219], v[110:113]
	v_mfma_f32_16x16x32_bf16 v[106:109], v[184:187], v[216:219], v[106:109]
	v_mfma_f32_16x16x32_bf16 v[94:97], v[176:179], v[224:227], v[94:97]
	v_mfma_f32_16x16x32_bf16 v[90:93], v[184:187], v[224:227], v[90:93]
	v_mfma_f32_16x16x32_bf16 v[78:81], v[176:179], v[232:235], v[78:81]
	v_mfma_f32_16x16x32_bf16 v[74:77], v[184:187], v[232:235], v[74:77]
	v_mfma_f32_16x16x32_bf16 v[118:121], v[188:191], v[204:207], v[118:121]
	v_mfma_f32_16x16x32_bf16 v[114:117], v[196:199], v[204:207], v[114:117]
	v_mfma_f32_16x16x32_bf16 v[102:105], v[188:191], v[212:215], v[102:105]
	v_mfma_f32_16x16x32_bf16 v[98:101], v[196:199], v[212:215], v[98:101]
	v_mfma_f32_16x16x32_bf16 v[86:89], v[188:191], v[220:223], v[86:89]
	v_mfma_f32_16x16x32_bf16 v[82:85], v[196:199], v[220:223], v[82:85]
	v_mfma_f32_16x16x32_bf16 v[70:73], v[188:191], v[228:231], v[70:73]
	v_mfma_f32_16x16x32_bf16 v[66:69], v[196:199], v[228:231], v[66:69]
	v_mfma_f32_16x16x32_bf16 v[118:121], v[192:195], v[208:211], v[118:121]
	v_mfma_f32_16x16x32_bf16 v[114:117], v[200:203], v[208:211], v[114:117]
	v_mfma_f32_16x16x32_bf16 v[102:105], v[192:195], v[216:219], v[102:105]
	v_mfma_f32_16x16x32_bf16 v[98:101], v[200:203], v[216:219], v[98:101]
	v_mfma_f32_16x16x32_bf16 v[86:89], v[192:195], v[224:227], v[86:89]
	v_mfma_f32_16x16x32_bf16 v[82:85], v[200:203], v[224:227], v[82:85]
	v_mfma_f32_16x16x32_bf16 v[70:73], v[192:195], v[232:235], v[70:73]
	v_mfma_f32_16x16x32_bf16 v[66:69], v[200:203], v[232:235], v[66:69]
	s_setprio 0
	s_barrier
	s_mov_b32 m0, s50
	v_lshl_add_u64 v[236:237], s[18:19], 0, v[146:147]
	s_add_u32 s58, s18, 0x80000
	ds_read_b128 v[204:207], v169 offset:16384
	ds_read_b128 v[208:211], v169 offset:17408
	ds_read_b128 v[212:215], v169 offset:18432
	ds_read_b128 v[216:219], v169 offset:19456
	ds_read_b128 v[220:223], v169 offset:20480
	ds_read_b128 v[224:227], v169 offset:21504
	ds_read_b128 v[228:231], v169 offset:22528
	ds_read_b128 v[232:235], v169 offset:23552
	global_load_lds_dwordx4 v[236:237], off
	v_lshl_add_u64 v[238:239], s[18:19], 0, v[144:145]
	s_mov_b32 m0, s51
	s_addc_u32 s59, s19, 0
	global_load_lds_dwordx4 v[238:239], off
	v_lshl_add_u64 v[240:241], s[58:59], 0, v[146:147]
	s_mov_b32 m0, s52
	v_lshl_add_u64 v[242:243], s[22:23], 0, v[150:151]
	global_load_lds_dwordx4 v[240:241], off
	v_lshl_add_u64 v[240:241], s[58:59], 0, v[144:145]
	s_mov_b32 m0, s53
	s_nop 0
	global_load_lds_dwordx4 v[240:241], off
	v_lshl_add_u64 v[240:241], s[22:23], 0, v[148:149]
	s_mov_b32 m0, s27
	s_nop 0
	global_load_lds_dwordx4 v[240:241], off
	s_mov_b32 m0, s35
	s_nop 0
	global_load_lds_dwordx4 v[242:243], off
	s_waitcnt vmcnt(8)
	s_waitcnt lgkmcnt(0)
	s_barrier
; #define PG8_STAGE(bufoff, gbase, voff) do { _Pragma("unroll") for (int _i = 0; _i < 2; ++_i) \
;         __builtin_amdgcn_global_load_lds((const unsigned*)((const char*)(gbase) + (voff)[_i]), (PG8_LAS unsigned*)(lds + (bufoff) + ldsw + _i * 8192), 16, 0, 0); } while (0)
; #define PG8_LDA(dst, b, h) do { _Pragma("unroll") for (int m = 0; m < 4; ++m) _Pragma("unroll") for (int k = 0; k < 2; ++k) dst[m][k] = *(const PG8_LAS bf16x8*)(lds + PG8_SA(b, h) + aoff + m * 2048 + k * 1024); } while (0)
; #define PG8_LDB(dst, b, h) do { _Pragma("unroll") for (int n = 0; n < 2; ++n) _Pragma("unroll") for (int k = 0; k < 2; ++k) dst[n][k] = *(const PG8_LAS bf16x8*)(lds + PG8_SB(b, h) + boff + n * 2048 + k * 1024); } while (0)
; #define PG8_MMA(ai, bj, At, Bt) do { __builtin_amdgcn_s_setprio(1); _Pragma("unroll") for (int m = 0; m < 4; ++m) _Pragma("unroll") for (int n = 0; n < 2; ++n) _Pragma("unroll") for (int k = 0; k < 2; ++k) \
;         acc[ai][bj][m][n] = __builtin_amdgcn_mfma_f32_16x16x32_bf16(Bt[n][k], At[m][k], acc[ai][bj][m][n], 0, 0, 0); __builtin_amdgcn_s_setprio(0); } while (0)
; #define PG8_WAIT_V(n) asm volatile("s_waitcnt vmcnt(" #n ")" ::: "memory")
; #define PG8_WAIT_L(n) asm volatile("s_waitcnt lgkmcnt(" #n ")" ::: "memory")
; #define PG8_BAR __builtin_amdgcn_s_barrier()
; #define PG8_SCHED __builtin_amdgcn_sched_barrier(0)
; template <class Epi, class Sched, bool ALIGN_EPI = false>
; __device__ __forceinline__ void gemm_phase(PG8_LAS unsigned char* lds, const Gemm g, const Sched& S, const Epi& E) {
;     ...
;             PG8_WAIT_V(8); PG8_WAIT_L(0); PG8_BAR; PG8_MMA(1, 0, At, B0); PG8_MMA(1, 1, At, B1); PG8_BAR; PG8_SCHED;
;             PG8_LDB(B0, 1, 0); PG8_LDB(B1, 1, 1); PG8_SCHED; PG8_LDA(At, 1, 0); PG8_STAGE(PG8_SA(0, 1), a2 + hstepA, w1);
;             PG8_WAIT_V(8); PG8_WAIT_L(0); PG8_BAR; PG8_MMA(0, 0, At, B0); PG8_MMA(0, 1, At, B1); PG8_BAR; PG8_SCHED;
	s_setprio 1
	v_mfma_f32_16x16x32_bf16 v[62:65], v[172:175], v[204:207], v[62:65]
	v_mfma_f32_16x16x32_bf16 v[58:61], v[180:183], v[204:207], v[58:61]
	v_mfma_f32_16x16x32_bf16 v[50:53], v[172:175], v[212:215], v[50:53]
	v_mfma_f32_16x16x32_bf16 v[42:45], v[180:183], v[212:215], v[42:45]
	v_mfma_f32_16x16x32_bf16 v[34:37], v[172:175], v[220:223], v[34:37]
	v_mfma_f32_16x16x32_bf16 v[26:29], v[180:183], v[220:223], v[26:29]
	v_mfma_f32_16x16x32_bf16 v[14:17], v[172:175], v[228:231], v[14:17]
	v_mfma_f32_16x16x32_bf16 v[2:5], v[180:183], v[228:231], v[2:5]
	v_mfma_f32_16x16x32_bf16 v[62:65], v[176:179], v[208:211], v[62:65]
	v_mfma_f32_16x16x32_bf16 v[58:61], v[184:187], v[208:211], v[58:61]
	v_mfma_f32_16x16x32_bf16 v[50:53], v[176:179], v[216:219], v[50:53]
	v_mfma_f32_16x16x32_bf16 v[42:45], v[184:187], v[216:219], v[42:45]
	v_mfma_f32_16x16x32_bf16 v[34:37], v[176:179], v[224:227], v[34:37]
	v_mfma_f32_16x16x32_bf16 v[26:29], v[184:187], v[224:227], v[26:29]
	v_mfma_f32_16x16x32_bf16 v[14:17], v[176:179], v[232:235], v[14:17]
	v_mfma_f32_16x16x32_bf16 v[2:5], v[184:187], v[232:235], v[2:5]
	v_mfma_f32_16x16x32_bf16 v[54:57], v[188:191], v[204:207], v[54:57]
	v_mfma_f32_16x16x32_bf16 v[46:49], v[196:199], v[204:207], v[46:49]
	v_mfma_f32_16x16x32_bf16 v[38:41], v[188:191], v[212:215], v[38:41]
	v_mfma_f32_16x16x32_bf16 v[30:33], v[196:199], v[212:215], v[30:33]
	v_mfma_f32_16x16x32_bf16 v[22:25], v[188:191], v[220:223], v[22:25]
	v_mfma_f32_16x16x32_bf16 v[18:21], v[196:199], v[220:223], v[18:21]
	v_mfma_f32_16x16x32_bf16 v[10:13], v[188:191], v[228:231], v[10:13]
	v_mfma_f32_16x16x32_bf16 v[6:9], v[196:199], v[228:231], v[6:9]
	v_mfma_f32_16x16x32_bf16 v[54:57], v[192:195], v[208:211], v[54:57]
	v_mfma_f32_16x16x32_bf16 v[46:49], v[200:203], v[208:211], v[46:49]
	v_mfma_f32_16x16x32_bf16 v[38:41], v[192:195], v[216:219], v[38:41]
	v_mfma_f32_16x16x32_bf16 v[30:33], v[200:203], v[216:219], v[30:33]
	v_mfma_f32_16x16x32_bf16 v[22:25], v[192:195], v[224:227], v[22:25]
	v_mfma_f32_16x16x32_bf16 v[18:21], v[200:203], v[224:227], v[18:21]
	v_mfma_f32_16x16x32_bf16 v[10:13], v[192:195], v[232:235], v[10:13]
	v_mfma_f32_16x16x32_bf16 v[6:9], v[200:203], v[232:235], v[6:9]
	s_setprio 0
	s_barrier
	ds_read_b128 v[172:175], v170
	ds_read_b128 v[176:179], v170 offset:1024
	ds_read_b128 v[180:183], v170 offset:2048
	ds_read_b128 v[184:187], v170 offset:3072
	ds_read_b128 v[188:191], v171
	ds_read_b128 v[192:195], v171 offset:1024
	ds_read_b128 v[196:199], v171 offset:2048
	ds_read_b128 v[200:203], v171 offset:3072
	s_mov_b32 m0, s40
	v_lshl_add_u64 v[244:245], s[22:23], 0, v[152:153]
	ds_read_b128 v[204:207], v169 offset:32768
	ds_read_b128 v[208:211], v169 offset:33792
	ds_read_b128 v[212:215], v169 offset:34816
	ds_read_b128 v[216:219], v169 offset:35840
	ds_read_b128 v[220:223], v169 offset:36864
	ds_read_b128 v[224:227], v169 offset:37888
	ds_read_b128 v[228:231], v169 offset:38912
	ds_read_b128 v[232:235], v169 offset:39936
	global_load_lds_dwordx4 v[244:245], off
	v_lshl_add_u64 v[244:245], s[22:23], 0, v[154:155]
	s_mov_b32 m0, s41
	s_nop 0
	global_load_lds_dwordx4 v[244:245], off
	s_waitcnt vmcnt(8)
	s_waitcnt lgkmcnt(0)
	s_barrier
	s_setprio 1
	v_mfma_f32_16x16x32_bf16 v[126:129], v[172:175], v[204:207], v[126:129]
	v_mfma_f32_16x16x32_bf16 v[122:125], v[180:183], v[204:207], v[122:125]
	v_mfma_f32_16x16x32_bf16 v[110:113], v[172:175], v[212:215], v[110:113]
	v_mfma_f32_16x16x32_bf16 v[106:109], v[180:183], v[212:215], v[106:109]
	v_mfma_f32_16x16x32_bf16 v[94:97], v[172:175], v[220:223], v[94:97]
	v_mfma_f32_16x16x32_bf16 v[90:93], v[180:183], v[220:223], v[90:93]
	v_mfma_f32_16x16x32_bf16 v[78:81], v[172:175], v[228:231], v[78:81]
	v_mfma_f32_16x16x32_bf16 v[74:77], v[180:183], v[228:231], v[74:77]
	v_mfma_f32_16x16x32_bf16 v[126:129], v[176:179], v[208:211], v[126:129]
	v_mfma_f32_16x16x32_bf16 v[122:125], v[184:187], v[208:211], v[122:125]
	v_mfma_f32_16x16x32_bf16 v[110:113], v[176:179], v[216:219], v[110:113]
	v_mfma_f32_16x16x32_bf16 v[106:109], v[184:187], v[216:219], v[106:109]
	v_mfma_f32_16x16x32_bf16 v[94:97], v[176:179], v[224:227], v[94:97]
	v_mfma_f32_16x16x32_bf16 v[90:93], v[184:187], v[224:227], v[90:93]
	v_mfma_f32_16x16x32_bf16 v[78:81], v[176:179], v[232:235], v[78:81]
	v_mfma_f32_16x16x32_bf16 v[74:77], v[184:187], v[232:235], v[74:77]
	v_mfma_f32_16x16x32_bf16 v[118:121], v[188:191], v[204:207], v[118:121]
	v_mfma_f32_16x16x32_bf16 v[114:117], v[196:199], v[204:207], v[114:117]
	v_mfma_f32_16x16x32_bf16 v[102:105], v[188:191], v[212:215], v[102:105]
	v_mfma_f32_16x16x32_bf16 v[98:101], v[196:199], v[212:215], v[98:101]
	v_mfma_f32_16x16x32_bf16 v[86:89], v[188:191], v[220:223], v[86:89]
	v_mfma_f32_16x16x32_bf16 v[82:85], v[196:199], v[220:223], v[82:85]
	v_mfma_f32_16x16x32_bf16 v[70:73], v[188:191], v[228:231], v[70:73]
	v_mfma_f32_16x16x32_bf16 v[66:69], v[196:199], v[228:231], v[66:69]
	v_mfma_f32_16x16x32_bf16 v[118:121], v[192:195], v[208:211], v[118:121]
	v_mfma_f32_16x16x32_bf16 v[114:117], v[200:203], v[208:211], v[114:117]
	v_mfma_f32_16x16x32_bf16 v[102:105], v[192:195], v[216:219], v[102:105]
	v_mfma_f32_16x16x32_bf16 v[98:101], v[200:203], v[216:219], v[98:101]
	v_mfma_f32_16x16x32_bf16 v[86:89], v[192:195], v[224:227], v[86:89]
	v_mfma_f32_16x16x32_bf16 v[82:85], v[200:203], v[224:227], v[82:85]
	v_mfma_f32_16x16x32_bf16 v[70:73], v[192:195], v[232:235], v[70:73]
	v_mfma_f32_16x16x32_bf16 v[66:69], v[200:203], v[232:235], v[66:69]
	s_setprio 0
	s_barrier
; #define PG8_STAGE(bufoff, gbase, voff) do { _Pragma("unroll") for (int _i = 0; _i < 2; ++_i) \
;         __builtin_amdgcn_global_load_lds((const unsigned*)((const char*)(gbase) + (voff)[_i]), (PG8_LAS unsigned*)(lds + (bufoff) + ldsw + _i * 8192), 16, 0, 0); } while (0)
; #define PG8_LDA(dst, b, h) do { _Pragma("unroll") for (int m = 0; m < 4; ++m) _Pragma("unroll") for (int k = 0; k < 2; ++k) dst[m][k] = *(const PG8_LAS bf16x8*)(lds + PG8_SA(b, h) + aoff + m * 2048 + k * 1024); } while (0)
; #define PG8_MMA(ai, bj, At, Bt) do { __builtin_amdgcn_s_setprio(1); _Pragma("unroll") for (int m = 0; m < 4; ++m) _Pragma("unroll") for (int n = 0; n < 2; ++n) _Pragma("unroll") for (int k = 0; k < 2; ++k) \
;         acc[ai][bj][m][n] = __builtin_amdgcn_mfma_f32_16x16x32_bf16(Bt[n][k], At[m][k], acc[ai][bj][m][n], 0, 0, 0); __builtin_amdgcn_s_setprio(0); } while (0)
; #define PG8_WAIT_V(n) asm volatile("s_waitcnt vmcnt(" #n ")" ::: "memory")
; #define PG8_WAIT_L(n) asm volatile("s_waitcnt lgkmcnt(" #n ")" ::: "memory")
; #define PG8_BAR __builtin_amdgcn_s_barrier()
; #define PG8_SCHED __builtin_amdgcn_sched_barrier(0)
; template <class Epi, class Sched, bool ALIGN_EPI = false>
; __device__ __forceinline__ void gemm_phase(PG8_LAS unsigned char* lds, const Gemm g, const Sched& S, const Epi& E) {
;     ...
;         for (int t = 0; t < nt; t += 2) {
;     ...
;             PG8_LDA(At, 1, 1); PG8_STAGE(PG8_SB(1, 0), b3, voffB); PG8_STAGE(PG8_SB(1, 1), b3 + hstep, voffB); PG8_STAGE(PG8_SA(1, 0), a3, w0);
;             PG8_WAIT_V(8); PG8_WAIT_L(0); PG8_BAR; PG8_MMA(1, 0, At, B0); PG8_MMA(1, 1, At, B1); PG8_BAR; PG8_SCHED;
;             if constexpr (Epi::KSCALE) { if (((t + 2) & 7) == 0 && t + 2 < nt) { E.kscale(acc, pf, ((t + 2) >> 3) - 1, wr, fr); PG8_SCHED; } }
;         }
	s_mov_b32 m0, s54
	v_lshl_add_u64 v[236:237], v[236:237], 0, s[14:15]
	s_add_u32 s18, s18, 0x80080
	ds_read_b128 v[204:207], v169 offset:49152
	ds_read_b128 v[208:211], v169 offset:50176
	ds_read_b128 v[212:215], v169 offset:51200
	ds_read_b128 v[216:219], v169 offset:52224
	ds_read_b128 v[220:223], v169 offset:53248
	ds_read_b128 v[224:227], v169 offset:54272
	ds_read_b128 v[228:231], v169 offset:55296
	ds_read_b128 v[232:235], v169 offset:56320
	global_load_lds_dwordx4 v[236:237], off
	v_lshl_add_u64 v[236:237], v[238:239], 0, s[14:15]
	s_mov_b32 m0, s55
	s_addc_u32 s19, s19, 0
	global_load_lds_dwordx4 v[236:237], off
	v_lshl_add_u64 v[236:237], s[18:19], 0, v[146:147]
	s_mov_b32 m0, s56
	s_nop 0
	global_load_lds_dwordx4 v[236:237], off
	v_lshl_add_u64 v[236:237], s[18:19], 0, v[144:145]
	s_mov_b32 m0, s57
	s_nop 0
	global_load_lds_dwordx4 v[236:237], off
	v_lshl_add_u64 v[236:237], v[240:241], 0, s[14:15]
	s_mov_b32 m0, s43
	s_nop 0
	global_load_lds_dwordx4 v[236:237], off
	v_lshl_add_u64 v[236:237], v[242:243], 0, s[14:15]
	s_mov_b32 m0, s44
	s_nop 0
	global_load_lds_dwordx4 v[236:237], off
	s_waitcnt vmcnt(8)
	s_waitcnt lgkmcnt(0)
	s_barrier
	s_setprio 1
	v_mfma_f32_16x16x32_bf16 v[62:65], v[172:175], v[204:207], v[62:65]
	v_mfma_f32_16x16x32_bf16 v[58:61], v[180:183], v[204:207], v[58:61]
	v_mfma_f32_16x16x32_bf16 v[50:53], v[172:175], v[212:215], v[50:53]
	v_mfma_f32_16x16x32_bf16 v[42:45], v[180:183], v[212:215], v[42:45]
	v_mfma_f32_16x16x32_bf16 v[34:37], v[172:175], v[220:223], v[34:37]
	v_mfma_f32_16x16x32_bf16 v[26:29], v[180:183], v[220:223], v[26:29]
	v_mfma_f32_16x16x32_bf16 v[14:17], v[172:175], v[228:231], v[14:17]
	v_mfma_f32_16x16x32_bf16 v[2:5], v[180:183], v[228:231], v[2:5]
	v_mfma_f32_16x16x32_bf16 v[62:65], v[176:179], v[208:211], v[62:65]
	v_mfma_f32_16x16x32_bf16 v[58:61], v[184:187], v[208:211], v[58:61]
	v_mfma_f32_16x16x32_bf16 v[50:53], v[176:179], v[216:219], v[50:53]
	v_mfma_f32_16x16x32_bf16 v[42:45], v[184:187], v[216:219], v[42:45]
	v_mfma_f32_16x16x32_bf16 v[34:37], v[176:179], v[224:227], v[34:37]
	v_mfma_f32_16x16x32_bf16 v[26:29], v[184:187], v[224:227], v[26:29]
	v_mfma_f32_16x16x32_bf16 v[14:17], v[176:179], v[232:235], v[14:17]
	v_mfma_f32_16x16x32_bf16 v[2:5], v[184:187], v[232:235], v[2:5]
	v_mfma_f32_16x16x32_bf16 v[54:57], v[188:191], v[204:207], v[54:57]
	v_mfma_f32_16x16x32_bf16 v[46:49], v[196:199], v[204:207], v[46:49]
	v_mfma_f32_16x16x32_bf16 v[38:41], v[188:191], v[212:215], v[38:41]
	v_mfma_f32_16x16x32_bf16 v[30:33], v[196:199], v[212:215], v[30:33]
	v_mfma_f32_16x16x32_bf16 v[22:25], v[188:191], v[220:223], v[22:25]
	v_mfma_f32_16x16x32_bf16 v[18:21], v[196:199], v[220:223], v[18:21]
	v_mfma_f32_16x16x32_bf16 v[10:13], v[188:191], v[228:231], v[10:13]
	v_mfma_f32_16x16x32_bf16 v[6:9], v[196:199], v[228:231], v[6:9]
	v_mfma_f32_16x16x32_bf16 v[54:57], v[192:195], v[208:211], v[54:57]
	v_mfma_f32_16x16x32_bf16 v[46:49], v[200:203], v[208:211], v[46:49]
	v_mfma_f32_16x16x32_bf16 v[38:41], v[192:195], v[216:219], v[38:41]
	v_mfma_f32_16x16x32_bf16 v[30:33], v[200:203], v[216:219], v[30:33]
	v_mfma_f32_16x16x32_bf16 v[22:25], v[192:195], v[224:227], v[22:25]
	v_mfma_f32_16x16x32_bf16 v[18:21], v[200:203], v[224:227], v[18:21]
	v_mfma_f32_16x16x32_bf16 v[10:13], v[192:195], v[232:235], v[10:13]
	v_mfma_f32_16x16x32_bf16 v[6:9], v[200:203], v[232:235], v[6:9]
	s_setprio 0
	s_barrier
	s_add_i32 s47, s47, 2
	s_add_u32 s16, s16, 0x100
	s_addc_u32 s17, s17, 0
	s_cmp_gt_u32 s47, 29
	s_cbranch_scc0 .LBB0_787
	s_cmpk_lt_u32 s24, 0x100
	s_cbranch_scc0 .LBB0_790
	s_barrier

; #define PG8_STAGE(bufoff, gbase, voff) do { _Pragma("unroll") for (int _i = 0; _i < 2; ++_i) \
;         __builtin_amdgcn_global_load_lds((const unsigned*)((const char*)(gbase) + (voff)[_i]), (PG8_LAS unsigned*)(lds + (bufoff) + ldsw + _i * 8192), 16, 0, 0); } while (0)
; #define PG8_LDA(dst, b, h) do { _Pragma("unroll") for (int m = 0; m < 4; ++m) _Pragma("unroll") for (int k = 0; k < 2; ++k) dst[m][k] = *(const PG8_LAS bf16x8*)(lds + PG8_SA(b, h) + aoff + m * 2048 + k * 1024); } while (0)
; #define PG8_LDB(dst, b, h) do { _Pragma("unroll") for (int n = 0; n < 2; ++n) _Pragma("unroll") for (int k = 0; k < 2; ++k) dst[n][k] = *(const PG8_LAS bf16x8*)(lds + PG8_SB(b, h) + boff + n * 2048 + k * 1024); } while (0)
; #define PG8_MMA(ai, bj, At, Bt) do { __builtin_amdgcn_s_setprio(1); _Pragma("unroll") for (int m = 0; m < 4; ++m) _Pragma("unroll") for (int n = 0; n < 2; ++n) _Pragma("unroll") for (int k = 0; k < 2; ++k) \
;         acc[ai][bj][m][n] = __builtin_amdgcn_mfma_f32_16x16x32_bf16(Bt[n][k], At[m][k], acc[ai][bj][m][n], 0, 0, 0); __builtin_amdgcn_s_setprio(0); } while (0)
; #define PG8_WAIT_V(n) asm volatile("s_waitcnt vmcnt(" #n ")" ::: "memory")
; #define PG8_WAIT_L(n) asm volatile("s_waitcnt lgkmcnt(" #n ")" ::: "memory")
; #define PG8_BAR __builtin_amdgcn_s_barrier()
; #define PG8_SCHED __builtin_amdgcn_sched_barrier(0)
; template <class Epi, class Sched, bool ALIGN_EPI = false>
; __device__ __forceinline__ void gemm_phase(PG8_LAS unsigned char* lds, const Gemm g, const Sched& S, const Epi& E) {
;     ...
;             PG8_LDB(B0, 0, 0); PG8_LDB(B1, 0, 1); PG8_SCHED; PG8_LDA(At, 0, 0); PG8_STAGE(PG8_SA(1, 1), a1 + hstepA, vc1);
;             PG8_WAIT_V(8); PG8_WAIT_L(0); PG8_BAR; PG8_MMA(0, 0, At, B0); PG8_MMA(0, 1, At, B1); PG8_BAR; PG8_SCHED;
;             PG8_LDA(At, 0, 1); PG8_STAGE(PG8_SB(0, 0), b2, voffB); PG8_STAGE(PG8_SB(0, 1), b2 + hstep, voffB); PG8_STAGE(PG8_SA(0, 0), a2, w0);
;             PG8_WAIT_V(8); PG8_WAIT_L(0); PG8_BAR; PG8_MMA(1, 0, At, B0); PG8_MMA(1, 1, At, B1); PG8_BAR; PG8_SCHED;
.LBB0_805:
	ds_read_b128 v[142:145], v1
	ds_read_b128 v[158:161], v1 offset:1024
	ds_read_b128 v[162:165], v1 offset:2048
	ds_read_b128 v[166:169], v1 offset:3072
	ds_read_b128 v[170:173], v156
	ds_read_b128 v[174:177], v156 offset:1024
	ds_read_b128 v[178:181], v156 offset:2048
	ds_read_b128 v[182:185], v156 offset:3072
	s_add_u32 s62, s60, 0xfffe0080
	s_addc_u32 s63, s61, -1
	s_cmp_eq_u32 s92, 4
	s_cselect_b32 s65, s45, s63
	s_cselect_b32 s64, s57, s62
	s_cselect_b32 s63, s47, s91
	s_cselect_b32 s62, s89, s90
	v_lshl_add_u64 v[218:219], s[60:61], 0, v[140:141]
	s_add_i32 m0, s59, 0xc000
	ds_read_b128 v[186:189], v157
	ds_read_b128 v[190:193], v157 offset:1024
	ds_read_b128 v[194:197], v157 offset:2048
	ds_read_b128 v[198:201], v157 offset:3072
	ds_read_b128 v[202:205], v157 offset:4096
	ds_read_b128 v[206:209], v157 offset:5120
	ds_read_b128 v[210:213], v157 offset:6144
	ds_read_b128 v[214:217], v157 offset:7168
	global_load_lds_dwordx4 v[218:219], off
	v_lshl_add_u64 v[218:219], s[60:61], 0, v[138:139]
	s_add_i32 m0, s59, 0xe000
	s_nop 0
	global_load_lds_dwordx4 v[218:219], off
	s_waitcnt vmcnt(8)
	s_waitcnt lgkmcnt(0)
	s_barrier
	s_setprio 1
	v_mfma_f32_16x16x32_bf16 v[126:129], v[142:145], v[186:189], v[126:129]
	v_mfma_f32_16x16x32_bf16 v[122:125], v[162:165], v[186:189], v[122:125]
	v_mfma_f32_16x16x32_bf16 v[114:117], v[142:145], v[194:197], v[114:117]
	v_mfma_f32_16x16x32_bf16 v[106:109], v[162:165], v[194:197], v[106:109]
	v_mfma_f32_16x16x32_bf16 v[98:101], v[142:145], v[202:205], v[98:101]
	v_mfma_f32_16x16x32_bf16 v[90:93], v[162:165], v[202:205], v[90:93]
	v_mfma_f32_16x16x32_bf16 v[82:85], v[142:145], v[210:213], v[82:85]
	v_mfma_f32_16x16x32_bf16 v[74:77], v[162:165], v[210:213], v[74:77]
	v_mfma_f32_16x16x32_bf16 v[126:129], v[158:161], v[190:193], v[126:129]
	v_mfma_f32_16x16x32_bf16 v[122:125], v[166:169], v[190:193], v[122:125]
	v_mfma_f32_16x16x32_bf16 v[114:117], v[158:161], v[198:201], v[114:117]
	v_mfma_f32_16x16x32_bf16 v[106:109], v[166:169], v[198:201], v[106:109]
	v_mfma_f32_16x16x32_bf16 v[98:101], v[158:161], v[206:209], v[98:101]
	v_mfma_f32_16x16x32_bf16 v[90:93], v[166:169], v[206:209], v[90:93]
	v_mfma_f32_16x16x32_bf16 v[82:85], v[158:161], v[214:217], v[82:85]
	v_mfma_f32_16x16x32_bf16 v[74:77], v[166:169], v[214:217], v[74:77]
	v_mfma_f32_16x16x32_bf16 v[118:121], v[170:173], v[186:189], v[118:121]
	v_mfma_f32_16x16x32_bf16 v[110:113], v[178:181], v[186:189], v[110:113]
	v_mfma_f32_16x16x32_bf16 v[102:105], v[170:173], v[194:197], v[102:105]
	v_mfma_f32_16x16x32_bf16 v[94:97], v[178:181], v[194:197], v[94:97]
	v_mfma_f32_16x16x32_bf16 v[86:89], v[170:173], v[202:205], v[86:89]
	v_mfma_f32_16x16x32_bf16 v[78:81], v[178:181], v[202:205], v[78:81]
	v_mfma_f32_16x16x32_bf16 v[62:65], v[170:173], v[210:213], v[62:65]
	v_mfma_f32_16x16x32_bf16 v[58:61], v[178:181], v[210:213], v[58:61]
	v_mfma_f32_16x16x32_bf16 v[118:121], v[174:177], v[190:193], v[118:121]
	v_mfma_f32_16x16x32_bf16 v[110:113], v[182:185], v[190:193], v[110:113]
	v_mfma_f32_16x16x32_bf16 v[102:105], v[174:177], v[198:201], v[102:105]
	v_mfma_f32_16x16x32_bf16 v[94:97], v[182:185], v[198:201], v[94:97]
	v_mfma_f32_16x16x32_bf16 v[86:89], v[174:177], v[206:209], v[86:89]
	v_mfma_f32_16x16x32_bf16 v[78:81], v[182:185], v[206:209], v[78:81]
	v_mfma_f32_16x16x32_bf16 v[62:65], v[174:177], v[214:217], v[62:65]
	v_mfma_f32_16x16x32_bf16 v[58:61], v[182:185], v[214:217], v[58:61]
	s_setprio 0
	s_barrier
	s_add_i32 s93, s79, s66
	v_lshl_add_u64 v[218:219], s[62:63], 0, v[132:133]
	s_mov_b32 m0, s93
	ds_read_b128 v[186:189], v157 offset:16384
	ds_read_b128 v[190:193], v157 offset:17408
	ds_read_b128 v[194:197], v157 offset:18432
	ds_read_b128 v[198:201], v157 offset:19456
	ds_read_b128 v[202:205], v157 offset:20480
	ds_read_b128 v[206:209], v157 offset:21504
	ds_read_b128 v[210:213], v157 offset:22528
	ds_read_b128 v[214:217], v157 offset:23552
	global_load_lds_dwordx4 v[218:219], off
	s_add_i32 m0, s93, 0x2000
	s_add_u32 s94, s62, 0x20000
	v_lshl_add_u64 v[220:221], s[62:63], 0, v[136:137]
	s_addc_u32 s95, s63, 0
	s_add_i32 s93, s80, s66
	global_load_lds_dwordx4 v[220:221], off
	v_lshl_add_u64 v[222:223], s[94:95], 0, v[132:133]
	s_mov_b32 m0, s93
	v_lshl_add_u64 v[224:225], s[64:65], 0, v[134:135]
	global_load_lds_dwordx4 v[222:223], off
	v_lshl_add_u64 v[222:223], s[94:95], 0, v[136:137]
	s_add_i32 m0, s93, 0x2000
	s_nop 0
	global_load_lds_dwordx4 v[222:223], off
	v_lshl_add_u64 v[222:223], s[64:65], 0, v[130:131]
	s_mov_b32 m0, s59
	s_nop 0
	global_load_lds_dwordx4 v[222:223], off
	s_mov_b32 m0, s67
	s_nop 0
	global_load_lds_dwordx4 v[224:225], off
	s_waitcnt vmcnt(8)
	s_waitcnt lgkmcnt(0)
	s_barrier
; #define PG8_STAGE(bufoff, gbase, voff) do { _Pragma("unroll") for (int _i = 0; _i < 2; ++_i) \
;         __builtin_amdgcn_global_load_lds((const unsigned*)((const char*)(gbase) + (voff)[_i]), (PG8_LAS unsigned*)(lds + (bufoff) + ldsw + _i * 8192), 16, 0, 0); } while (0)
; #define PG8_LDA(dst, b, h) do { _Pragma("unroll") for (int m = 0; m < 4; ++m) _Pragma("unroll") for (int k = 0; k < 2; ++k) dst[m][k] = *(const PG8_LAS bf16x8*)(lds + PG8_SA(b, h) + aoff + m * 2048 + k * 1024); } while (0)
; #define PG8_LDB(dst, b, h) do { _Pragma("unroll") for (int n = 0; n < 2; ++n) _Pragma("unroll") for (int k = 0; k < 2; ++k) dst[n][k] = *(const PG8_LAS bf16x8*)(lds + PG8_SB(b, h) + boff + n * 2048 + k * 1024); } while (0)
; #define PG8_MMA(ai, bj, At, Bt) do { __builtin_amdgcn_s_setprio(1); _Pragma("unroll") for (int m = 0; m < 4; ++m) _Pragma("unroll") for (int n = 0; n < 2; ++n) _Pragma("unroll") for (int k = 0; k < 2; ++k) \
;         acc[ai][bj][m][n] = __builtin_amdgcn_mfma_f32_16x16x32_bf16(Bt[n][k], At[m][k], acc[ai][bj][m][n], 0, 0, 0); __builtin_amdgcn_s_setprio(0); } while (0)
; #define PG8_WAIT_V(n) asm volatile("s_waitcnt vmcnt(" #n ")" ::: "memory")
; #define PG8_WAIT_L(n) asm volatile("s_waitcnt lgkmcnt(" #n ")" ::: "memory")
; #define PG8_BAR __builtin_amdgcn_s_barrier()
; #define PG8_SCHED __builtin_amdgcn_sched_barrier(0)
; template <class Epi, class Sched, bool ALIGN_EPI = false>
; __device__ __forceinline__ void gemm_phase(PG8_LAS unsigned char* lds, const Gemm g, const Sched& S, const Epi& E) {
;     ...
;             PG8_WAIT_V(8); PG8_WAIT_L(0); PG8_BAR; PG8_MMA(1, 0, At, B0); PG8_MMA(1, 1, At, B1); PG8_BAR; PG8_SCHED;
;             PG8_LDB(B0, 1, 0); PG8_LDB(B1, 1, 1); PG8_SCHED; PG8_LDA(At, 1, 0); PG8_STAGE(PG8_SA(0, 1), a2 + hstepA, w1);
;             PG8_WAIT_V(8); PG8_WAIT_L(0); PG8_BAR; PG8_MMA(0, 0, At, B0); PG8_MMA(0, 1, At, B1); PG8_BAR; PG8_SCHED;
	s_setprio 1
	v_mfma_f32_16x16x32_bf16 v[54:57], v[142:145], v[186:189], v[54:57]
	v_mfma_f32_16x16x32_bf16 v[42:45], v[162:165], v[186:189], v[42:45]
	v_mfma_f32_16x16x32_bf16 v[30:33], v[142:145], v[194:197], v[30:33]
	v_mfma_f32_16x16x32_bf16 v[26:29], v[162:165], v[194:197], v[26:29]
	v_mfma_f32_16x16x32_bf16 v[14:17], v[142:145], v[202:205], v[14:17]
	v_mfma_f32_16x16x32_bf16 v[10:13], v[162:165], v[202:205], v[10:13]
	v_mfma_f32_16x16x32_bf16 v[6:9], v[142:145], v[210:213], v[6:9]
	v_mfma_f32_16x16x32_bf16 v[2:5], v[162:165], v[210:213], v[2:5]
	v_mfma_f32_16x16x32_bf16 v[54:57], v[158:161], v[190:193], v[54:57]
	v_mfma_f32_16x16x32_bf16 v[42:45], v[166:169], v[190:193], v[42:45]
	v_mfma_f32_16x16x32_bf16 v[30:33], v[158:161], v[198:201], v[30:33]
	v_mfma_f32_16x16x32_bf16 v[26:29], v[166:169], v[198:201], v[26:29]
	v_mfma_f32_16x16x32_bf16 v[14:17], v[158:161], v[206:209], v[14:17]
	v_mfma_f32_16x16x32_bf16 v[10:13], v[166:169], v[206:209], v[10:13]
	v_mfma_f32_16x16x32_bf16 v[6:9], v[158:161], v[214:217], v[6:9]
	v_mfma_f32_16x16x32_bf16 v[2:5], v[166:169], v[214:217], v[2:5]
	v_mfma_f32_16x16x32_bf16 v[70:73], v[170:173], v[186:189], v[70:73]
	v_mfma_f32_16x16x32_bf16 v[66:69], v[178:181], v[186:189], v[66:69]
	v_mfma_f32_16x16x32_bf16 v[50:53], v[170:173], v[194:197], v[50:53]
	v_mfma_f32_16x16x32_bf16 v[46:49], v[178:181], v[194:197], v[46:49]
	v_mfma_f32_16x16x32_bf16 v[38:41], v[170:173], v[202:205], v[38:41]
	v_mfma_f32_16x16x32_bf16 v[34:37], v[178:181], v[202:205], v[34:37]
	v_mfma_f32_16x16x32_bf16 v[22:25], v[170:173], v[210:213], v[22:25]
	v_mfma_f32_16x16x32_bf16 v[18:21], v[178:181], v[210:213], v[18:21]
	v_mfma_f32_16x16x32_bf16 v[70:73], v[174:177], v[190:193], v[70:73]
	v_mfma_f32_16x16x32_bf16 v[66:69], v[182:185], v[190:193], v[66:69]
	v_mfma_f32_16x16x32_bf16 v[50:53], v[174:177], v[198:201], v[50:53]
	v_mfma_f32_16x16x32_bf16 v[46:49], v[182:185], v[198:201], v[46:49]
	v_mfma_f32_16x16x32_bf16 v[38:41], v[174:177], v[206:209], v[38:41]
	v_mfma_f32_16x16x32_bf16 v[34:37], v[182:185], v[206:209], v[34:37]
	v_mfma_f32_16x16x32_bf16 v[22:25], v[174:177], v[214:217], v[22:25]
	v_mfma_f32_16x16x32_bf16 v[18:21], v[182:185], v[214:217], v[18:21]
	s_setprio 0
	s_barrier
	s_add_i32 s93, 0, 0x18000
	s_add_i32 s94, 0, 0x1c000
	v_add_u32_e32 v166, s93, v147
	v_add_u32_e32 v182, s94, v147
	ds_read_b128 v[142:145], v166
	ds_read_b128 v[158:161], v166 offset:1024
	ds_read_b128 v[162:165], v166 offset:2048
	ds_read_b128 v[166:169], v166 offset:3072
	ds_read_b128 v[170:173], v182
	ds_read_b128 v[174:177], v182 offset:1024
	ds_read_b128 v[178:181], v182 offset:2048
	ds_read_b128 v[182:185], v182 offset:3072
	s_add_u32 s64, s64, 0x20000
	s_addc_u32 s65, s65, 0
	s_mov_b32 m0, s68
	v_lshl_add_u64 v[226:227], s[64:65], 0, v[130:131]
	ds_read_b128 v[186:189], v157 offset:32768
	ds_read_b128 v[190:193], v157 offset:33792
	ds_read_b128 v[194:197], v157 offset:34816
	ds_read_b128 v[198:201], v157 offset:35840
	ds_read_b128 v[202:205], v157 offset:36864
	ds_read_b128 v[206:209], v157 offset:37888
	ds_read_b128 v[210:213], v157 offset:38912
	ds_read_b128 v[214:217], v157 offset:39936
	global_load_lds_dwordx4 v[226:227], off
	v_lshl_add_u64 v[226:227], s[64:65], 0, v[134:135]
	s_mov_b32 m0, s69
	s_nop 0
	global_load_lds_dwordx4 v[226:227], off
	s_waitcnt vmcnt(8)
	s_waitcnt lgkmcnt(0)
	s_barrier
	s_setprio 1
	v_mfma_f32_16x16x32_bf16 v[126:129], v[142:145], v[186:189], v[126:129]
	v_mfma_f32_16x16x32_bf16 v[122:125], v[162:165], v[186:189], v[122:125]
	v_mfma_f32_16x16x32_bf16 v[114:117], v[142:145], v[194:197], v[114:117]
	v_mfma_f32_16x16x32_bf16 v[106:109], v[162:165], v[194:197], v[106:109]
	v_mfma_f32_16x16x32_bf16 v[98:101], v[142:145], v[202:205], v[98:101]
	v_mfma_f32_16x16x32_bf16 v[90:93], v[162:165], v[202:205], v[90:93]
	v_mfma_f32_16x16x32_bf16 v[82:85], v[142:145], v[210:213], v[82:85]
	v_mfma_f32_16x16x32_bf16 v[74:77], v[162:165], v[210:213], v[74:77]
	v_mfma_f32_16x16x32_bf16 v[126:129], v[158:161], v[190:193], v[126:129]
	v_mfma_f32_16x16x32_bf16 v[122:125], v[166:169], v[190:193], v[122:125]
	v_mfma_f32_16x16x32_bf16 v[114:117], v[158:161], v[198:201], v[114:117]
	v_mfma_f32_16x16x32_bf16 v[106:109], v[166:169], v[198:201], v[106:109]
	v_mfma_f32_16x16x32_bf16 v[98:101], v[158:161], v[206:209], v[98:101]
	v_mfma_f32_16x16x32_bf16 v[90:93], v[166:169], v[206:209], v[90:93]
	v_mfma_f32_16x16x32_bf16 v[82:85], v[158:161], v[214:217], v[82:85]
	v_mfma_f32_16x16x32_bf16 v[74:77], v[166:169], v[214:217], v[74:77]
	v_mfma_f32_16x16x32_bf16 v[118:121], v[170:173], v[186:189], v[118:121]
	v_mfma_f32_16x16x32_bf16 v[110:113], v[178:181], v[186:189], v[110:113]
	v_mfma_f32_16x16x32_bf16 v[102:105], v[170:173], v[194:197], v[102:105]
	v_mfma_f32_16x16x32_bf16 v[94:97], v[178:181], v[194:197], v[94:97]
	v_mfma_f32_16x16x32_bf16 v[86:89], v[170:173], v[202:205], v[86:89]
	v_mfma_f32_16x16x32_bf16 v[78:81], v[178:181], v[202:205], v[78:81]
	v_mfma_f32_16x16x32_bf16 v[62:65], v[170:173], v[210:213], v[62:65]
	v_mfma_f32_16x16x32_bf16 v[58:61], v[178:181], v[210:213], v[58:61]
	v_mfma_f32_16x16x32_bf16 v[118:121], v[174:177], v[190:193], v[118:121]
	v_mfma_f32_16x16x32_bf16 v[110:113], v[182:185], v[190:193], v[110:113]
	v_mfma_f32_16x16x32_bf16 v[102:105], v[174:177], v[198:201], v[102:105]
	v_mfma_f32_16x16x32_bf16 v[94:97], v[182:185], v[198:201], v[94:97]
	v_mfma_f32_16x16x32_bf16 v[86:89], v[174:177], v[206:209], v[86:89]
	v_mfma_f32_16x16x32_bf16 v[78:81], v[182:185], v[206:209], v[78:81]
	v_mfma_f32_16x16x32_bf16 v[62:65], v[174:177], v[214:217], v[62:65]
	v_mfma_f32_16x16x32_bf16 v[58:61], v[182:185], v[214:217], v[58:61]
	s_setprio 0
	s_barrier
; #define PG8_STAGE(bufoff, gbase, voff) do { _Pragma("unroll") for (int _i = 0; _i < 2; ++_i) \
;         __builtin_amdgcn_global_load_lds((const unsigned*)((const char*)(gbase) + (voff)[_i]), (PG8_LAS unsigned*)(lds + (bufoff) + ldsw + _i * 8192), 16, 0, 0); } while (0)
; #define PG8_LDA(dst, b, h) do { _Pragma("unroll") for (int m = 0; m < 4; ++m) _Pragma("unroll") for (int k = 0; k < 2; ++k) dst[m][k] = *(const PG8_LAS bf16x8*)(lds + PG8_SA(b, h) + aoff + m * 2048 + k * 1024); } while (0)
; #define PG8_MMA(ai, bj, At, Bt) do { __builtin_amdgcn_s_setprio(1); _Pragma("unroll") for (int m = 0; m < 4; ++m) _Pragma("unroll") for (int n = 0; n < 2; ++n) _Pragma("unroll") for (int k = 0; k < 2; ++k) \
;         acc[ai][bj][m][n] = __builtin_amdgcn_mfma_f32_16x16x32_bf16(Bt[n][k], At[m][k], acc[ai][bj][m][n], 0, 0, 0); __builtin_amdgcn_s_setprio(0); } while (0)
; #define PG8_WAIT_V(n) asm volatile("s_waitcnt vmcnt(" #n ")" ::: "memory")
; #define PG8_WAIT_L(n) asm volatile("s_waitcnt lgkmcnt(" #n ")" ::: "memory")
; #define PG8_BAR __builtin_amdgcn_s_barrier()
; #define PG8_SCHED __builtin_amdgcn_sched_barrier(0)
; template <class Epi, class Sched, bool ALIGN_EPI = false>
; __device__ __forceinline__ void gemm_phase(PG8_LAS unsigned char* lds, const Gemm g, const Sched& S, const Epi& E) {
;     ...
;         for (int t = 0; t < nt; t += 2) {
;     ...
;             PG8_LDA(At, 1, 1); PG8_STAGE(PG8_SB(1, 0), b3, voffB); PG8_STAGE(PG8_SB(1, 1), b3 + hstep, voffB); PG8_STAGE(PG8_SA(1, 0), a3, w0);
;             PG8_WAIT_V(8); PG8_WAIT_L(0); PG8_BAR; PG8_MMA(1, 0, At, B0); PG8_MMA(1, 1, At, B1); PG8_BAR; PG8_SCHED;
;             if constexpr (Epi::KSCALE) { if (((t + 2) & 7) == 0 && t + 2 < nt) { E.kscale(acc, pf, ((t + 2) >> 3) - 1, wr, fr); PG8_SCHED; } }
;         }
	s_add_i32 s64, s93, s66
	v_lshl_add_u64 v[218:219], v[218:219], 0, s[18:19]
	s_mov_b32 m0, s64
	ds_read_b128 v[186:189], v157 offset:49152
	ds_read_b128 v[190:193], v157 offset:50176
	ds_read_b128 v[194:197], v157 offset:51200
	ds_read_b128 v[198:201], v157 offset:52224
	ds_read_b128 v[202:205], v157 offset:53248
	ds_read_b128 v[206:209], v157 offset:54272
	ds_read_b128 v[210:213], v157 offset:55296
	ds_read_b128 v[214:217], v157 offset:56320
	global_load_lds_dwordx4 v[218:219], off
	s_add_i32 m0, s64, 0x2000
	s_add_u32 s62, s62, 0x20080
	v_lshl_add_u64 v[218:219], v[220:221], 0, s[18:19]
	s_addc_u32 s63, s63, 0
	s_add_i32 s64, s94, s66
	global_load_lds_dwordx4 v[218:219], off
	v_lshl_add_u64 v[218:219], s[62:63], 0, v[132:133]
	s_mov_b32 m0, s64
	s_nop 0
	global_load_lds_dwordx4 v[218:219], off
	v_lshl_add_u64 v[218:219], s[62:63], 0, v[136:137]
	s_add_i32 m0, s64, 0x2000
	s_nop 0
	global_load_lds_dwordx4 v[218:219], off
	v_lshl_add_u64 v[218:219], v[222:223], 0, s[18:19]
	s_mov_b32 m0, s73
	s_nop 0
	global_load_lds_dwordx4 v[218:219], off
	v_lshl_add_u64 v[218:219], v[224:225], 0, s[18:19]
	s_mov_b32 m0, s74
	s_nop 0
	global_load_lds_dwordx4 v[218:219], off
	s_waitcnt vmcnt(8)
	s_waitcnt lgkmcnt(0)
	s_barrier
	s_setprio 1
	v_mfma_f32_16x16x32_bf16 v[54:57], v[142:145], v[186:189], v[54:57]
	v_mfma_f32_16x16x32_bf16 v[42:45], v[162:165], v[186:189], v[42:45]
	v_mfma_f32_16x16x32_bf16 v[30:33], v[142:145], v[194:197], v[30:33]
	v_mfma_f32_16x16x32_bf16 v[26:29], v[162:165], v[194:197], v[26:29]
	v_mfma_f32_16x16x32_bf16 v[14:17], v[142:145], v[202:205], v[14:17]
	v_mfma_f32_16x16x32_bf16 v[10:13], v[162:165], v[202:205], v[10:13]
	v_mfma_f32_16x16x32_bf16 v[6:9], v[142:145], v[210:213], v[6:9]
	v_mfma_f32_16x16x32_bf16 v[2:5], v[162:165], v[210:213], v[2:5]
	v_mfma_f32_16x16x32_bf16 v[54:57], v[158:161], v[190:193], v[54:57]
	v_mfma_f32_16x16x32_bf16 v[42:45], v[166:169], v[190:193], v[42:45]
	v_mfma_f32_16x16x32_bf16 v[30:33], v[158:161], v[198:201], v[30:33]
	v_mfma_f32_16x16x32_bf16 v[26:29], v[166:169], v[198:201], v[26:29]
	v_mfma_f32_16x16x32_bf16 v[14:17], v[158:161], v[206:209], v[14:17]
	v_mfma_f32_16x16x32_bf16 v[10:13], v[166:169], v[206:209], v[10:13]
	v_mfma_f32_16x16x32_bf16 v[6:9], v[158:161], v[214:217], v[6:9]
	v_mfma_f32_16x16x32_bf16 v[2:5], v[166:169], v[214:217], v[2:5]
	v_mfma_f32_16x16x32_bf16 v[70:73], v[170:173], v[186:189], v[70:73]
	v_mfma_f32_16x16x32_bf16 v[66:69], v[178:181], v[186:189], v[66:69]
	v_mfma_f32_16x16x32_bf16 v[50:53], v[170:173], v[194:197], v[50:53]
	v_mfma_f32_16x16x32_bf16 v[46:49], v[178:181], v[194:197], v[46:49]
	v_mfma_f32_16x16x32_bf16 v[38:41], v[170:173], v[202:205], v[38:41]
	v_mfma_f32_16x16x32_bf16 v[34:37], v[178:181], v[202:205], v[34:37]
	v_mfma_f32_16x16x32_bf16 v[22:25], v[170:173], v[210:213], v[22:25]
	v_mfma_f32_16x16x32_bf16 v[18:21], v[178:181], v[210:213], v[18:21]
	v_mfma_f32_16x16x32_bf16 v[70:73], v[174:177], v[190:193], v[70:73]
	v_mfma_f32_16x16x32_bf16 v[66:69], v[182:185], v[190:193], v[66:69]
	v_mfma_f32_16x16x32_bf16 v[50:53], v[174:177], v[198:201], v[50:53]
	v_mfma_f32_16x16x32_bf16 v[46:49], v[182:185], v[198:201], v[46:49]
	v_mfma_f32_16x16x32_bf16 v[38:41], v[174:177], v[206:209], v[38:41]
	v_mfma_f32_16x16x32_bf16 v[34:37], v[182:185], v[206:209], v[34:37]
	v_mfma_f32_16x16x32_bf16 v[22:25], v[174:177], v[214:217], v[22:25]
	v_mfma_f32_16x16x32_bf16 v[18:21], v[182:185], v[214:217], v[18:21]
	s_setprio 0
	s_barrier
	s_add_i32 s92, s92, 2
	s_add_u32 s90, s90, 0x100
	s_addc_u32 s91, s91, 0
	s_add_u32 s60, s60, 0x100
	s_addc_u32 s61, s61, 0
	s_cmp_gt_u32 s92, 5
	s_cbranch_scc0 .LBB0_805
	s_and_b64 vcc, exec, s[22:23]
	s_cbranch_vccz .LBB0_808
	s_barrier

; #define PG8_STAGE(bufoff, gbase, voff) do { _Pragma("unroll") for (int _i = 0; _i < 2; ++_i) \
;         __builtin_amdgcn_global_load_lds((const unsigned*)((const char*)(gbase) + (voff)[_i]), (PG8_LAS unsigned*)(lds + (bufoff) + ldsw + _i * 8192), 16, 0, 0); } while (0)
; #define PG8_LDA(dst, b, h) do { _Pragma("unroll") for (int m = 0; m < 4; ++m) _Pragma("unroll") for (int k = 0; k < 2; ++k) dst[m][k] = *(const PG8_LAS bf16x8*)(lds + PG8_SA(b, h) + aoff + m * 2048 + k * 1024); } while (0)
; #define PG8_LDB(dst, b, h) do { _Pragma("unroll") for (int n = 0; n < 2; ++n) _Pragma("unroll") for (int k = 0; k < 2; ++k) dst[n][k] = *(const PG8_LAS bf16x8*)(lds + PG8_SB(b, h) + boff + n * 2048 + k * 1024); } while (0)
; #define PG8_MMA(ai, bj, At, Bt) do { __builtin_amdgcn_s_setprio(1); _Pragma("unroll") for (int m = 0; m < 4; ++m) _Pragma("unroll") for (int n = 0; n < 2; ++n) _Pragma("unroll") for (int k = 0; k < 2; ++k) \
;         acc[ai][bj][m][n] = __builtin_amdgcn_mfma_f32_16x16x32_bf16(Bt[n][k], At[m][k], acc[ai][bj][m][n], 0, 0, 0); __builtin_amdgcn_s_setprio(0); } while (0)
; #define PG8_WAIT_V(n) asm volatile("s_waitcnt vmcnt(" #n ")" ::: "memory")
; #define PG8_WAIT_L(n) asm volatile("s_waitcnt lgkmcnt(" #n ")" ::: "memory")
; #define PG8_BAR __builtin_amdgcn_s_barrier()
; #define PG8_SCHED __builtin_amdgcn_sched_barrier(0)
; template <class Epi, class Sched, bool ALIGN_EPI = false>
; __device__ __forceinline__ void gemm_phase(PG8_LAS unsigned char* lds, const Gemm g, const Sched& S, const Epi& E) {
;     ...
;             PG8_LDB(B0, 0, 0); PG8_LDB(B1, 0, 1); PG8_SCHED; PG8_LDA(At, 0, 0); PG8_STAGE(PG8_SA(1, 1), a1 + hstepA, vc1);
;             PG8_WAIT_V(8); PG8_WAIT_L(0); PG8_BAR; PG8_MMA(0, 0, At, B0); PG8_MMA(0, 1, At, B1); PG8_BAR; PG8_SCHED;
;             PG8_LDA(At, 0, 1); PG8_STAGE(PG8_SB(0, 0), b2, voffB); PG8_STAGE(PG8_SB(0, 1), b2 + hstep, voffB); PG8_STAGE(PG8_SA(0, 0), a2, w0);
;             PG8_WAIT_V(8); PG8_WAIT_L(0); PG8_BAR; PG8_MMA(1, 0, At, B0); PG8_MMA(1, 1, At, B1); PG8_BAR; PG8_SCHED;
.LBB0_908:
	ds_read_b128 v[144:147], v157
	ds_read_b128 v[160:163], v157 offset:1024
	ds_read_b128 v[164:167], v157 offset:2048
	ds_read_b128 v[168:171], v157 offset:3072
	ds_read_b128 v[172:175], v158
	ds_read_b128 v[176:179], v158 offset:1024
	ds_read_b128 v[180:183], v158 offset:2048
	ds_read_b128 v[184:187], v158 offset:3072
	s_add_u32 s58, s56, 0xfffe0080
	s_addc_u32 s59, s57, -1
	s_cmp_eq_u32 s92, 4
	s_cselect_b32 s61, s41, s59
	s_cselect_b32 s60, s47, s58
	s_cselect_b32 s59, s43, s91
	s_cselect_b32 s58, s89, s90
	v_lshl_add_u64 v[220:221], s[56:57], 0, v[142:143]
	s_add_i32 m0, s49, 0xc000
	ds_read_b128 v[188:191], v159
	ds_read_b128 v[192:195], v159 offset:1024
	ds_read_b128 v[196:199], v159 offset:2048
	ds_read_b128 v[200:203], v159 offset:3072
	ds_read_b128 v[204:207], v159 offset:4096
	ds_read_b128 v[208:211], v159 offset:5120
	ds_read_b128 v[212:215], v159 offset:6144
	ds_read_b128 v[216:219], v159 offset:7168
	global_load_lds_dwordx4 v[220:221], off
	v_lshl_add_u64 v[220:221], s[56:57], 0, v[140:141]
	s_add_i32 m0, s49, 0xe000
	s_nop 0
	global_load_lds_dwordx4 v[220:221], off
	s_waitcnt vmcnt(8)
	s_waitcnt lgkmcnt(0)
	s_barrier
	s_setprio 1
	v_mfma_f32_16x16x32_bf16 v[126:129], v[144:147], v[188:191], v[126:129]
	v_mfma_f32_16x16x32_bf16 v[122:125], v[164:167], v[188:191], v[122:125]
	v_mfma_f32_16x16x32_bf16 v[114:117], v[144:147], v[196:199], v[114:117]
	v_mfma_f32_16x16x32_bf16 v[106:109], v[164:167], v[196:199], v[106:109]
	v_mfma_f32_16x16x32_bf16 v[98:101], v[144:147], v[204:207], v[98:101]
	v_mfma_f32_16x16x32_bf16 v[90:93], v[164:167], v[204:207], v[90:93]
	v_mfma_f32_16x16x32_bf16 v[82:85], v[144:147], v[212:215], v[82:85]
	v_mfma_f32_16x16x32_bf16 v[74:77], v[164:167], v[212:215], v[74:77]
	v_mfma_f32_16x16x32_bf16 v[126:129], v[160:163], v[192:195], v[126:129]
	v_mfma_f32_16x16x32_bf16 v[122:125], v[168:171], v[192:195], v[122:125]
	v_mfma_f32_16x16x32_bf16 v[114:117], v[160:163], v[200:203], v[114:117]
	v_mfma_f32_16x16x32_bf16 v[106:109], v[168:171], v[200:203], v[106:109]
	v_mfma_f32_16x16x32_bf16 v[98:101], v[160:163], v[208:211], v[98:101]
	v_mfma_f32_16x16x32_bf16 v[90:93], v[168:171], v[208:211], v[90:93]
	v_mfma_f32_16x16x32_bf16 v[82:85], v[160:163], v[216:219], v[82:85]
	v_mfma_f32_16x16x32_bf16 v[74:77], v[168:171], v[216:219], v[74:77]
	v_mfma_f32_16x16x32_bf16 v[118:121], v[172:175], v[188:191], v[118:121]
	v_mfma_f32_16x16x32_bf16 v[110:113], v[180:183], v[188:191], v[110:113]
	v_mfma_f32_16x16x32_bf16 v[102:105], v[172:175], v[196:199], v[102:105]
	v_mfma_f32_16x16x32_bf16 v[94:97], v[180:183], v[196:199], v[94:97]
	v_mfma_f32_16x16x32_bf16 v[86:89], v[172:175], v[204:207], v[86:89]
	v_mfma_f32_16x16x32_bf16 v[78:81], v[180:183], v[204:207], v[78:81]
	v_mfma_f32_16x16x32_bf16 v[62:65], v[172:175], v[212:215], v[62:65]
	v_mfma_f32_16x16x32_bf16 v[58:61], v[180:183], v[212:215], v[58:61]
	v_mfma_f32_16x16x32_bf16 v[118:121], v[176:179], v[192:195], v[118:121]
	v_mfma_f32_16x16x32_bf16 v[110:113], v[184:187], v[192:195], v[110:113]
	v_mfma_f32_16x16x32_bf16 v[102:105], v[176:179], v[200:203], v[102:105]
	v_mfma_f32_16x16x32_bf16 v[94:97], v[184:187], v[200:203], v[94:97]
	v_mfma_f32_16x16x32_bf16 v[86:89], v[176:179], v[208:211], v[86:89]
	v_mfma_f32_16x16x32_bf16 v[78:81], v[184:187], v[208:211], v[78:81]
	v_mfma_f32_16x16x32_bf16 v[62:65], v[176:179], v[216:219], v[62:65]
	v_mfma_f32_16x16x32_bf16 v[58:61], v[184:187], v[216:219], v[58:61]
	s_setprio 0
	s_barrier
	s_add_i32 s93, s79, s66
	v_lshl_add_u64 v[220:221], s[58:59], 0, v[134:135]
	s_mov_b32 m0, s93
	ds_read_b128 v[188:191], v159 offset:16384
	ds_read_b128 v[192:195], v159 offset:17408
	ds_read_b128 v[196:199], v159 offset:18432
	ds_read_b128 v[200:203], v159 offset:19456
	ds_read_b128 v[204:207], v159 offset:20480
	ds_read_b128 v[208:211], v159 offset:21504
	ds_read_b128 v[212:215], v159 offset:22528
	ds_read_b128 v[216:219], v159 offset:23552
	global_load_lds_dwordx4 v[220:221], off
	s_add_i32 m0, s93, 0x2000
	s_add_u32 s94, s58, 0x20000
	v_lshl_add_u64 v[222:223], s[58:59], 0, v[138:139]
	s_addc_u32 s95, s59, 0
	s_add_i32 s93, s80, s66
	global_load_lds_dwordx4 v[222:223], off
	v_lshl_add_u64 v[224:225], s[94:95], 0, v[134:135]
	s_mov_b32 m0, s93
	v_lshl_add_u64 v[226:227], s[60:61], 0, v[136:137]
	global_load_lds_dwordx4 v[224:225], off
	v_lshl_add_u64 v[224:225], s[94:95], 0, v[138:139]
	s_add_i32 m0, s93, 0x2000
	s_nop 0
	global_load_lds_dwordx4 v[224:225], off
	v_lshl_add_u64 v[224:225], s[60:61], 0, v[132:133]
	s_mov_b32 m0, s49
	s_nop 0
	global_load_lds_dwordx4 v[224:225], off
	s_mov_b32 m0, s67
	s_nop 0
	global_load_lds_dwordx4 v[226:227], off
	s_waitcnt vmcnt(8)
	s_waitcnt lgkmcnt(0)
	s_barrier
; #define PG8_STAGE(bufoff, gbase, voff) do { _Pragma("unroll") for (int _i = 0; _i < 2; ++_i) \
;         __builtin_amdgcn_global_load_lds((const unsigned*)((const char*)(gbase) + (voff)[_i]), (PG8_LAS unsigned*)(lds + (bufoff) + ldsw + _i * 8192), 16, 0, 0); } while (0)
; #define PG8_LDA(dst, b, h) do { _Pragma("unroll") for (int m = 0; m < 4; ++m) _Pragma("unroll") for (int k = 0; k < 2; ++k) dst[m][k] = *(const PG8_LAS bf16x8*)(lds + PG8_SA(b, h) + aoff + m * 2048 + k * 1024); } while (0)
; #define PG8_LDB(dst, b, h) do { _Pragma("unroll") for (int n = 0; n < 2; ++n) _Pragma("unroll") for (int k = 0; k < 2; ++k) dst[n][k] = *(const PG8_LAS bf16x8*)(lds + PG8_SB(b, h) + boff + n * 2048 + k * 1024); } while (0)
; #define PG8_MMA(ai, bj, At, Bt) do { __builtin_amdgcn_s_setprio(1); _Pragma("unroll") for (int m = 0; m < 4; ++m) _Pragma("unroll") for (int n = 0; n < 2; ++n) _Pragma("unroll") for (int k = 0; k < 2; ++k) \
;         acc[ai][bj][m][n] = __builtin_amdgcn_mfma_f32_16x16x32_bf16(Bt[n][k], At[m][k], acc[ai][bj][m][n], 0, 0, 0); __builtin_amdgcn_s_setprio(0); } while (0)
; #define PG8_WAIT_V(n) asm volatile("s_waitcnt vmcnt(" #n ")" ::: "memory")
; #define PG8_WAIT_L(n) asm volatile("s_waitcnt lgkmcnt(" #n ")" ::: "memory")
; #define PG8_BAR __builtin_amdgcn_s_barrier()
; #define PG8_SCHED __builtin_amdgcn_sched_barrier(0)
; template <class Epi, class Sched, bool ALIGN_EPI = false>
; __device__ __forceinline__ void gemm_phase(PG8_LAS unsigned char* lds, const Gemm g, const Sched& S, const Epi& E) {
;     ...
;             PG8_WAIT_V(8); PG8_WAIT_L(0); PG8_BAR; PG8_MMA(1, 0, At, B0); PG8_MMA(1, 1, At, B1); PG8_BAR; PG8_SCHED;
;             PG8_LDB(B0, 1, 0); PG8_LDB(B1, 1, 1); PG8_SCHED; PG8_LDA(At, 1, 0); PG8_STAGE(PG8_SA(0, 1), a2 + hstepA, w1);
;             PG8_WAIT_V(8); PG8_WAIT_L(0); PG8_BAR; PG8_MMA(0, 0, At, B0); PG8_MMA(0, 1, At, B1); PG8_BAR; PG8_SCHED;
	s_setprio 1
	v_mfma_f32_16x16x32_bf16 v[54:57], v[144:147], v[188:191], v[54:57]
	v_mfma_f32_16x16x32_bf16 v[42:45], v[164:167], v[188:191], v[42:45]
	v_mfma_f32_16x16x32_bf16 v[30:33], v[144:147], v[196:199], v[30:33]
	v_mfma_f32_16x16x32_bf16 v[26:29], v[164:167], v[196:199], v[26:29]
	v_mfma_f32_16x16x32_bf16 v[14:17], v[144:147], v[204:207], v[14:17]
	v_mfma_f32_16x16x32_bf16 v[10:13], v[164:167], v[204:207], v[10:13]
	v_mfma_f32_16x16x32_bf16 v[6:9], v[144:147], v[212:215], v[6:9]
	v_mfma_f32_16x16x32_bf16 v[2:5], v[164:167], v[212:215], v[2:5]
	v_mfma_f32_16x16x32_bf16 v[54:57], v[160:163], v[192:195], v[54:57]
	v_mfma_f32_16x16x32_bf16 v[42:45], v[168:171], v[192:195], v[42:45]
	v_mfma_f32_16x16x32_bf16 v[30:33], v[160:163], v[200:203], v[30:33]
	v_mfma_f32_16x16x32_bf16 v[26:29], v[168:171], v[200:203], v[26:29]
	v_mfma_f32_16x16x32_bf16 v[14:17], v[160:163], v[208:211], v[14:17]
	v_mfma_f32_16x16x32_bf16 v[10:13], v[168:171], v[208:211], v[10:13]
	v_mfma_f32_16x16x32_bf16 v[6:9], v[160:163], v[216:219], v[6:9]
	v_mfma_f32_16x16x32_bf16 v[2:5], v[168:171], v[216:219], v[2:5]
	v_mfma_f32_16x16x32_bf16 v[70:73], v[172:175], v[188:191], v[70:73]
	v_mfma_f32_16x16x32_bf16 v[66:69], v[180:183], v[188:191], v[66:69]
	v_mfma_f32_16x16x32_bf16 v[50:53], v[172:175], v[196:199], v[50:53]
	v_mfma_f32_16x16x32_bf16 v[46:49], v[180:183], v[196:199], v[46:49]
	v_mfma_f32_16x16x32_bf16 v[38:41], v[172:175], v[204:207], v[38:41]
	v_mfma_f32_16x16x32_bf16 v[34:37], v[180:183], v[204:207], v[34:37]
	v_mfma_f32_16x16x32_bf16 v[22:25], v[172:175], v[212:215], v[22:25]
	v_mfma_f32_16x16x32_bf16 v[18:21], v[180:183], v[212:215], v[18:21]
	v_mfma_f32_16x16x32_bf16 v[70:73], v[176:179], v[192:195], v[70:73]
	v_mfma_f32_16x16x32_bf16 v[66:69], v[184:187], v[192:195], v[66:69]
	v_mfma_f32_16x16x32_bf16 v[50:53], v[176:179], v[200:203], v[50:53]
	v_mfma_f32_16x16x32_bf16 v[46:49], v[184:187], v[200:203], v[46:49]
	v_mfma_f32_16x16x32_bf16 v[38:41], v[176:179], v[208:211], v[38:41]
	v_mfma_f32_16x16x32_bf16 v[34:37], v[184:187], v[208:211], v[34:37]
	v_mfma_f32_16x16x32_bf16 v[22:25], v[176:179], v[216:219], v[22:25]
	v_mfma_f32_16x16x32_bf16 v[18:21], v[184:187], v[216:219], v[18:21]
	s_setprio 0
	s_barrier
	s_add_i32 s93, 0, 0x18000
	s_add_i32 s94, 0, 0x1c000
	v_add_u32_e32 v168, s93, v148
	v_add_u32_e32 v184, s94, v148
	ds_read_b128 v[144:147], v168
	ds_read_b128 v[160:163], v168 offset:1024
	ds_read_b128 v[164:167], v168 offset:2048
	ds_read_b128 v[168:171], v168 offset:3072
	ds_read_b128 v[172:175], v184
	ds_read_b128 v[176:179], v184 offset:1024
	ds_read_b128 v[180:183], v184 offset:2048
	ds_read_b128 v[184:187], v184 offset:3072
	s_add_u32 s60, s60, 0x20000
	s_addc_u32 s61, s61, 0
	s_mov_b32 m0, s68
	v_lshl_add_u64 v[228:229], s[60:61], 0, v[132:133]
	ds_read_b128 v[188:191], v159 offset:32768
	ds_read_b128 v[192:195], v159 offset:33792
	ds_read_b128 v[196:199], v159 offset:34816
	ds_read_b128 v[200:203], v159 offset:35840
	ds_read_b128 v[204:207], v159 offset:36864
	ds_read_b128 v[208:211], v159 offset:37888
	ds_read_b128 v[212:215], v159 offset:38912
	ds_read_b128 v[216:219], v159 offset:39936
	global_load_lds_dwordx4 v[228:229], off
	v_lshl_add_u64 v[228:229], s[60:61], 0, v[136:137]
	s_mov_b32 m0, s69
	s_nop 0
	global_load_lds_dwordx4 v[228:229], off
	s_waitcnt vmcnt(8)
	s_waitcnt lgkmcnt(0)
	s_barrier
	s_setprio 1
	v_mfma_f32_16x16x32_bf16 v[126:129], v[144:147], v[188:191], v[126:129]
	v_mfma_f32_16x16x32_bf16 v[122:125], v[164:167], v[188:191], v[122:125]
	v_mfma_f32_16x16x32_bf16 v[114:117], v[144:147], v[196:199], v[114:117]
	v_mfma_f32_16x16x32_bf16 v[106:109], v[164:167], v[196:199], v[106:109]
	v_mfma_f32_16x16x32_bf16 v[98:101], v[144:147], v[204:207], v[98:101]
	v_mfma_f32_16x16x32_bf16 v[90:93], v[164:167], v[204:207], v[90:93]
	v_mfma_f32_16x16x32_bf16 v[82:85], v[144:147], v[212:215], v[82:85]
	v_mfma_f32_16x16x32_bf16 v[74:77], v[164:167], v[212:215], v[74:77]
	v_mfma_f32_16x16x32_bf16 v[126:129], v[160:163], v[192:195], v[126:129]
	v_mfma_f32_16x16x32_bf16 v[122:125], v[168:171], v[192:195], v[122:125]
	v_mfma_f32_16x16x32_bf16 v[114:117], v[160:163], v[200:203], v[114:117]
	v_mfma_f32_16x16x32_bf16 v[106:109], v[168:171], v[200:203], v[106:109]
	v_mfma_f32_16x16x32_bf16 v[98:101], v[160:163], v[208:211], v[98:101]
	v_mfma_f32_16x16x32_bf16 v[90:93], v[168:171], v[208:211], v[90:93]
	v_mfma_f32_16x16x32_bf16 v[82:85], v[160:163], v[216:219], v[82:85]
	v_mfma_f32_16x16x32_bf16 v[74:77], v[168:171], v[216:219], v[74:77]
	v_mfma_f32_16x16x32_bf16 v[118:121], v[172:175], v[188:191], v[118:121]
	v_mfma_f32_16x16x32_bf16 v[110:113], v[180:183], v[188:191], v[110:113]
	v_mfma_f32_16x16x32_bf16 v[102:105], v[172:175], v[196:199], v[102:105]
	v_mfma_f32_16x16x32_bf16 v[94:97], v[180:183], v[196:199], v[94:97]
	v_mfma_f32_16x16x32_bf16 v[86:89], v[172:175], v[204:207], v[86:89]
	v_mfma_f32_16x16x32_bf16 v[78:81], v[180:183], v[204:207], v[78:81]
	v_mfma_f32_16x16x32_bf16 v[62:65], v[172:175], v[212:215], v[62:65]
	v_mfma_f32_16x16x32_bf16 v[58:61], v[180:183], v[212:215], v[58:61]
	v_mfma_f32_16x16x32_bf16 v[118:121], v[176:179], v[192:195], v[118:121]
	v_mfma_f32_16x16x32_bf16 v[110:113], v[184:187], v[192:195], v[110:113]
	v_mfma_f32_16x16x32_bf16 v[102:105], v[176:179], v[200:203], v[102:105]
	v_mfma_f32_16x16x32_bf16 v[94:97], v[184:187], v[200:203], v[94:97]
	v_mfma_f32_16x16x32_bf16 v[86:89], v[176:179], v[208:211], v[86:89]
	v_mfma_f32_16x16x32_bf16 v[78:81], v[184:187], v[208:211], v[78:81]
	v_mfma_f32_16x16x32_bf16 v[62:65], v[176:179], v[216:219], v[62:65]
	v_mfma_f32_16x16x32_bf16 v[58:61], v[184:187], v[216:219], v[58:61]
	s_setprio 0
	s_barrier
; #define PG8_STAGE(bufoff, gbase, voff) do { _Pragma("unroll") for (int _i = 0; _i < 2; ++_i) \
;         __builtin_amdgcn_global_load_lds((const unsigned*)((const char*)(gbase) + (voff)[_i]), (PG8_LAS unsigned*)(lds + (bufoff) + ldsw + _i * 8192), 16, 0, 0); } while (0)
; #define PG8_LDA(dst, b, h) do { _Pragma("unroll") for (int m = 0; m < 4; ++m) _Pragma("unroll") for (int k = 0; k < 2; ++k) dst[m][k] = *(const PG8_LAS bf16x8*)(lds + PG8_SA(b, h) + aoff + m * 2048 + k * 1024); } while (0)
; #define PG8_MMA(ai, bj, At, Bt) do { __builtin_amdgcn_s_setprio(1); _Pragma("unroll") for (int m = 0; m < 4; ++m) _Pragma("unroll") for (int n = 0; n < 2; ++n) _Pragma("unroll") for (int k = 0; k < 2; ++k) \
;         acc[ai][bj][m][n] = __builtin_amdgcn_mfma_f32_16x16x32_bf16(Bt[n][k], At[m][k], acc[ai][bj][m][n], 0, 0, 0); __builtin_amdgcn_s_setprio(0); } while (0)
; #define PG8_WAIT_V(n) asm volatile("s_waitcnt vmcnt(" #n ")" ::: "memory")
; #define PG8_WAIT_L(n) asm volatile("s_waitcnt lgkmcnt(" #n ")" ::: "memory")
; #define PG8_BAR __builtin_amdgcn_s_barrier()
; #define PG8_SCHED __builtin_amdgcn_sched_barrier(0)
; template <class Epi, class Sched, bool ALIGN_EPI = false>
; __device__ __forceinline__ void gemm_phase(PG8_LAS unsigned char* lds, const Gemm g, const Sched& S, const Epi& E) {
;     ...
;         for (int t = 0; t < nt; t += 2) {
;     ...
;             PG8_LDA(At, 1, 1); PG8_STAGE(PG8_SB(1, 0), b3, voffB); PG8_STAGE(PG8_SB(1, 1), b3 + hstep, voffB); PG8_STAGE(PG8_SA(1, 0), a3, w0);
;             PG8_WAIT_V(8); PG8_WAIT_L(0); PG8_BAR; PG8_MMA(1, 0, At, B0); PG8_MMA(1, 1, At, B1); PG8_BAR; PG8_SCHED;
;             if constexpr (Epi::KSCALE) { if (((t + 2) & 7) == 0 && t + 2 < nt) { E.kscale(acc, pf, ((t + 2) >> 3) - 1, wr, fr); PG8_SCHED; } }
;         }
	s_add_i32 s60, s93, s66
	v_lshl_add_u64 v[220:221], v[220:221], 0, s[14:15]
	s_mov_b32 m0, s60
	ds_read_b128 v[188:191], v159 offset:49152
	ds_read_b128 v[192:195], v159 offset:50176
	ds_read_b128 v[196:199], v159 offset:51200
	ds_read_b128 v[200:203], v159 offset:52224
	ds_read_b128 v[204:207], v159 offset:53248
	ds_read_b128 v[208:211], v159 offset:54272
	ds_read_b128 v[212:215], v159 offset:55296
	ds_read_b128 v[216:219], v159 offset:56320
	global_load_lds_dwordx4 v[220:221], off
	s_add_i32 m0, s60, 0x2000
	s_add_u32 s58, s58, 0x20080
	v_lshl_add_u64 v[220:221], v[222:223], 0, s[14:15]
	s_addc_u32 s59, s59, 0
	s_add_i32 s60, s94, s66
	global_load_lds_dwordx4 v[220:221], off
	v_lshl_add_u64 v[220:221], s[58:59], 0, v[134:135]
	s_mov_b32 m0, s60
	s_nop 0
	global_load_lds_dwordx4 v[220:221], off
	v_lshl_add_u64 v[220:221], s[58:59], 0, v[138:139]
	s_add_i32 m0, s60, 0x2000
	s_nop 0
	global_load_lds_dwordx4 v[220:221], off
	v_lshl_add_u64 v[220:221], v[224:225], 0, s[14:15]
	s_mov_b32 m0, s74
	s_nop 0
	global_load_lds_dwordx4 v[220:221], off
	v_lshl_add_u64 v[220:221], v[226:227], 0, s[14:15]
	s_mov_b32 m0, s75
	s_nop 0
	global_load_lds_dwordx4 v[220:221], off
	s_waitcnt vmcnt(8)
	s_waitcnt lgkmcnt(0)
	s_barrier
	s_setprio 1
	v_mfma_f32_16x16x32_bf16 v[54:57], v[144:147], v[188:191], v[54:57]
	v_mfma_f32_16x16x32_bf16 v[42:45], v[164:167], v[188:191], v[42:45]
	v_mfma_f32_16x16x32_bf16 v[30:33], v[144:147], v[196:199], v[30:33]
	v_mfma_f32_16x16x32_bf16 v[26:29], v[164:167], v[196:199], v[26:29]
	v_mfma_f32_16x16x32_bf16 v[14:17], v[144:147], v[204:207], v[14:17]
	v_mfma_f32_16x16x32_bf16 v[10:13], v[164:167], v[204:207], v[10:13]
	v_mfma_f32_16x16x32_bf16 v[6:9], v[144:147], v[212:215], v[6:9]
	v_mfma_f32_16x16x32_bf16 v[2:5], v[164:167], v[212:215], v[2:5]
	v_mfma_f32_16x16x32_bf16 v[54:57], v[160:163], v[192:195], v[54:57]
	v_mfma_f32_16x16x32_bf16 v[42:45], v[168:171], v[192:195], v[42:45]
	v_mfma_f32_16x16x32_bf16 v[30:33], v[160:163], v[200:203], v[30:33]
	v_mfma_f32_16x16x32_bf16 v[26:29], v[168:171], v[200:203], v[26:29]
	v_mfma_f32_16x16x32_bf16 v[14:17], v[160:163], v[208:211], v[14:17]
	v_mfma_f32_16x16x32_bf16 v[10:13], v[168:171], v[208:211], v[10:13]
	v_mfma_f32_16x16x32_bf16 v[6:9], v[160:163], v[216:219], v[6:9]
	v_mfma_f32_16x16x32_bf16 v[2:5], v[168:171], v[216:219], v[2:5]
	v_mfma_f32_16x16x32_bf16 v[70:73], v[172:175], v[188:191], v[70:73]
	v_mfma_f32_16x16x32_bf16 v[66:69], v[180:183], v[188:191], v[66:69]
	v_mfma_f32_16x16x32_bf16 v[50:53], v[172:175], v[196:199], v[50:53]
	v_mfma_f32_16x16x32_bf16 v[46:49], v[180:183], v[196:199], v[46:49]
	v_mfma_f32_16x16x32_bf16 v[38:41], v[172:175], v[204:207], v[38:41]
	v_mfma_f32_16x16x32_bf16 v[34:37], v[180:183], v[204:207], v[34:37]
	v_mfma_f32_16x16x32_bf16 v[22:25], v[172:175], v[212:215], v[22:25]
	v_mfma_f32_16x16x32_bf16 v[18:21], v[180:183], v[212:215], v[18:21]
	v_mfma_f32_16x16x32_bf16 v[70:73], v[176:179], v[192:195], v[70:73]
	v_mfma_f32_16x16x32_bf16 v[66:69], v[184:187], v[192:195], v[66:69]
	v_mfma_f32_16x16x32_bf16 v[50:53], v[176:179], v[200:203], v[50:53]
	v_mfma_f32_16x16x32_bf16 v[46:49], v[184:187], v[200:203], v[46:49]
	v_mfma_f32_16x16x32_bf16 v[38:41], v[176:179], v[208:211], v[38:41]
	v_mfma_f32_16x16x32_bf16 v[34:37], v[184:187], v[208:211], v[34:37]
	v_mfma_f32_16x16x32_bf16 v[22:25], v[176:179], v[216:219], v[22:25]
	v_mfma_f32_16x16x32_bf16 v[18:21], v[184:187], v[216:219], v[18:21]
	s_setprio 0
	s_barrier
	s_add_i32 s92, s92, 2
	s_add_u32 s90, s90, 0x100
	s_addc_u32 s91, s91, 0
	s_add_u32 s56, s56, 0x100
	s_addc_u32 s57, s57, 0
	s_cmp_gt_u32 s92, 5
	s_cbranch_scc0 .LBB0_908
	s_and_b64 vcc, exec, s[16:17]
	s_cbranch_vccz .LBB0_911
	s_barrier

; #define PG8_STAGE(bufoff, gbase, voff) do { _Pragma("unroll") for (int _i = 0; _i < 2; ++_i) \
;         __builtin_amdgcn_global_load_lds((const unsigned*)((const char*)(gbase) + (voff)[_i]), (PG8_LAS unsigned*)(lds + (bufoff) + ldsw + _i * 8192), 16, 0, 0); } while (0)
; #define PG8_LDA(dst, b, h) do { _Pragma("unroll") for (int m = 0; m < 4; ++m) _Pragma("unroll") for (int k = 0; k < 2; ++k) dst[m][k] = *(const PG8_LAS bf16x8*)(lds + PG8_SA(b, h) + aoff + m * 2048 + k * 1024); } while (0)
; #define PG8_LDB(dst, b, h) do { _Pragma("unroll") for (int n = 0; n < 2; ++n) _Pragma("unroll") for (int k = 0; k < 2; ++k) dst[n][k] = *(const PG8_LAS bf16x8*)(lds + PG8_SB(b, h) + boff + n * 2048 + k * 1024); } while (0)
; #define PG8_MMA(ai, bj, At, Bt) do { __builtin_amdgcn_s_setprio(1); _Pragma("unroll") for (int m = 0; m < 4; ++m) _Pragma("unroll") for (int n = 0; n < 2; ++n) _Pragma("unroll") for (int k = 0; k < 2; ++k) \
;         acc[ai][bj][m][n] = __builtin_amdgcn_mfma_f32_16x16x32_bf16(Bt[n][k], At[m][k], acc[ai][bj][m][n], 0, 0, 0); __builtin_amdgcn_s_setprio(0); } while (0)
; #define PG8_WAIT_V(n) asm volatile("s_waitcnt vmcnt(" #n ")" ::: "memory")
; #define PG8_WAIT_L(n) asm volatile("s_waitcnt lgkmcnt(" #n ")" ::: "memory")
; #define PG8_BAR __builtin_amdgcn_s_barrier()
; #define PG8_SCHED __builtin_amdgcn_sched_barrier(0)
; template <class Epi, class Sched, bool ALIGN_EPI = false>
; __device__ __forceinline__ void gemm_phase(PG8_LAS unsigned char* lds, const Gemm g, const Sched& S, const Epi& E) {
;     ...
;             PG8_LDB(B0, 0, 0); PG8_LDB(B1, 0, 1); PG8_SCHED; PG8_LDA(At, 0, 0); PG8_STAGE(PG8_SA(1, 1), a1 + hstepA, vc1);
;             PG8_WAIT_V(8); PG8_WAIT_L(0); PG8_BAR; PG8_MMA(0, 0, At, B0); PG8_MMA(0, 1, At, B1); PG8_BAR; PG8_SCHED;
;             PG8_LDA(At, 0, 1); PG8_STAGE(PG8_SB(0, 0), b2, voffB); PG8_STAGE(PG8_SB(0, 1), b2 + hstep, voffB); PG8_STAGE(PG8_SA(0, 0), a2, w0);
;             PG8_WAIT_V(8); PG8_WAIT_L(0); PG8_BAR; PG8_MMA(1, 0, At, B0); PG8_MMA(1, 1, At, B1); PG8_BAR; PG8_SCHED;
.LBB0_1055:
	ds_read_b128 v[166:169], v155
	ds_read_b128 v[170:173], v155 offset:1024
	ds_read_b128 v[174:177], v155 offset:2048
	ds_read_b128 v[178:181], v155 offset:3072
	ds_read_b128 v[182:185], v157
	ds_read_b128 v[186:189], v157 offset:1024
	ds_read_b128 v[190:193], v157 offset:2048
	ds_read_b128 v[194:197], v157 offset:3072
	s_add_u32 s56, s54, 0xfff80080
	s_addc_u32 s57, s55, -1
	s_cmp_eq_u32 s83, 28
	s_cselect_b32 s59, s15, s57
	s_cselect_b32 s58, s79, s56
	s_cselect_b32 s57, s49, s82
	s_cselect_b32 s56, s80, s81
	v_lshl_add_u64 v[230:231], s[54:55], 0, v[140:141]
	s_add_i32 m0, s63, 0xc000
	ds_read_b128 v[198:201], v159
	ds_read_b128 v[202:205], v159 offset:1024
	ds_read_b128 v[206:209], v159 offset:2048
	ds_read_b128 v[210:213], v159 offset:3072
	ds_read_b128 v[214:217], v159 offset:4096
	ds_read_b128 v[218:221], v159 offset:5120
	ds_read_b128 v[222:225], v159 offset:6144
	ds_read_b128 v[226:229], v159 offset:7168
	global_load_lds_dwordx4 v[230:231], off
	v_lshl_add_u64 v[230:231], s[54:55], 0, v[142:143]
	s_add_i32 m0, s63, 0xe000
	s_nop 0
	global_load_lds_dwordx4 v[230:231], off
	s_waitcnt vmcnt(8)
	s_waitcnt lgkmcnt(0)
	s_barrier
	s_setprio 1
	v_mfma_f32_16x16x32_bf16 v[126:129], v[166:169], v[198:201], v[126:129]
	v_mfma_f32_16x16x32_bf16 v[122:125], v[174:177], v[198:201], v[122:125]
	v_mfma_f32_16x16x32_bf16 v[114:117], v[166:169], v[206:209], v[114:117]
	v_mfma_f32_16x16x32_bf16 v[106:109], v[174:177], v[206:209], v[106:109]
	v_mfma_f32_16x16x32_bf16 v[98:101], v[166:169], v[214:217], v[98:101]
	v_mfma_f32_16x16x32_bf16 v[90:93], v[174:177], v[214:217], v[90:93]
	v_mfma_f32_16x16x32_bf16 v[82:85], v[166:169], v[222:225], v[82:85]
	v_mfma_f32_16x16x32_bf16 v[74:77], v[174:177], v[222:225], v[74:77]
	v_mfma_f32_16x16x32_bf16 v[126:129], v[170:173], v[202:205], v[126:129]
	v_mfma_f32_16x16x32_bf16 v[122:125], v[178:181], v[202:205], v[122:125]
	v_mfma_f32_16x16x32_bf16 v[114:117], v[170:173], v[210:213], v[114:117]
	v_mfma_f32_16x16x32_bf16 v[106:109], v[178:181], v[210:213], v[106:109]
	v_mfma_f32_16x16x32_bf16 v[98:101], v[170:173], v[218:221], v[98:101]
	v_mfma_f32_16x16x32_bf16 v[90:93], v[178:181], v[218:221], v[90:93]
	v_mfma_f32_16x16x32_bf16 v[82:85], v[170:173], v[226:229], v[82:85]
	v_mfma_f32_16x16x32_bf16 v[74:77], v[178:181], v[226:229], v[74:77]
	v_mfma_f32_16x16x32_bf16 v[118:121], v[182:185], v[198:201], v[118:121]
	v_mfma_f32_16x16x32_bf16 v[110:113], v[190:193], v[198:201], v[110:113]
	v_mfma_f32_16x16x32_bf16 v[102:105], v[182:185], v[206:209], v[102:105]
	v_mfma_f32_16x16x32_bf16 v[94:97], v[190:193], v[206:209], v[94:97]
	v_mfma_f32_16x16x32_bf16 v[86:89], v[182:185], v[214:217], v[86:89]
	v_mfma_f32_16x16x32_bf16 v[78:81], v[190:193], v[214:217], v[78:81]
	v_mfma_f32_16x16x32_bf16 v[62:65], v[182:185], v[222:225], v[62:65]
	v_mfma_f32_16x16x32_bf16 v[58:61], v[190:193], v[222:225], v[58:61]
	v_mfma_f32_16x16x32_bf16 v[118:121], v[186:189], v[202:205], v[118:121]
	v_mfma_f32_16x16x32_bf16 v[110:113], v[194:197], v[202:205], v[110:113]
	v_mfma_f32_16x16x32_bf16 v[102:105], v[186:189], v[210:213], v[102:105]
	v_mfma_f32_16x16x32_bf16 v[94:97], v[194:197], v[210:213], v[94:97]
	v_mfma_f32_16x16x32_bf16 v[86:89], v[186:189], v[218:221], v[86:89]
	v_mfma_f32_16x16x32_bf16 v[78:81], v[194:197], v[218:221], v[78:81]
	v_mfma_f32_16x16x32_bf16 v[62:65], v[186:189], v[226:229], v[62:65]
	v_mfma_f32_16x16x32_bf16 v[58:61], v[194:197], v[226:229], v[58:61]
	s_setprio 0
	s_barrier
	s_add_i32 s84, s73, s61
	v_lshl_add_u64 v[230:231], s[56:57], 0, v[132:133]
	s_mov_b32 m0, s84
	ds_read_b128 v[198:201], v159 offset:16384
	ds_read_b128 v[202:205], v159 offset:17408
	ds_read_b128 v[206:209], v159 offset:18432
	ds_read_b128 v[210:213], v159 offset:19456
	ds_read_b128 v[214:217], v159 offset:20480
	ds_read_b128 v[218:221], v159 offset:21504
	ds_read_b128 v[222:225], v159 offset:22528
	ds_read_b128 v[226:229], v159 offset:23552
	global_load_lds_dwordx4 v[230:231], off
	s_add_i32 m0, s84, 0x2000
	s_add_u32 s84, s56, 0x80000
	v_lshl_add_u64 v[232:233], s[56:57], 0, v[136:137]
	s_addc_u32 s85, s57, 0
	s_add_i32 s86, s74, s61
	global_load_lds_dwordx4 v[232:233], off
	v_lshl_add_u64 v[234:235], s[84:85], 0, v[132:133]
	s_mov_b32 m0, s86
	v_lshl_add_u64 v[236:237], s[58:59], 0, v[134:135]
	global_load_lds_dwordx4 v[234:235], off
	v_lshl_add_u64 v[234:235], s[84:85], 0, v[136:137]
	s_add_i32 m0, s86, 0x2000
	s_nop 0
	global_load_lds_dwordx4 v[234:235], off
	v_lshl_add_u64 v[234:235], s[58:59], 0, v[130:131]
	s_mov_b32 m0, s63
	s_nop 0
	global_load_lds_dwordx4 v[234:235], off
	s_mov_b32 m0, s64
	s_nop 0
	global_load_lds_dwordx4 v[236:237], off
	s_waitcnt vmcnt(8)
	s_waitcnt lgkmcnt(0)
	s_barrier
; #define PG8_STAGE(bufoff, gbase, voff) do { _Pragma("unroll") for (int _i = 0; _i < 2; ++_i) \
;         __builtin_amdgcn_global_load_lds((const unsigned*)((const char*)(gbase) + (voff)[_i]), (PG8_LAS unsigned*)(lds + (bufoff) + ldsw + _i * 8192), 16, 0, 0); } while (0)
; #define PG8_LDA(dst, b, h) do { _Pragma("unroll") for (int m = 0; m < 4; ++m) _Pragma("unroll") for (int k = 0; k < 2; ++k) dst[m][k] = *(const PG8_LAS bf16x8*)(lds + PG8_SA(b, h) + aoff + m * 2048 + k * 1024); } while (0)
; #define PG8_LDB(dst, b, h) do { _Pragma("unroll") for (int n = 0; n < 2; ++n) _Pragma("unroll") for (int k = 0; k < 2; ++k) dst[n][k] = *(const PG8_LAS bf16x8*)(lds + PG8_SB(b, h) + boff + n * 2048 + k * 1024); } while (0)
; #define PG8_MMA(ai, bj, At, Bt) do { __builtin_amdgcn_s_setprio(1); _Pragma("unroll") for (int m = 0; m < 4; ++m) _Pragma("unroll") for (int n = 0; n < 2; ++n) _Pragma("unroll") for (int k = 0; k < 2; ++k) \
;         acc[ai][bj][m][n] = __builtin_amdgcn_mfma_f32_16x16x32_bf16(Bt[n][k], At[m][k], acc[ai][bj][m][n], 0, 0, 0); __builtin_amdgcn_s_setprio(0); } while (0)
; #define PG8_WAIT_V(n) asm volatile("s_waitcnt vmcnt(" #n ")" ::: "memory")
; #define PG8_WAIT_L(n) asm volatile("s_waitcnt lgkmcnt(" #n ")" ::: "memory")
; #define PG8_BAR __builtin_amdgcn_s_barrier()
; #define PG8_SCHED __builtin_amdgcn_sched_barrier(0)
; template <class Epi, class Sched, bool ALIGN_EPI = false>
; __device__ __forceinline__ void gemm_phase(PG8_LAS unsigned char* lds, const Gemm g, const Sched& S, const Epi& E) {
;     ...
;             PG8_WAIT_V(8); PG8_WAIT_L(0); PG8_BAR; PG8_MMA(1, 0, At, B0); PG8_MMA(1, 1, At, B1); PG8_BAR; PG8_SCHED;
;             PG8_LDB(B0, 1, 0); PG8_LDB(B1, 1, 1); PG8_SCHED; PG8_LDA(At, 1, 0); PG8_STAGE(PG8_SA(0, 1), a2 + hstepA, w1);
;             PG8_WAIT_V(8); PG8_WAIT_L(0); PG8_BAR; PG8_MMA(0, 0, At, B0); PG8_MMA(0, 1, At, B1); PG8_BAR; PG8_SCHED;
	s_setprio 1
	v_mfma_f32_16x16x32_bf16 v[54:57], v[166:169], v[198:201], v[54:57]
	v_mfma_f32_16x16x32_bf16 v[42:45], v[174:177], v[198:201], v[42:45]
	v_mfma_f32_16x16x32_bf16 v[30:33], v[166:169], v[206:209], v[30:33]
	v_mfma_f32_16x16x32_bf16 v[26:29], v[174:177], v[206:209], v[26:29]
	v_mfma_f32_16x16x32_bf16 v[14:17], v[166:169], v[214:217], v[14:17]
	v_mfma_f32_16x16x32_bf16 v[10:13], v[174:177], v[214:217], v[10:13]
	v_mfma_f32_16x16x32_bf16 v[6:9], v[166:169], v[222:225], v[6:9]
	v_mfma_f32_16x16x32_bf16 v[2:5], v[174:177], v[222:225], v[2:5]
	v_mfma_f32_16x16x32_bf16 v[54:57], v[170:173], v[202:205], v[54:57]
	v_mfma_f32_16x16x32_bf16 v[42:45], v[178:181], v[202:205], v[42:45]
	v_mfma_f32_16x16x32_bf16 v[30:33], v[170:173], v[210:213], v[30:33]
	v_mfma_f32_16x16x32_bf16 v[26:29], v[178:181], v[210:213], v[26:29]
	v_mfma_f32_16x16x32_bf16 v[14:17], v[170:173], v[218:221], v[14:17]
	v_mfma_f32_16x16x32_bf16 v[10:13], v[178:181], v[218:221], v[10:13]
	v_mfma_f32_16x16x32_bf16 v[6:9], v[170:173], v[226:229], v[6:9]
	v_mfma_f32_16x16x32_bf16 v[2:5], v[178:181], v[226:229], v[2:5]
	v_mfma_f32_16x16x32_bf16 v[66:69], v[182:185], v[198:201], v[66:69]
	v_mfma_f32_16x16x32_bf16 v[70:73], v[190:193], v[198:201], v[70:73]
	v_mfma_f32_16x16x32_bf16 v[46:49], v[182:185], v[206:209], v[46:49]
	v_mfma_f32_16x16x32_bf16 v[50:53], v[190:193], v[206:209], v[50:53]
	v_mfma_f32_16x16x32_bf16 v[34:37], v[182:185], v[214:217], v[34:37]
	v_mfma_f32_16x16x32_bf16 v[38:41], v[190:193], v[214:217], v[38:41]
	v_mfma_f32_16x16x32_bf16 v[18:21], v[182:185], v[222:225], v[18:21]
	v_mfma_f32_16x16x32_bf16 v[22:25], v[190:193], v[222:225], v[22:25]
	v_mfma_f32_16x16x32_bf16 v[66:69], v[186:189], v[202:205], v[66:69]
	v_mfma_f32_16x16x32_bf16 v[70:73], v[194:197], v[202:205], v[70:73]
	v_mfma_f32_16x16x32_bf16 v[46:49], v[186:189], v[210:213], v[46:49]
	v_mfma_f32_16x16x32_bf16 v[50:53], v[194:197], v[210:213], v[50:53]
	v_mfma_f32_16x16x32_bf16 v[34:37], v[186:189], v[218:221], v[34:37]
	v_mfma_f32_16x16x32_bf16 v[38:41], v[194:197], v[218:221], v[38:41]
	v_mfma_f32_16x16x32_bf16 v[18:21], v[186:189], v[226:229], v[18:21]
	v_mfma_f32_16x16x32_bf16 v[22:25], v[194:197], v[226:229], v[22:25]
	s_setprio 0
	s_barrier
	s_add_i32 s84, 0, 0x18000
	v_add_u32_e32 v138, s84, v149
	s_add_i32 s85, 0, 0x1c000
	ds_read_b128 v[166:169], v138
	ds_read_b128 v[170:173], v138 offset:1024
	ds_read_b128 v[174:177], v138 offset:2048
	ds_read_b128 v[178:181], v138 offset:3072
	v_add_u32_e32 v138, s85, v149
	ds_read_b128 v[182:185], v138
	ds_read_b128 v[186:189], v138 offset:1024
	ds_read_b128 v[190:193], v138 offset:2048
	ds_read_b128 v[194:197], v138 offset:3072
	s_add_u32 s58, s58, 0x80000
	s_addc_u32 s59, s59, 0
	s_mov_b32 m0, s65
	v_lshl_add_u64 v[238:239], s[58:59], 0, v[130:131]
	ds_read_b128 v[198:201], v159 offset:32768
	ds_read_b128 v[202:205], v159 offset:33792
	ds_read_b128 v[206:209], v159 offset:34816
	ds_read_b128 v[210:213], v159 offset:35840
	ds_read_b128 v[214:217], v159 offset:36864
	ds_read_b128 v[218:221], v159 offset:37888
	ds_read_b128 v[222:225], v159 offset:38912
	ds_read_b128 v[226:229], v159 offset:39936
	global_load_lds_dwordx4 v[238:239], off
	v_lshl_add_u64 v[238:239], s[58:59], 0, v[134:135]
	s_mov_b32 m0, s66
	s_nop 0
	global_load_lds_dwordx4 v[238:239], off
	s_waitcnt vmcnt(8)
	s_waitcnt lgkmcnt(0)
	s_barrier
	s_setprio 1
	v_mfma_f32_16x16x32_bf16 v[126:129], v[166:169], v[198:201], v[126:129]
	v_mfma_f32_16x16x32_bf16 v[122:125], v[174:177], v[198:201], v[122:125]
	v_mfma_f32_16x16x32_bf16 v[114:117], v[166:169], v[206:209], v[114:117]
	v_mfma_f32_16x16x32_bf16 v[106:109], v[174:177], v[206:209], v[106:109]
	v_mfma_f32_16x16x32_bf16 v[98:101], v[166:169], v[214:217], v[98:101]
	v_mfma_f32_16x16x32_bf16 v[90:93], v[174:177], v[214:217], v[90:93]
	v_mfma_f32_16x16x32_bf16 v[82:85], v[166:169], v[222:225], v[82:85]
	v_mfma_f32_16x16x32_bf16 v[74:77], v[174:177], v[222:225], v[74:77]
	v_mfma_f32_16x16x32_bf16 v[126:129], v[170:173], v[202:205], v[126:129]
	v_mfma_f32_16x16x32_bf16 v[122:125], v[178:181], v[202:205], v[122:125]
	v_mfma_f32_16x16x32_bf16 v[114:117], v[170:173], v[210:213], v[114:117]
	v_mfma_f32_16x16x32_bf16 v[106:109], v[178:181], v[210:213], v[106:109]
	v_mfma_f32_16x16x32_bf16 v[98:101], v[170:173], v[218:221], v[98:101]
	v_mfma_f32_16x16x32_bf16 v[90:93], v[178:181], v[218:221], v[90:93]
	v_mfma_f32_16x16x32_bf16 v[82:85], v[170:173], v[226:229], v[82:85]
	v_mfma_f32_16x16x32_bf16 v[74:77], v[178:181], v[226:229], v[74:77]
	v_mfma_f32_16x16x32_bf16 v[118:121], v[182:185], v[198:201], v[118:121]
	v_mfma_f32_16x16x32_bf16 v[110:113], v[190:193], v[198:201], v[110:113]
	v_mfma_f32_16x16x32_bf16 v[102:105], v[182:185], v[206:209], v[102:105]
	v_mfma_f32_16x16x32_bf16 v[94:97], v[190:193], v[206:209], v[94:97]
	v_mfma_f32_16x16x32_bf16 v[86:89], v[182:185], v[214:217], v[86:89]
	v_mfma_f32_16x16x32_bf16 v[78:81], v[190:193], v[214:217], v[78:81]
	v_mfma_f32_16x16x32_bf16 v[62:65], v[182:185], v[222:225], v[62:65]
	v_mfma_f32_16x16x32_bf16 v[58:61], v[190:193], v[222:225], v[58:61]
	v_mfma_f32_16x16x32_bf16 v[118:121], v[186:189], v[202:205], v[118:121]
	v_mfma_f32_16x16x32_bf16 v[110:113], v[194:197], v[202:205], v[110:113]
	v_mfma_f32_16x16x32_bf16 v[102:105], v[186:189], v[210:213], v[102:105]
	v_mfma_f32_16x16x32_bf16 v[94:97], v[194:197], v[210:213], v[94:97]
	v_mfma_f32_16x16x32_bf16 v[86:89], v[186:189], v[218:221], v[86:89]
	v_mfma_f32_16x16x32_bf16 v[78:81], v[194:197], v[218:221], v[78:81]
	v_mfma_f32_16x16x32_bf16 v[62:65], v[186:189], v[226:229], v[62:65]
	v_mfma_f32_16x16x32_bf16 v[58:61], v[194:197], v[226:229], v[58:61]
	s_setprio 0
	s_barrier
; #define PG8_STAGE(bufoff, gbase, voff) do { _Pragma("unroll") for (int _i = 0; _i < 2; ++_i) \
;         __builtin_amdgcn_global_load_lds((const unsigned*)((const char*)(gbase) + (voff)[_i]), (PG8_LAS unsigned*)(lds + (bufoff) + ldsw + _i * 8192), 16, 0, 0); } while (0)
; #define PG8_LDA(dst, b, h) do { _Pragma("unroll") for (int m = 0; m < 4; ++m) _Pragma("unroll") for (int k = 0; k < 2; ++k) dst[m][k] = *(const PG8_LAS bf16x8*)(lds + PG8_SA(b, h) + aoff + m * 2048 + k * 1024); } while (0)
; #define PG8_MMA(ai, bj, At, Bt) do { __builtin_amdgcn_s_setprio(1); _Pragma("unroll") for (int m = 0; m < 4; ++m) _Pragma("unroll") for (int n = 0; n < 2; ++n) _Pragma("unroll") for (int k = 0; k < 2; ++k) \
;         acc[ai][bj][m][n] = __builtin_amdgcn_mfma_f32_16x16x32_bf16(Bt[n][k], At[m][k], acc[ai][bj][m][n], 0, 0, 0); __builtin_amdgcn_s_setprio(0); } while (0)
; #define PG8_WAIT_V(n) asm volatile("s_waitcnt vmcnt(" #n ")" ::: "memory")
; #define PG8_WAIT_L(n) asm volatile("s_waitcnt lgkmcnt(" #n ")" ::: "memory")
; #define PG8_BAR __builtin_amdgcn_s_barrier()
; #define PG8_SCHED __builtin_amdgcn_sched_barrier(0)
; template <class Epi, class Sched, bool ALIGN_EPI = false>
; __device__ __forceinline__ void gemm_phase(PG8_LAS unsigned char* lds, const Gemm g, const Sched& S, const Epi& E) {
;     ...
;         for (int t = 0; t < nt; t += 2) {
;     ...
;             PG8_LDA(At, 1, 1); PG8_STAGE(PG8_SB(1, 0), b3, voffB); PG8_STAGE(PG8_SB(1, 1), b3 + hstep, voffB); PG8_STAGE(PG8_SA(1, 0), a3, w0);
;             PG8_WAIT_V(8); PG8_WAIT_L(0); PG8_BAR; PG8_MMA(1, 0, At, B0); PG8_MMA(1, 1, At, B1); PG8_BAR; PG8_SCHED;
;             if constexpr (Epi::KSCALE) { if (((t + 2) & 7) == 0 && t + 2 < nt) { E.kscale(acc, pf, ((t + 2) >> 3) - 1, wr, fr); PG8_SCHED; } }
;         }
	s_add_i32 s58, s84, s61
	v_lshl_add_u64 v[230:231], v[230:231], 0, s[26:27]
	s_mov_b32 m0, s58
	ds_read_b128 v[198:201], v159 offset:49152
	ds_read_b128 v[202:205], v159 offset:50176
	ds_read_b128 v[206:209], v159 offset:51200
	ds_read_b128 v[210:213], v159 offset:52224
	ds_read_b128 v[214:217], v159 offset:53248
	ds_read_b128 v[218:221], v159 offset:54272
	ds_read_b128 v[222:225], v159 offset:55296
	ds_read_b128 v[226:229], v159 offset:56320
	global_load_lds_dwordx4 v[230:231], off
	s_add_i32 m0, s58, 0x2000
	s_add_u32 s56, s56, 0x80080
	v_lshl_add_u64 v[230:231], v[232:233], 0, s[26:27]
	s_addc_u32 s57, s57, 0
	s_add_i32 s58, s85, s61
	global_load_lds_dwordx4 v[230:231], off
	v_lshl_add_u64 v[230:231], s[56:57], 0, v[132:133]
	s_mov_b32 m0, s58
	s_nop 0
	global_load_lds_dwordx4 v[230:231], off
	v_lshl_add_u64 v[230:231], s[56:57], 0, v[136:137]
	s_add_i32 m0, s58, 0x2000
	s_nop 0
	global_load_lds_dwordx4 v[230:231], off
	v_lshl_add_u64 v[230:231], v[234:235], 0, s[26:27]
	s_mov_b32 m0, s69
	s_nop 0
	global_load_lds_dwordx4 v[230:231], off
	v_lshl_add_u64 v[230:231], v[236:237], 0, s[26:27]
	s_mov_b32 m0, s72
	s_nop 0
	global_load_lds_dwordx4 v[230:231], off
	s_waitcnt vmcnt(8)
	s_waitcnt lgkmcnt(0)
	s_barrier
	s_setprio 1
	v_mfma_f32_16x16x32_bf16 v[54:57], v[166:169], v[198:201], v[54:57]
	v_mfma_f32_16x16x32_bf16 v[42:45], v[174:177], v[198:201], v[42:45]
	v_mfma_f32_16x16x32_bf16 v[30:33], v[166:169], v[206:209], v[30:33]
	v_mfma_f32_16x16x32_bf16 v[26:29], v[174:177], v[206:209], v[26:29]
	v_mfma_f32_16x16x32_bf16 v[14:17], v[166:169], v[214:217], v[14:17]
	v_mfma_f32_16x16x32_bf16 v[10:13], v[174:177], v[214:217], v[10:13]
	v_mfma_f32_16x16x32_bf16 v[6:9], v[166:169], v[222:225], v[6:9]
	v_mfma_f32_16x16x32_bf16 v[2:5], v[174:177], v[222:225], v[2:5]
	v_mfma_f32_16x16x32_bf16 v[54:57], v[170:173], v[202:205], v[54:57]
	v_mfma_f32_16x16x32_bf16 v[42:45], v[178:181], v[202:205], v[42:45]
	v_mfma_f32_16x16x32_bf16 v[30:33], v[170:173], v[210:213], v[30:33]
	v_mfma_f32_16x16x32_bf16 v[26:29], v[178:181], v[210:213], v[26:29]
	v_mfma_f32_16x16x32_bf16 v[14:17], v[170:173], v[218:221], v[14:17]
	v_mfma_f32_16x16x32_bf16 v[10:13], v[178:181], v[218:221], v[10:13]
	v_mfma_f32_16x16x32_bf16 v[6:9], v[170:173], v[226:229], v[6:9]
	v_mfma_f32_16x16x32_bf16 v[2:5], v[178:181], v[226:229], v[2:5]
	v_mfma_f32_16x16x32_bf16 v[66:69], v[182:185], v[198:201], v[66:69]
	v_mfma_f32_16x16x32_bf16 v[70:73], v[190:193], v[198:201], v[70:73]
	v_mfma_f32_16x16x32_bf16 v[46:49], v[182:185], v[206:209], v[46:49]
	v_mfma_f32_16x16x32_bf16 v[50:53], v[190:193], v[206:209], v[50:53]
	v_mfma_f32_16x16x32_bf16 v[34:37], v[182:185], v[214:217], v[34:37]
	v_mfma_f32_16x16x32_bf16 v[38:41], v[190:193], v[214:217], v[38:41]
	v_mfma_f32_16x16x32_bf16 v[18:21], v[182:185], v[222:225], v[18:21]
	v_mfma_f32_16x16x32_bf16 v[22:25], v[190:193], v[222:225], v[22:25]
	v_mfma_f32_16x16x32_bf16 v[66:69], v[186:189], v[202:205], v[66:69]
	v_mfma_f32_16x16x32_bf16 v[70:73], v[194:197], v[202:205], v[70:73]
	v_mfma_f32_16x16x32_bf16 v[46:49], v[186:189], v[210:213], v[46:49]
	v_mfma_f32_16x16x32_bf16 v[50:53], v[194:197], v[210:213], v[50:53]
	v_mfma_f32_16x16x32_bf16 v[34:37], v[186:189], v[218:221], v[34:37]
	v_mfma_f32_16x16x32_bf16 v[38:41], v[194:197], v[218:221], v[38:41]
	v_mfma_f32_16x16x32_bf16 v[18:21], v[186:189], v[226:229], v[18:21]
	v_mfma_f32_16x16x32_bf16 v[22:25], v[194:197], v[226:229], v[22:25]
	s_setprio 0
	s_barrier
	s_add_i32 s83, s83, 2
	s_add_u32 s54, s54, 0x100
	s_addc_u32 s55, s55, 0
	s_add_u32 s81, s81, 0x100
	s_addc_u32 s82, s82, 0
	s_cmp_gt_u32 s83, 29
	s_cbranch_scc0 .LBB0_1055
	s_and_b64 vcc, exec, s[40:41]
	s_cbranch_vccz .LBB0_1058
	s_barrier

; #define PG8_STAGE(bufoff, gbase, voff) do { _Pragma("unroll") for (int _i = 0; _i < 2; ++_i) \
;         __builtin_amdgcn_global_load_lds((const unsigned*)((const char*)(gbase) + (voff)[_i]), (PG8_LAS unsigned*)(lds + (bufoff) + ldsw + _i * 8192), 16, 0, 0); } while (0)
; #define PG8_LDA(dst, b, h) do { _Pragma("unroll") for (int m = 0; m < 4; ++m) _Pragma("unroll") for (int k = 0; k < 2; ++k) dst[m][k] = *(const PG8_LAS bf16x8*)(lds + PG8_SA(b, h) + aoff + m * 2048 + k * 1024); } while (0)
; #define PG8_LDB(dst, b, h) do { _Pragma("unroll") for (int n = 0; n < 2; ++n) _Pragma("unroll") for (int k = 0; k < 2; ++k) dst[n][k] = *(const PG8_LAS bf16x8*)(lds + PG8_SB(b, h) + boff + n * 2048 + k * 1024); } while (0)
; #define PG8_MMA(ai, bj, At, Bt) do { __builtin_amdgcn_s_setprio(1); _Pragma("unroll") for (int m = 0; m < 4; ++m) _Pragma("unroll") for (int n = 0; n < 2; ++n) _Pragma("unroll") for (int k = 0; k < 2; ++k) \
;         acc[ai][bj][m][n] = __builtin_amdgcn_mfma_f32_16x16x32_bf16(Bt[n][k], At[m][k], acc[ai][bj][m][n], 0, 0, 0); __builtin_amdgcn_s_setprio(0); } while (0)
; #define PG8_WAIT_V(n) asm volatile("s_waitcnt vmcnt(" #n ")" ::: "memory")
; #define PG8_WAIT_L(n) asm volatile("s_waitcnt lgkmcnt(" #n ")" ::: "memory")
; #define PG8_BAR __builtin_amdgcn_s_barrier()
; #define PG8_SCHED __builtin_amdgcn_sched_barrier(0)
; template <class Epi, class Sched, bool ALIGN_EPI = false>
; __device__ __forceinline__ void gemm_phase(PG8_LAS unsigned char* lds, const Gemm g, const Sched& S, const Epi& E) {
;     ...
;             PG8_LDB(B0, 0, 0); PG8_LDB(B1, 0, 1); PG8_SCHED; PG8_LDA(At, 0, 0); PG8_STAGE(PG8_SA(1, 1), a1 + hstepA, vc1);
;             PG8_WAIT_V(8); PG8_WAIT_L(0); PG8_BAR; PG8_MMA(0, 0, At, B0); PG8_MMA(0, 1, At, B1); PG8_BAR; PG8_SCHED;
;             PG8_LDA(At, 0, 1); PG8_STAGE(PG8_SB(0, 0), b2, voffB); PG8_STAGE(PG8_SB(0, 1), b2 + hstep, voffB); PG8_STAGE(PG8_SA(0, 0), a2, w0);
;             PG8_WAIT_V(8); PG8_WAIT_L(0); PG8_BAR; PG8_MMA(1, 0, At, B0); PG8_MMA(1, 1, At, B1); PG8_BAR; PG8_SCHED;
.LBB0_1198:
	ds_read_b128 v[130:133], v168
	ds_read_b128 v[134:137], v168 offset:1024
	ds_read_b128 v[154:157], v168 offset:2048
	ds_read_b128 v[158:161], v168 offset:3072
	ds_read_b128 v[162:165], v169
	ds_read_b128 v[172:175], v169 offset:1024
	ds_read_b128 v[176:179], v169 offset:2048
	ds_read_b128 v[180:183], v169 offset:3072
	s_add_u32 s54, s52, 0xfff80080
	s_addc_u32 s55, s53, -1
	s_cmp_eq_u32 s78, 28
	s_cselect_b32 s57, s45, s55
	s_cselect_b32 s56, s74, s54
	s_cselect_b32 s55, s43, s77
	s_cselect_b32 s54, s75, s76
	v_lshl_add_u64 v[216:217], s[52:53], 0, v[146:147]
	s_add_i32 m0, s51, 0xc000
	ds_read_b128 v[184:187], v170
	ds_read_b128 v[188:191], v170 offset:1024
	ds_read_b128 v[192:195], v170 offset:2048
	ds_read_b128 v[196:199], v170 offset:3072
	ds_read_b128 v[200:203], v170 offset:4096
	ds_read_b128 v[204:207], v170 offset:5120
	ds_read_b128 v[208:211], v170 offset:6144
	ds_read_b128 v[212:215], v170 offset:7168
	global_load_lds_dwordx4 v[216:217], off
	v_lshl_add_u64 v[216:217], s[52:53], 0, v[148:149]
	s_add_i32 m0, s51, 0xe000
	s_nop 0
	global_load_lds_dwordx4 v[216:217], off
	s_waitcnt vmcnt(8)
	s_waitcnt lgkmcnt(0)
	s_barrier
	s_setprio 1
	v_mfma_f32_16x16x32_bf16 v[126:129], v[130:133], v[184:187], v[126:129]
	v_mfma_f32_16x16x32_bf16 v[122:125], v[154:157], v[184:187], v[122:125]
	v_mfma_f32_16x16x32_bf16 v[118:121], v[130:133], v[192:195], v[118:121]
	v_mfma_f32_16x16x32_bf16 v[114:117], v[154:157], v[192:195], v[114:117]
	v_mfma_f32_16x16x32_bf16 v[94:97], v[130:133], v[200:203], v[94:97]
	v_mfma_f32_16x16x32_bf16 v[90:93], v[154:157], v[200:203], v[90:93]
	v_mfma_f32_16x16x32_bf16 v[78:81], v[130:133], v[208:211], v[78:81]
	v_mfma_f32_16x16x32_bf16 v[74:77], v[154:157], v[208:211], v[74:77]
	v_mfma_f32_16x16x32_bf16 v[126:129], v[134:137], v[188:191], v[126:129]
	v_mfma_f32_16x16x32_bf16 v[122:125], v[158:161], v[188:191], v[122:125]
	v_mfma_f32_16x16x32_bf16 v[118:121], v[134:137], v[196:199], v[118:121]
	v_mfma_f32_16x16x32_bf16 v[114:117], v[158:161], v[196:199], v[114:117]
	v_mfma_f32_16x16x32_bf16 v[94:97], v[134:137], v[204:207], v[94:97]
	v_mfma_f32_16x16x32_bf16 v[90:93], v[158:161], v[204:207], v[90:93]
	v_mfma_f32_16x16x32_bf16 v[78:81], v[134:137], v[212:215], v[78:81]
	v_mfma_f32_16x16x32_bf16 v[74:77], v[158:161], v[212:215], v[74:77]
	v_mfma_f32_16x16x32_bf16 v[110:113], v[162:165], v[184:187], v[110:113]
	v_mfma_f32_16x16x32_bf16 v[106:109], v[176:179], v[184:187], v[106:109]
	v_mfma_f32_16x16x32_bf16 v[102:105], v[162:165], v[192:195], v[102:105]
	v_mfma_f32_16x16x32_bf16 v[98:101], v[176:179], v[192:195], v[98:101]
	v_mfma_f32_16x16x32_bf16 v[86:89], v[162:165], v[200:203], v[86:89]
	v_mfma_f32_16x16x32_bf16 v[82:85], v[176:179], v[200:203], v[82:85]
	v_mfma_f32_16x16x32_bf16 v[70:73], v[162:165], v[208:211], v[70:73]
	v_mfma_f32_16x16x32_bf16 v[66:69], v[176:179], v[208:211], v[66:69]
	v_mfma_f32_16x16x32_bf16 v[110:113], v[172:175], v[188:191], v[110:113]
	v_mfma_f32_16x16x32_bf16 v[106:109], v[180:183], v[188:191], v[106:109]
	v_mfma_f32_16x16x32_bf16 v[102:105], v[172:175], v[196:199], v[102:105]
	v_mfma_f32_16x16x32_bf16 v[98:101], v[180:183], v[196:199], v[98:101]
	v_mfma_f32_16x16x32_bf16 v[86:89], v[172:175], v[204:207], v[86:89]
	v_mfma_f32_16x16x32_bf16 v[82:85], v[180:183], v[204:207], v[82:85]
	v_mfma_f32_16x16x32_bf16 v[70:73], v[172:175], v[212:215], v[70:73]
	v_mfma_f32_16x16x32_bf16 v[66:69], v[180:183], v[212:215], v[66:69]
	s_setprio 0
	s_barrier
	s_add_i32 s79, s69, s61
	v_lshl_add_u64 v[216:217], s[54:55], 0, v[140:141]
	s_mov_b32 m0, s79
	ds_read_b128 v[184:187], v170 offset:16384
	ds_read_b128 v[188:191], v170 offset:17408
	ds_read_b128 v[192:195], v170 offset:18432
	ds_read_b128 v[196:199], v170 offset:19456
	ds_read_b128 v[200:203], v170 offset:20480
	ds_read_b128 v[204:207], v170 offset:21504
	ds_read_b128 v[208:211], v170 offset:22528
	ds_read_b128 v[212:215], v170 offset:23552
	global_load_lds_dwordx4 v[216:217], off
	s_add_i32 m0, s79, 0x2000
	s_add_u32 s80, s54, 0x80000
	v_lshl_add_u64 v[218:219], s[54:55], 0, v[144:145]
	s_addc_u32 s81, s55, 0
	s_add_i32 s79, s72, s61
	global_load_lds_dwordx4 v[218:219], off
	v_lshl_add_u64 v[220:221], s[80:81], 0, v[140:141]
	s_mov_b32 m0, s79
	v_lshl_add_u64 v[222:223], s[56:57], 0, v[142:143]
	global_load_lds_dwordx4 v[220:221], off
	v_lshl_add_u64 v[220:221], s[80:81], 0, v[144:145]
	s_add_i32 m0, s79, 0x2000
	s_nop 0
	global_load_lds_dwordx4 v[220:221], off
	v_lshl_add_u64 v[220:221], s[56:57], 0, v[138:139]
	s_mov_b32 m0, s51
	s_nop 0
	global_load_lds_dwordx4 v[220:221], off
	s_mov_b32 m0, s62
	s_nop 0
	global_load_lds_dwordx4 v[222:223], off
	s_waitcnt vmcnt(8)
	s_waitcnt lgkmcnt(0)
	s_barrier
; #define PG8_STAGE(bufoff, gbase, voff) do { _Pragma("unroll") for (int _i = 0; _i < 2; ++_i) \
;         __builtin_amdgcn_global_load_lds((const unsigned*)((const char*)(gbase) + (voff)[_i]), (PG8_LAS unsigned*)(lds + (bufoff) + ldsw + _i * 8192), 16, 0, 0); } while (0)
; #define PG8_LDA(dst, b, h) do { _Pragma("unroll") for (int m = 0; m < 4; ++m) _Pragma("unroll") for (int k = 0; k < 2; ++k) dst[m][k] = *(const PG8_LAS bf16x8*)(lds + PG8_SA(b, h) + aoff + m * 2048 + k * 1024); } while (0)
; #define PG8_LDB(dst, b, h) do { _Pragma("unroll") for (int n = 0; n < 2; ++n) _Pragma("unroll") for (int k = 0; k < 2; ++k) dst[n][k] = *(const PG8_LAS bf16x8*)(lds + PG8_SB(b, h) + boff + n * 2048 + k * 1024); } while (0)
; #define PG8_MMA(ai, bj, At, Bt) do { __builtin_amdgcn_s_setprio(1); _Pragma("unroll") for (int m = 0; m < 4; ++m) _Pragma("unroll") for (int n = 0; n < 2; ++n) _Pragma("unroll") for (int k = 0; k < 2; ++k) \
;         acc[ai][bj][m][n] = __builtin_amdgcn_mfma_f32_16x16x32_bf16(Bt[n][k], At[m][k], acc[ai][bj][m][n], 0, 0, 0); __builtin_amdgcn_s_setprio(0); } while (0)
; #define PG8_WAIT_V(n) asm volatile("s_waitcnt vmcnt(" #n ")" ::: "memory")
; #define PG8_WAIT_L(n) asm volatile("s_waitcnt lgkmcnt(" #n ")" ::: "memory")
; #define PG8_BAR __builtin_amdgcn_s_barrier()
; #define PG8_SCHED __builtin_amdgcn_sched_barrier(0)
; template <class Epi, class Sched, bool ALIGN_EPI = false>
; __device__ __forceinline__ void gemm_phase(PG8_LAS unsigned char* lds, const Gemm g, const Sched& S, const Epi& E) {
;     ...
;             PG8_WAIT_V(8); PG8_WAIT_L(0); PG8_BAR; PG8_MMA(1, 0, At, B0); PG8_MMA(1, 1, At, B1); PG8_BAR; PG8_SCHED;
;             PG8_LDB(B0, 1, 0); PG8_LDB(B1, 1, 1); PG8_SCHED; PG8_LDA(At, 1, 0); PG8_STAGE(PG8_SA(0, 1), a2 + hstepA, w1);
;             PG8_WAIT_V(8); PG8_WAIT_L(0); PG8_BAR; PG8_MMA(0, 0, At, B0); PG8_MMA(0, 1, At, B1); PG8_BAR; PG8_SCHED;
	s_setprio 1
	v_mfma_f32_16x16x32_bf16 v[54:57], v[130:133], v[184:187], v[54:57]
	v_mfma_f32_16x16x32_bf16 v[50:53], v[154:157], v[184:187], v[50:53]
	v_mfma_f32_16x16x32_bf16 v[38:41], v[130:133], v[192:195], v[38:41]
	v_mfma_f32_16x16x32_bf16 v[34:37], v[154:157], v[192:195], v[34:37]
	v_mfma_f32_16x16x32_bf16 v[22:25], v[130:133], v[200:203], v[22:25]
	v_mfma_f32_16x16x32_bf16 v[18:21], v[154:157], v[200:203], v[18:21]
	v_mfma_f32_16x16x32_bf16 v[6:9], v[130:133], v[208:211], v[6:9]
	v_mfma_f32_16x16x32_bf16 v[2:5], v[154:157], v[208:211], v[2:5]
	v_mfma_f32_16x16x32_bf16 v[54:57], v[134:137], v[188:191], v[54:57]
	v_mfma_f32_16x16x32_bf16 v[50:53], v[158:161], v[188:191], v[50:53]
	v_mfma_f32_16x16x32_bf16 v[38:41], v[134:137], v[196:199], v[38:41]
	v_mfma_f32_16x16x32_bf16 v[34:37], v[158:161], v[196:199], v[34:37]
	v_mfma_f32_16x16x32_bf16 v[22:25], v[134:137], v[204:207], v[22:25]
	v_mfma_f32_16x16x32_bf16 v[18:21], v[158:161], v[204:207], v[18:21]
	v_mfma_f32_16x16x32_bf16 v[6:9], v[134:137], v[212:215], v[6:9]
	v_mfma_f32_16x16x32_bf16 v[2:5], v[158:161], v[212:215], v[2:5]
	v_mfma_f32_16x16x32_bf16 v[62:65], v[162:165], v[184:187], v[62:65]
	v_mfma_f32_16x16x32_bf16 v[58:61], v[176:179], v[184:187], v[58:61]
	v_mfma_f32_16x16x32_bf16 v[46:49], v[162:165], v[192:195], v[46:49]
	v_mfma_f32_16x16x32_bf16 v[42:45], v[176:179], v[192:195], v[42:45]
	v_mfma_f32_16x16x32_bf16 v[30:33], v[162:165], v[200:203], v[30:33]
	v_mfma_f32_16x16x32_bf16 v[26:29], v[176:179], v[200:203], v[26:29]
	v_mfma_f32_16x16x32_bf16 v[14:17], v[162:165], v[208:211], v[14:17]
	v_mfma_f32_16x16x32_bf16 v[10:13], v[176:179], v[208:211], v[10:13]
	v_mfma_f32_16x16x32_bf16 v[62:65], v[172:175], v[188:191], v[62:65]
	v_mfma_f32_16x16x32_bf16 v[58:61], v[180:183], v[188:191], v[58:61]
	v_mfma_f32_16x16x32_bf16 v[46:49], v[172:175], v[196:199], v[46:49]
	v_mfma_f32_16x16x32_bf16 v[42:45], v[180:183], v[196:199], v[42:45]
	v_mfma_f32_16x16x32_bf16 v[30:33], v[172:175], v[204:207], v[30:33]
	v_mfma_f32_16x16x32_bf16 v[26:29], v[180:183], v[204:207], v[26:29]
	v_mfma_f32_16x16x32_bf16 v[14:17], v[172:175], v[212:215], v[14:17]
	v_mfma_f32_16x16x32_bf16 v[10:13], v[180:183], v[212:215], v[10:13]
	s_setprio 0
	s_barrier
	s_add_i32 s79, 0, 0x18000
	s_add_i32 s80, 0, 0x1c000
	v_add_u32_e32 v158, s79, v166
	v_add_u32_e32 v171, s80, v166
	ds_read_b128 v[130:133], v158
	ds_read_b128 v[134:137], v158 offset:1024
	ds_read_b128 v[154:157], v158 offset:2048
	ds_read_b128 v[158:161], v158 offset:3072
	ds_read_b128 v[162:165], v171
	ds_read_b128 v[172:175], v171 offset:1024
	ds_read_b128 v[176:179], v171 offset:2048
	ds_read_b128 v[180:183], v171 offset:3072
	s_add_u32 s56, s56, 0x80000
	s_addc_u32 s57, s57, 0
	s_mov_b32 m0, s63
	v_lshl_add_u64 v[224:225], s[56:57], 0, v[138:139]
	ds_read_b128 v[184:187], v170 offset:32768
	ds_read_b128 v[188:191], v170 offset:33792
	ds_read_b128 v[192:195], v170 offset:34816
	ds_read_b128 v[196:199], v170 offset:35840
	ds_read_b128 v[200:203], v170 offset:36864
	ds_read_b128 v[204:207], v170 offset:37888
	ds_read_b128 v[208:211], v170 offset:38912
	ds_read_b128 v[212:215], v170 offset:39936
	global_load_lds_dwordx4 v[224:225], off
	v_lshl_add_u64 v[224:225], s[56:57], 0, v[142:143]
	s_mov_b32 m0, s64
	s_nop 0
	global_load_lds_dwordx4 v[224:225], off
	s_waitcnt vmcnt(8)
	s_waitcnt lgkmcnt(0)
	s_barrier
	s_setprio 1
	v_mfma_f32_16x16x32_bf16 v[126:129], v[130:133], v[184:187], v[126:129]
	v_mfma_f32_16x16x32_bf16 v[122:125], v[154:157], v[184:187], v[122:125]
	v_mfma_f32_16x16x32_bf16 v[118:121], v[130:133], v[192:195], v[118:121]
	v_mfma_f32_16x16x32_bf16 v[114:117], v[154:157], v[192:195], v[114:117]
	v_mfma_f32_16x16x32_bf16 v[94:97], v[130:133], v[200:203], v[94:97]
	v_mfma_f32_16x16x32_bf16 v[90:93], v[154:157], v[200:203], v[90:93]
	v_mfma_f32_16x16x32_bf16 v[78:81], v[130:133], v[208:211], v[78:81]
	v_mfma_f32_16x16x32_bf16 v[74:77], v[154:157], v[208:211], v[74:77]
	v_mfma_f32_16x16x32_bf16 v[126:129], v[134:137], v[188:191], v[126:129]
	v_mfma_f32_16x16x32_bf16 v[122:125], v[158:161], v[188:191], v[122:125]
	v_mfma_f32_16x16x32_bf16 v[118:121], v[134:137], v[196:199], v[118:121]
	v_mfma_f32_16x16x32_bf16 v[114:117], v[158:161], v[196:199], v[114:117]
	v_mfma_f32_16x16x32_bf16 v[94:97], v[134:137], v[204:207], v[94:97]
	v_mfma_f32_16x16x32_bf16 v[90:93], v[158:161], v[204:207], v[90:93]
	v_mfma_f32_16x16x32_bf16 v[78:81], v[134:137], v[212:215], v[78:81]
	v_mfma_f32_16x16x32_bf16 v[74:77], v[158:161], v[212:215], v[74:77]
	v_mfma_f32_16x16x32_bf16 v[110:113], v[162:165], v[184:187], v[110:113]
	v_mfma_f32_16x16x32_bf16 v[106:109], v[176:179], v[184:187], v[106:109]
	v_mfma_f32_16x16x32_bf16 v[102:105], v[162:165], v[192:195], v[102:105]
	v_mfma_f32_16x16x32_bf16 v[98:101], v[176:179], v[192:195], v[98:101]
	v_mfma_f32_16x16x32_bf16 v[86:89], v[162:165], v[200:203], v[86:89]
	v_mfma_f32_16x16x32_bf16 v[82:85], v[176:179], v[200:203], v[82:85]
	v_mfma_f32_16x16x32_bf16 v[70:73], v[162:165], v[208:211], v[70:73]
	v_mfma_f32_16x16x32_bf16 v[66:69], v[176:179], v[208:211], v[66:69]
	v_mfma_f32_16x16x32_bf16 v[110:113], v[172:175], v[188:191], v[110:113]
	v_mfma_f32_16x16x32_bf16 v[106:109], v[180:183], v[188:191], v[106:109]
	v_mfma_f32_16x16x32_bf16 v[102:105], v[172:175], v[196:199], v[102:105]
	v_mfma_f32_16x16x32_bf16 v[98:101], v[180:183], v[196:199], v[98:101]
	v_mfma_f32_16x16x32_bf16 v[86:89], v[172:175], v[204:207], v[86:89]
	v_mfma_f32_16x16x32_bf16 v[82:85], v[180:183], v[204:207], v[82:85]
	v_mfma_f32_16x16x32_bf16 v[70:73], v[172:175], v[212:215], v[70:73]
	v_mfma_f32_16x16x32_bf16 v[66:69], v[180:183], v[212:215], v[66:69]
	s_setprio 0
	s_barrier
; #define PG8_STAGE(bufoff, gbase, voff) do { _Pragma("unroll") for (int _i = 0; _i < 2; ++_i) \
;         __builtin_amdgcn_global_load_lds((const unsigned*)((const char*)(gbase) + (voff)[_i]), (PG8_LAS unsigned*)(lds + (bufoff) + ldsw + _i * 8192), 16, 0, 0); } while (0)
; #define PG8_LDA(dst, b, h) do { _Pragma("unroll") for (int m = 0; m < 4; ++m) _Pragma("unroll") for (int k = 0; k < 2; ++k) dst[m][k] = *(const PG8_LAS bf16x8*)(lds + PG8_SA(b, h) + aoff + m * 2048 + k * 1024); } while (0)
; #define PG8_MMA(ai, bj, At, Bt) do { __builtin_amdgcn_s_setprio(1); _Pragma("unroll") for (int m = 0; m < 4; ++m) _Pragma("unroll") for (int n = 0; n < 2; ++n) _Pragma("unroll") for (int k = 0; k < 2; ++k) \
;         acc[ai][bj][m][n] = __builtin_amdgcn_mfma_f32_16x16x32_bf16(Bt[n][k], At[m][k], acc[ai][bj][m][n], 0, 0, 0); __builtin_amdgcn_s_setprio(0); } while (0)
; #define PG8_WAIT_V(n) asm volatile("s_waitcnt vmcnt(" #n ")" ::: "memory")
; #define PG8_WAIT_L(n) asm volatile("s_waitcnt lgkmcnt(" #n ")" ::: "memory")
; #define PG8_BAR __builtin_amdgcn_s_barrier()
; #define PG8_SCHED __builtin_amdgcn_sched_barrier(0)
; template <class Epi, class Sched, bool ALIGN_EPI = false>
; __device__ __forceinline__ void gemm_phase(PG8_LAS unsigned char* lds, const Gemm g, const Sched& S, const Epi& E) {
;     ...
;         for (int t = 0; t < nt; t += 2) {
;     ...
;             PG8_LDA(At, 1, 1); PG8_STAGE(PG8_SB(1, 0), b3, voffB); PG8_STAGE(PG8_SB(1, 1), b3 + hstep, voffB); PG8_STAGE(PG8_SA(1, 0), a3, w0);
;             PG8_WAIT_V(8); PG8_WAIT_L(0); PG8_BAR; PG8_MMA(1, 0, At, B0); PG8_MMA(1, 1, At, B1); PG8_BAR; PG8_SCHED;
;             if constexpr (Epi::KSCALE) { if (((t + 2) & 7) == 0 && t + 2 < nt) { E.kscale(acc, pf, ((t + 2) >> 3) - 1, wr, fr); PG8_SCHED; } }
;         }
	s_add_i32 s56, s79, s61
	v_lshl_add_u64 v[216:217], v[216:217], 0, s[18:19]
	s_mov_b32 m0, s56
	ds_read_b128 v[184:187], v170 offset:49152
	ds_read_b128 v[188:191], v170 offset:50176
	ds_read_b128 v[192:195], v170 offset:51200
	ds_read_b128 v[196:199], v170 offset:52224
	ds_read_b128 v[200:203], v170 offset:53248
	ds_read_b128 v[204:207], v170 offset:54272
	ds_read_b128 v[208:211], v170 offset:55296
	ds_read_b128 v[212:215], v170 offset:56320
	global_load_lds_dwordx4 v[216:217], off
	s_add_i32 m0, s56, 0x2000
	s_add_u32 s54, s54, 0x80080
	v_lshl_add_u64 v[216:217], v[218:219], 0, s[18:19]
	s_addc_u32 s55, s55, 0
	s_add_i32 s56, s80, s61
	global_load_lds_dwordx4 v[216:217], off
	v_lshl_add_u64 v[216:217], s[54:55], 0, v[140:141]
	s_mov_b32 m0, s56
	s_nop 0
	global_load_lds_dwordx4 v[216:217], off
	v_lshl_add_u64 v[216:217], s[54:55], 0, v[144:145]
	s_add_i32 m0, s56, 0x2000
	s_nop 0
	global_load_lds_dwordx4 v[216:217], off
	v_lshl_add_u64 v[216:217], v[220:221], 0, s[18:19]
	s_mov_b32 m0, s67
	s_nop 0
	global_load_lds_dwordx4 v[216:217], off
	v_lshl_add_u64 v[216:217], v[222:223], 0, s[18:19]
	s_mov_b32 m0, s68
	s_nop 0
	global_load_lds_dwordx4 v[216:217], off
	s_waitcnt vmcnt(8)
	s_waitcnt lgkmcnt(0)
	s_barrier
	s_setprio 1
	v_mfma_f32_16x16x32_bf16 v[54:57], v[130:133], v[184:187], v[54:57]
	v_mfma_f32_16x16x32_bf16 v[50:53], v[154:157], v[184:187], v[50:53]
	v_mfma_f32_16x16x32_bf16 v[38:41], v[130:133], v[192:195], v[38:41]
	v_mfma_f32_16x16x32_bf16 v[34:37], v[154:157], v[192:195], v[34:37]
	v_mfma_f32_16x16x32_bf16 v[22:25], v[130:133], v[200:203], v[22:25]
	v_mfma_f32_16x16x32_bf16 v[18:21], v[154:157], v[200:203], v[18:21]
	v_mfma_f32_16x16x32_bf16 v[6:9], v[130:133], v[208:211], v[6:9]
	v_mfma_f32_16x16x32_bf16 v[2:5], v[154:157], v[208:211], v[2:5]
	v_mfma_f32_16x16x32_bf16 v[54:57], v[134:137], v[188:191], v[54:57]
	v_mfma_f32_16x16x32_bf16 v[50:53], v[158:161], v[188:191], v[50:53]
	v_mfma_f32_16x16x32_bf16 v[38:41], v[134:137], v[196:199], v[38:41]
	v_mfma_f32_16x16x32_bf16 v[34:37], v[158:161], v[196:199], v[34:37]
	v_mfma_f32_16x16x32_bf16 v[22:25], v[134:137], v[204:207], v[22:25]
	v_mfma_f32_16x16x32_bf16 v[18:21], v[158:161], v[204:207], v[18:21]
	v_mfma_f32_16x16x32_bf16 v[6:9], v[134:137], v[212:215], v[6:9]
	v_mfma_f32_16x16x32_bf16 v[2:5], v[158:161], v[212:215], v[2:5]
	v_mfma_f32_16x16x32_bf16 v[62:65], v[162:165], v[184:187], v[62:65]
	v_mfma_f32_16x16x32_bf16 v[58:61], v[176:179], v[184:187], v[58:61]
	v_mfma_f32_16x16x32_bf16 v[46:49], v[162:165], v[192:195], v[46:49]
	v_mfma_f32_16x16x32_bf16 v[42:45], v[176:179], v[192:195], v[42:45]
	v_mfma_f32_16x16x32_bf16 v[30:33], v[162:165], v[200:203], v[30:33]
	v_mfma_f32_16x16x32_bf16 v[26:29], v[176:179], v[200:203], v[26:29]
	v_mfma_f32_16x16x32_bf16 v[14:17], v[162:165], v[208:211], v[14:17]
	v_mfma_f32_16x16x32_bf16 v[10:13], v[176:179], v[208:211], v[10:13]
	v_mfma_f32_16x16x32_bf16 v[62:65], v[172:175], v[188:191], v[62:65]
	v_mfma_f32_16x16x32_bf16 v[58:61], v[180:183], v[188:191], v[58:61]
	v_mfma_f32_16x16x32_bf16 v[46:49], v[172:175], v[196:199], v[46:49]
	v_mfma_f32_16x16x32_bf16 v[42:45], v[180:183], v[196:199], v[42:45]
	v_mfma_f32_16x16x32_bf16 v[30:33], v[172:175], v[204:207], v[30:33]
	v_mfma_f32_16x16x32_bf16 v[26:29], v[180:183], v[204:207], v[26:29]
	v_mfma_f32_16x16x32_bf16 v[14:17], v[172:175], v[212:215], v[14:17]
	v_mfma_f32_16x16x32_bf16 v[10:13], v[180:183], v[212:215], v[10:13]
	s_setprio 0
	s_barrier
	s_add_i32 s78, s78, 2
	s_add_u32 s52, s52, 0x100
	s_addc_u32 s53, s53, 0
	s_add_u32 s76, s76, 0x100
	s_addc_u32 s77, s77, 0
	s_cmp_gt_u32 s78, 29
	s_cbranch_scc0 .LBB0_1198
	s_and_b64 vcc, exec, s[22:23]
	s_cbranch_vccz .LBB0_1201
	s_barrier

;     __device__ __forceinline__ int arow(const Unit& u, int r) const { if (!GATHER_) return u.pm * BM + r; int slot = u.s0 + r; slot = slot < u.cnt ? slot : u.cnt - 1; return list[u.e * 16384 + slot] >> 1; }
; #define PG8_STAGE(bufoff, gbase, voff) do { _Pragma("unroll") for (int _i = 0; _i < 2; ++_i) \
;         __builtin_amdgcn_global_load_lds((const unsigned*)((const char*)(gbase) + (voff)[_i]), (PG8_LAS unsigned*)(lds + (bufoff) + ldsw + _i * 8192), 16, 0, 0); } while (0)
; #define PG8_LDA(dst, b, h) do { _Pragma("unroll") for (int m = 0; m < 4; ++m) _Pragma("unroll") for (int k = 0; k < 2; ++k) dst[m][k] = *(const PG8_LAS bf16x8*)(lds + PG8_SA(b, h) + aoff + m * 2048 + k * 1024); } while (0)
; #define PG8_LDB(dst, b, h) do { _Pragma("unroll") for (int n = 0; n < 2; ++n) _Pragma("unroll") for (int k = 0; k < 2; ++k) dst[n][k] = *(const PG8_LAS bf16x8*)(lds + PG8_SB(b, h) + boff + n * 2048 + k * 1024); } while (0)
; #define PG8_WAIT_V(n) asm volatile("s_waitcnt vmcnt(" #n ")" ::: "memory")
; #define PG8_WAIT_L(n) asm volatile("s_waitcnt lgkmcnt(" #n ")" ::: "memory")
; #define PG8_BAR __builtin_amdgcn_s_barrier()
; template <class Epi, class Sched, bool ALIGN_EPI = false>
; __device__ __forceinline__ void gemm_phase(PG8_LAS unsigned char* lds, const Gemm g, const Sched& S, const Epi& E) {
;     ...
;         for (int i = 0; i < 2; ++i) { vc0[i] = (unsigned)(S.arow(cur, RA[i]) * K + CA[i]) * 2u; vc1[i] = (unsigned)(S.arow(cur, RA[i] + HALF) * K + CA[i]) * 2u; vn0[i] = vc0[i]; vn1[i] = vc1[i]; }
;     ...
;             const char* a2 = last ? nA : cA + (size_t)(t + 2) * kstep; const char* b2 = last ? nB : cB + (size_t)(t + 2) * kstep;
;             const char* a3 = a2 + kstep; const char* b3 = b2 + kstep;
;             unsigned w0[2], w1[2];
; #pragma unroll
;             for (int i = 0; i < 2; ++i) { w0[i] = (Sched::GATHER && last) ? vn0[i] : vc0[i]; w1[i] = (Sched::GATHER && last) ? vn1[i] : vc1[i]; }
;             if (last && has_next) S.a_ready(nxt);
;             PG8_LDB(B0, 0, 0); PG8_LDB(B1, 0, 1); PG8_SCHED; PG8_LDA(At, 0, 0); PG8_STAGE(PG8_SA(1, 1), a1 + hstepA, vc1);
;             PG8_WAIT_V(8); PG8_WAIT_L(0); PG8_BAR; PG8_MMA(0, 0, At, B0); PG8_MMA(0, 1, At, B1); PG8_BAR; PG8_SCHED;
;             PG8_LDA(At, 0, 1); PG8_STAGE(PG8_SB(0, 0), b2, voffB); PG8_STAGE(PG8_SB(0, 1), b2 + hstep, voffB); PG8_STAGE(PG8_SA(0, 0), a2, w0);
.LBB0_1414:
	s_add_u32 s56, s36, s54
	v_add_u32_e32 v155, s79, v143
	s_addc_u32 s57, s37, s55
	ds_read_b128 v[164:167], v155
	ds_read_b128 v[168:171], v155 offset:1024
	ds_read_b128 v[172:175], v155 offset:2048
	ds_read_b128 v[176:179], v155 offset:3072
	v_add_u32_e32 v155, s80, v143
	s_add_u32 s58, s56, 0x3c800100
	ds_read_b128 v[180:183], v155
	ds_read_b128 v[184:187], v155 offset:1024
	ds_read_b128 v[188:191], v155 offset:2048
	ds_read_b128 v[192:195], v155 offset:3072
	s_addc_u32 s59, s57, 0
	s_add_u32 s88, s47, s54
	s_addc_u32 s89, s86, s55
	s_cmpk_eq_i32 s54, 0xf00
	s_cselect_b64 vcc, -1, 0
	s_and_b64 s[56:57], vcc, exec
	v_cndmask_b32_e32 v134, v151, v149, vcc
	s_cselect_b32 s59, s21, s59
	s_cselect_b32 s58, s20, s58
	v_cndmask_b32_e32 v153, v152, v157, vcc
	v_cndmask_b32_e32 v228, v150, v162, vcc
	v_cndmask_b32_e32 v155, v154, v163, vcc
	s_cselect_b32 s57, s51, s89
	s_cselect_b32 s56, s50, s88
	v_lshl_add_u64 v[230:231], v[160:161], 0, s[54:55]
	s_add_i32 m0, s53, 0xc000
	ds_read_b128 v[196:199], v147
	ds_read_b128 v[200:203], v147 offset:1024
	ds_read_b128 v[204:207], v147 offset:2048
	ds_read_b128 v[208:211], v147 offset:3072
	ds_read_b128 v[212:215], v147 offset:4096
	ds_read_b128 v[216:219], v147 offset:5120
	ds_read_b128 v[220:223], v147 offset:6144
	ds_read_b128 v[224:227], v147 offset:7168
	global_load_lds_dwordx4 v[230:231], off
	v_lshl_add_u64 v[230:231], v[158:159], 0, s[54:55]
	s_add_i32 m0, s53, 0xe000
	s_nop 0
	global_load_lds_dwordx4 v[230:231], off
	s_waitcnt vmcnt(8)
	s_waitcnt lgkmcnt(0)
	s_barrier
	s_setprio 1
	v_mfma_f32_16x16x32_bf16 v[126:129], v[164:167], v[196:199], v[126:129]
	v_mfma_f32_16x16x32_bf16 v[122:125], v[172:175], v[196:199], v[122:125]
	v_mfma_f32_16x16x32_bf16 v[110:113], v[164:167], v[204:207], v[110:113]
	v_mfma_f32_16x16x32_bf16 v[106:109], v[172:175], v[204:207], v[106:109]
	v_mfma_f32_16x16x32_bf16 v[94:97], v[164:167], v[212:215], v[94:97]
	v_mfma_f32_16x16x32_bf16 v[90:93], v[172:175], v[212:215], v[90:93]
	v_mfma_f32_16x16x32_bf16 v[78:81], v[164:167], v[220:223], v[78:81]
	v_mfma_f32_16x16x32_bf16 v[74:77], v[172:175], v[220:223], v[74:77]
	v_mfma_f32_16x16x32_bf16 v[126:129], v[168:171], v[200:203], v[126:129]
	v_mfma_f32_16x16x32_bf16 v[122:125], v[176:179], v[200:203], v[122:125]
	v_mfma_f32_16x16x32_bf16 v[110:113], v[168:171], v[208:211], v[110:113]
	v_mfma_f32_16x16x32_bf16 v[106:109], v[176:179], v[208:211], v[106:109]
	v_mfma_f32_16x16x32_bf16 v[94:97], v[168:171], v[216:219], v[94:97]
	v_mfma_f32_16x16x32_bf16 v[90:93], v[176:179], v[216:219], v[90:93]
	v_mfma_f32_16x16x32_bf16 v[78:81], v[168:171], v[224:227], v[78:81]
	v_mfma_f32_16x16x32_bf16 v[74:77], v[176:179], v[224:227], v[74:77]
	v_mfma_f32_16x16x32_bf16 v[118:121], v[180:183], v[196:199], v[118:121]
	v_mfma_f32_16x16x32_bf16 v[114:117], v[188:191], v[196:199], v[114:117]
	v_mfma_f32_16x16x32_bf16 v[102:105], v[180:183], v[204:207], v[102:105]
	v_mfma_f32_16x16x32_bf16 v[98:101], v[188:191], v[204:207], v[98:101]
	v_mfma_f32_16x16x32_bf16 v[86:89], v[180:183], v[212:215], v[86:89]
	v_mfma_f32_16x16x32_bf16 v[82:85], v[188:191], v[212:215], v[82:85]
	v_mfma_f32_16x16x32_bf16 v[70:73], v[180:183], v[220:223], v[70:73]
	v_mfma_f32_16x16x32_bf16 v[66:69], v[188:191], v[220:223], v[66:69]
	v_mfma_f32_16x16x32_bf16 v[118:121], v[184:187], v[200:203], v[118:121]
	v_mfma_f32_16x16x32_bf16 v[114:117], v[192:195], v[200:203], v[114:117]
	v_mfma_f32_16x16x32_bf16 v[102:105], v[184:187], v[208:211], v[102:105]
	v_mfma_f32_16x16x32_bf16 v[98:101], v[192:195], v[208:211], v[98:101]
	v_mfma_f32_16x16x32_bf16 v[86:89], v[184:187], v[216:219], v[86:89]
	v_mfma_f32_16x16x32_bf16 v[82:85], v[192:195], v[216:219], v[82:85]
	v_mfma_f32_16x16x32_bf16 v[70:73], v[184:187], v[224:227], v[70:73]
	v_mfma_f32_16x16x32_bf16 v[66:69], v[192:195], v[224:227], v[66:69]
	s_setprio 0
	s_barrier
	s_add_i32 s88, s79, s71
	v_lshl_add_u64 v[230:231], s[56:57], 0, v[130:131]
	s_mov_b32 m0, s88
	ds_read_b128 v[196:199], v147 offset:16384
	ds_read_b128 v[200:203], v147 offset:17408
	ds_read_b128 v[204:207], v147 offset:18432
	ds_read_b128 v[208:211], v147 offset:19456
	ds_read_b128 v[212:215], v147 offset:20480
	ds_read_b128 v[216:219], v147 offset:21504
	ds_read_b128 v[220:223], v147 offset:22528
	ds_read_b128 v[224:227], v147 offset:23552
	global_load_lds_dwordx4 v[230:231], off
	s_add_i32 m0, s88, 0x2000
	s_add_u32 s88, s56, 0x80000
	v_lshl_add_u64 v[232:233], s[56:57], 0, v[132:133]
	s_addc_u32 s89, s57, 0
	s_add_i32 s90, s80, s71
	global_load_lds_dwordx4 v[232:233], off
	v_lshl_add_u64 v[234:235], s[88:89], 0, v[130:131]
	s_mov_b32 m0, s90
	v_mov_b32_e32 v229, v135
	global_load_lds_dwordx4 v[234:235], off
	v_lshl_add_u64 v[234:235], s[88:89], 0, v[132:133]
	s_add_i32 m0, s90, 0x2000
	s_nop 0
	global_load_lds_dwordx4 v[234:235], off
	s_mov_b32 m0, s53
	v_lshl_add_u64 v[234:235], s[58:59], 0, v[134:135]
	global_load_lds_dwordx4 v134, s[58:59]
	s_mov_b32 m0, s72
	s_nop 0
	global_load_lds_dwordx4 v228, s[58:59]
	s_waitcnt vmcnt(8)
	s_waitcnt lgkmcnt(0)
	v_lshl_add_u64 v[228:229], s[58:59], 0, v[228:229]
	s_barrier
; #define PG8_STAGE(bufoff, gbase, voff) do { _Pragma("unroll") for (int _i = 0; _i < 2; ++_i) \
;         __builtin_amdgcn_global_load_lds((const unsigned*)((const char*)(gbase) + (voff)[_i]), (PG8_LAS unsigned*)(lds + (bufoff) + ldsw + _i * 8192), 16, 0, 0); } while (0)
; #define PG8_LDA(dst, b, h) do { _Pragma("unroll") for (int m = 0; m < 4; ++m) _Pragma("unroll") for (int k = 0; k < 2; ++k) dst[m][k] = *(const PG8_LAS bf16x8*)(lds + PG8_SA(b, h) + aoff + m * 2048 + k * 1024); } while (0)
; #define PG8_LDB(dst, b, h) do { _Pragma("unroll") for (int n = 0; n < 2; ++n) _Pragma("unroll") for (int k = 0; k < 2; ++k) dst[n][k] = *(const PG8_LAS bf16x8*)(lds + PG8_SB(b, h) + boff + n * 2048 + k * 1024); } while (0)
; #define PG8_MMA(ai, bj, At, Bt) do { __builtin_amdgcn_s_setprio(1); _Pragma("unroll") for (int m = 0; m < 4; ++m) _Pragma("unroll") for (int n = 0; n < 2; ++n) _Pragma("unroll") for (int k = 0; k < 2; ++k) \
;         acc[ai][bj][m][n] = __builtin_amdgcn_mfma_f32_16x16x32_bf16(Bt[n][k], At[m][k], acc[ai][bj][m][n], 0, 0, 0); __builtin_amdgcn_s_setprio(0); } while (0)
; #define PG8_WAIT_V(n) asm volatile("s_waitcnt vmcnt(" #n ")" ::: "memory")
; template <class Epi, class Sched, bool ALIGN_EPI = false>
; __device__ __forceinline__ void gemm_phase(PG8_LAS unsigned char* lds, const Gemm g, const Sched& S, const Epi& E) {
;     ...
;             PG8_LDB(B0, 0, 0); PG8_LDB(B1, 0, 1); PG8_SCHED; PG8_LDA(At, 0, 0); PG8_STAGE(PG8_SA(1, 1), a1 + hstepA, vc1);
;             PG8_WAIT_V(8); PG8_WAIT_L(0); PG8_BAR; PG8_MMA(0, 0, At, B0); PG8_MMA(0, 1, At, B1); PG8_BAR; PG8_SCHED;
;             PG8_LDA(At, 0, 1); PG8_STAGE(PG8_SB(0, 0), b2, voffB); PG8_STAGE(PG8_SB(0, 1), b2 + hstep, voffB); PG8_STAGE(PG8_SA(0, 0), a2, w0);
;             PG8_WAIT_V(8); PG8_WAIT_L(0); PG8_BAR; PG8_MMA(1, 0, At, B0); PG8_MMA(1, 1, At, B1); PG8_BAR; PG8_SCHED;
;             PG8_LDB(B0, 1, 0); PG8_LDB(B1, 1, 1); PG8_SCHED; PG8_LDA(At, 1, 0); PG8_STAGE(PG8_SA(0, 1), a2 + hstepA, w1);
;             PG8_WAIT_V(8); PG8_WAIT_L(0); PG8_BAR; PG8_MMA(0, 0, At, B0); PG8_MMA(0, 1, At, B1); PG8_BAR; PG8_SCHED;
;             PG8_LDA(At, 1, 1); PG8_STAGE(PG8_SB(1, 0), b3, voffB); PG8_STAGE(PG8_SB(1, 1), b3 + hstep, voffB); PG8_STAGE(PG8_SA(1, 0), a3, w0);
;             PG8_WAIT_V(8); PG8_WAIT_L(0); PG8_BAR; PG8_MMA(1, 0, At, B0); PG8_MMA(1, 1, At, B1); PG8_BAR; PG8_SCHED;
	s_setprio 1
	v_mfma_f32_16x16x32_bf16 v[62:65], v[164:167], v[196:199], v[62:65]
	v_mfma_f32_16x16x32_bf16 v[58:61], v[172:175], v[196:199], v[58:61]
	v_mfma_f32_16x16x32_bf16 v[50:53], v[164:167], v[204:207], v[50:53]
	v_mfma_f32_16x16x32_bf16 v[42:45], v[172:175], v[204:207], v[42:45]
	v_mfma_f32_16x16x32_bf16 v[34:37], v[164:167], v[212:215], v[34:37]
	v_mfma_f32_16x16x32_bf16 v[30:33], v[172:175], v[212:215], v[30:33]
	v_mfma_f32_16x16x32_bf16 v[14:17], v[164:167], v[220:223], v[14:17]
	v_mfma_f32_16x16x32_bf16 v[2:5], v[172:175], v[220:223], v[2:5]
	v_mfma_f32_16x16x32_bf16 v[62:65], v[168:171], v[200:203], v[62:65]
	v_mfma_f32_16x16x32_bf16 v[58:61], v[176:179], v[200:203], v[58:61]
	v_mfma_f32_16x16x32_bf16 v[50:53], v[168:171], v[208:211], v[50:53]
	v_mfma_f32_16x16x32_bf16 v[42:45], v[176:179], v[208:211], v[42:45]
	v_mfma_f32_16x16x32_bf16 v[34:37], v[168:171], v[216:219], v[34:37]
	v_mfma_f32_16x16x32_bf16 v[30:33], v[176:179], v[216:219], v[30:33]
	v_mfma_f32_16x16x32_bf16 v[14:17], v[168:171], v[224:227], v[14:17]
	v_mfma_f32_16x16x32_bf16 v[2:5], v[176:179], v[224:227], v[2:5]
	v_mfma_f32_16x16x32_bf16 v[54:57], v[180:183], v[196:199], v[54:57]
	v_mfma_f32_16x16x32_bf16 v[46:49], v[188:191], v[196:199], v[46:49]
	v_mfma_f32_16x16x32_bf16 v[38:41], v[180:183], v[204:207], v[38:41]
	v_mfma_f32_16x16x32_bf16 v[26:29], v[188:191], v[204:207], v[26:29]
	v_mfma_f32_16x16x32_bf16 v[22:25], v[180:183], v[212:215], v[22:25]
	v_mfma_f32_16x16x32_bf16 v[18:21], v[188:191], v[212:215], v[18:21]
	v_mfma_f32_16x16x32_bf16 v[10:13], v[180:183], v[220:223], v[10:13]
	v_mfma_f32_16x16x32_bf16 v[6:9], v[188:191], v[220:223], v[6:9]
	v_mfma_f32_16x16x32_bf16 v[54:57], v[184:187], v[200:203], v[54:57]
	v_mfma_f32_16x16x32_bf16 v[46:49], v[192:195], v[200:203], v[46:49]
	v_mfma_f32_16x16x32_bf16 v[38:41], v[184:187], v[208:211], v[38:41]
	v_mfma_f32_16x16x32_bf16 v[26:29], v[192:195], v[208:211], v[26:29]
	v_mfma_f32_16x16x32_bf16 v[22:25], v[184:187], v[216:219], v[22:25]
	v_mfma_f32_16x16x32_bf16 v[18:21], v[192:195], v[216:219], v[18:21]
	v_mfma_f32_16x16x32_bf16 v[10:13], v[184:187], v[224:227], v[10:13]
	v_mfma_f32_16x16x32_bf16 v[6:9], v[192:195], v[224:227], v[6:9]
	s_setprio 0
	s_barrier
	s_add_i32 s88, 0, 0x18000
	v_add_u32_e32 v134, s88, v143
	s_add_i32 s89, 0, 0x1c000
	ds_read_b128 v[164:167], v134
	ds_read_b128 v[168:171], v134 offset:1024
	ds_read_b128 v[172:175], v134 offset:2048
	ds_read_b128 v[176:179], v134 offset:3072
	v_add_u32_e32 v134, s89, v143
	ds_read_b128 v[180:183], v134
	ds_read_b128 v[184:187], v134 offset:1024
	ds_read_b128 v[188:191], v134 offset:2048
	ds_read_b128 v[192:195], v134 offset:3072
	s_mov_b32 m0, s73
	ds_read_b128 v[196:199], v147 offset:32768
	ds_read_b128 v[200:203], v147 offset:33792
	ds_read_b128 v[204:207], v147 offset:34816
	ds_read_b128 v[208:211], v147 offset:35840
	ds_read_b128 v[212:215], v147 offset:36864
	ds_read_b128 v[216:219], v147 offset:37888
	ds_read_b128 v[220:223], v147 offset:38912
	ds_read_b128 v[224:227], v147 offset:39936
	global_load_lds_dwordx4 v153, s[58:59]
	s_mov_b32 m0, s74
	s_nop 0
	global_load_lds_dwordx4 v155, s[58:59]
	s_waitcnt vmcnt(8)
	s_waitcnt lgkmcnt(0)
	s_barrier
	s_setprio 1
	v_mfma_f32_16x16x32_bf16 v[126:129], v[164:167], v[196:199], v[126:129]
	v_mfma_f32_16x16x32_bf16 v[122:125], v[172:175], v[196:199], v[122:125]
	v_mfma_f32_16x16x32_bf16 v[110:113], v[164:167], v[204:207], v[110:113]
	v_mfma_f32_16x16x32_bf16 v[106:109], v[172:175], v[204:207], v[106:109]
	v_mfma_f32_16x16x32_bf16 v[94:97], v[164:167], v[212:215], v[94:97]
	v_mfma_f32_16x16x32_bf16 v[90:93], v[172:175], v[212:215], v[90:93]
	v_mfma_f32_16x16x32_bf16 v[78:81], v[164:167], v[220:223], v[78:81]
	v_mfma_f32_16x16x32_bf16 v[74:77], v[172:175], v[220:223], v[74:77]
	v_mfma_f32_16x16x32_bf16 v[126:129], v[168:171], v[200:203], v[126:129]
	v_mfma_f32_16x16x32_bf16 v[122:125], v[176:179], v[200:203], v[122:125]
	v_mfma_f32_16x16x32_bf16 v[110:113], v[168:171], v[208:211], v[110:113]
	v_mfma_f32_16x16x32_bf16 v[106:109], v[176:179], v[208:211], v[106:109]
	v_mfma_f32_16x16x32_bf16 v[94:97], v[168:171], v[216:219], v[94:97]
	v_mfma_f32_16x16x32_bf16 v[90:93], v[176:179], v[216:219], v[90:93]
	v_mfma_f32_16x16x32_bf16 v[78:81], v[168:171], v[224:227], v[78:81]
	v_mfma_f32_16x16x32_bf16 v[74:77], v[176:179], v[224:227], v[74:77]
	v_mfma_f32_16x16x32_bf16 v[118:121], v[180:183], v[196:199], v[118:121]
	v_mfma_f32_16x16x32_bf16 v[114:117], v[188:191], v[196:199], v[114:117]
	v_mfma_f32_16x16x32_bf16 v[102:105], v[180:183], v[204:207], v[102:105]
	v_mfma_f32_16x16x32_bf16 v[98:101], v[188:191], v[204:207], v[98:101]
	v_mfma_f32_16x16x32_bf16 v[86:89], v[180:183], v[212:215], v[86:89]
	v_mfma_f32_16x16x32_bf16 v[82:85], v[188:191], v[212:215], v[82:85]
	v_mfma_f32_16x16x32_bf16 v[70:73], v[180:183], v[220:223], v[70:73]
	v_mfma_f32_16x16x32_bf16 v[66:69], v[188:191], v[220:223], v[66:69]
	v_mfma_f32_16x16x32_bf16 v[118:121], v[184:187], v[200:203], v[118:121]
	v_mfma_f32_16x16x32_bf16 v[114:117], v[192:195], v[200:203], v[114:117]
	v_mfma_f32_16x16x32_bf16 v[102:105], v[184:187], v[208:211], v[102:105]
	v_mfma_f32_16x16x32_bf16 v[98:101], v[192:195], v[208:211], v[98:101]
	v_mfma_f32_16x16x32_bf16 v[86:89], v[184:187], v[216:219], v[86:89]
	v_mfma_f32_16x16x32_bf16 v[82:85], v[192:195], v[216:219], v[82:85]
	v_mfma_f32_16x16x32_bf16 v[70:73], v[184:187], v[224:227], v[70:73]
	v_mfma_f32_16x16x32_bf16 v[66:69], v[192:195], v[224:227], v[66:69]
	s_setprio 0
	s_barrier
; #define PG8_STAGE(bufoff, gbase, voff) do { _Pragma("unroll") for (int _i = 0; _i < 2; ++_i) \
;         __builtin_amdgcn_global_load_lds((const unsigned*)((const char*)(gbase) + (voff)[_i]), (PG8_LAS unsigned*)(lds + (bufoff) + ldsw + _i * 8192), 16, 0, 0); } while (0)
; #define PG8_LDA(dst, b, h) do { _Pragma("unroll") for (int m = 0; m < 4; ++m) _Pragma("unroll") for (int k = 0; k < 2; ++k) dst[m][k] = *(const PG8_LAS bf16x8*)(lds + PG8_SA(b, h) + aoff + m * 2048 + k * 1024); } while (0)
; #define PG8_MMA(ai, bj, At, Bt) do { __builtin_amdgcn_s_setprio(1); _Pragma("unroll") for (int m = 0; m < 4; ++m) _Pragma("unroll") for (int n = 0; n < 2; ++n) _Pragma("unroll") for (int k = 0; k < 2; ++k) \
;         acc[ai][bj][m][n] = __builtin_amdgcn_mfma_f32_16x16x32_bf16(Bt[n][k], At[m][k], acc[ai][bj][m][n], 0, 0, 0); __builtin_amdgcn_s_setprio(0); } while (0)
; #define PG8_WAIT_V(n) asm volatile("s_waitcnt vmcnt(" #n ")" ::: "memory")
; #define PG8_WAIT_L(n) asm volatile("s_waitcnt lgkmcnt(" #n ")" ::: "memory")
; #define PG8_BAR __builtin_amdgcn_s_barrier()
; #define PG8_SCHED __builtin_amdgcn_sched_barrier(0)
; template <class Epi, class Sched, bool ALIGN_EPI = false>
; __device__ __forceinline__ void gemm_phase(PG8_LAS unsigned char* lds, const Gemm g, const Sched& S, const Epi& E) {
;     ...
;             PG8_LDA(At, 1, 1); PG8_STAGE(PG8_SB(1, 0), b3, voffB); PG8_STAGE(PG8_SB(1, 1), b3 + hstep, voffB); PG8_STAGE(PG8_SA(1, 0), a3, w0);
;             PG8_WAIT_V(8); PG8_WAIT_L(0); PG8_BAR; PG8_MMA(1, 0, At, B0); PG8_MMA(1, 1, At, B1); PG8_BAR; PG8_SCHED;
;             if constexpr (Epi::KSCALE) { if (((t + 2) & 7) == 0 && t + 2 < nt) { E.kscale(acc, pf, ((t + 2) >> 3) - 1, wr, fr); PG8_SCHED; } }
;         }
;         if constexpr (ALIGN_EPI) { if (wr == 0) PG8_BAR; }
	s_add_i32 s58, s88, s71
	v_lshl_add_u64 v[230:231], v[230:231], 0, s[42:43]
	s_mov_b32 m0, s58
	ds_read_b128 v[196:199], v147 offset:49152
	ds_read_b128 v[200:203], v147 offset:50176
	ds_read_b128 v[204:207], v147 offset:51200
	ds_read_b128 v[208:211], v147 offset:52224
	ds_read_b128 v[212:215], v147 offset:53248
	ds_read_b128 v[216:219], v147 offset:54272
	ds_read_b128 v[220:223], v147 offset:55296
	ds_read_b128 v[224:227], v147 offset:56320
	global_load_lds_dwordx4 v[230:231], off
	s_add_i32 m0, s58, 0x2000
	s_add_u32 s56, s56, 0x80080
	v_lshl_add_u64 v[230:231], v[232:233], 0, s[42:43]
	s_addc_u32 s57, s57, 0
	s_add_i32 s58, s89, s71
	global_load_lds_dwordx4 v[230:231], off
	v_lshl_add_u64 v[230:231], s[56:57], 0, v[130:131]
	s_mov_b32 m0, s58
	v_lshl_add_u64 v[228:229], v[228:229], 0, s[42:43]
	global_load_lds_dwordx4 v[230:231], off
	v_lshl_add_u64 v[230:231], s[56:57], 0, v[132:133]
	s_add_i32 m0, s58, 0x2000
	s_nop 0
	global_load_lds_dwordx4 v[230:231], off
	v_lshl_add_u64 v[230:231], v[234:235], 0, s[42:43]
	s_mov_b32 m0, s77
	s_nop 0
	global_load_lds_dwordx4 v[230:231], off
	s_mov_b32 m0, s78
	s_nop 0
	global_load_lds_dwordx4 v[228:229], off
	s_waitcnt vmcnt(8)
	s_waitcnt lgkmcnt(0)
	s_barrier
	s_setprio 1
	v_mfma_f32_16x16x32_bf16 v[62:65], v[164:167], v[196:199], v[62:65]
	v_mfma_f32_16x16x32_bf16 v[58:61], v[172:175], v[196:199], v[58:61]
	v_mfma_f32_16x16x32_bf16 v[50:53], v[164:167], v[204:207], v[50:53]
	v_mfma_f32_16x16x32_bf16 v[42:45], v[172:175], v[204:207], v[42:45]
	v_mfma_f32_16x16x32_bf16 v[34:37], v[164:167], v[212:215], v[34:37]
	v_mfma_f32_16x16x32_bf16 v[30:33], v[172:175], v[212:215], v[30:33]
	v_mfma_f32_16x16x32_bf16 v[14:17], v[164:167], v[220:223], v[14:17]
	v_mfma_f32_16x16x32_bf16 v[2:5], v[172:175], v[220:223], v[2:5]
	v_mfma_f32_16x16x32_bf16 v[62:65], v[168:171], v[200:203], v[62:65]
	v_mfma_f32_16x16x32_bf16 v[58:61], v[176:179], v[200:203], v[58:61]
	v_mfma_f32_16x16x32_bf16 v[50:53], v[168:171], v[208:211], v[50:53]
	v_mfma_f32_16x16x32_bf16 v[42:45], v[176:179], v[208:211], v[42:45]
	v_mfma_f32_16x16x32_bf16 v[34:37], v[168:171], v[216:219], v[34:37]
	v_mfma_f32_16x16x32_bf16 v[30:33], v[176:179], v[216:219], v[30:33]
	v_mfma_f32_16x16x32_bf16 v[14:17], v[168:171], v[224:227], v[14:17]
	v_mfma_f32_16x16x32_bf16 v[2:5], v[176:179], v[224:227], v[2:5]
	v_mfma_f32_16x16x32_bf16 v[54:57], v[180:183], v[196:199], v[54:57]
	v_mfma_f32_16x16x32_bf16 v[46:49], v[188:191], v[196:199], v[46:49]
	v_mfma_f32_16x16x32_bf16 v[38:41], v[180:183], v[204:207], v[38:41]
	v_mfma_f32_16x16x32_bf16 v[26:29], v[188:191], v[204:207], v[26:29]
	v_mfma_f32_16x16x32_bf16 v[22:25], v[180:183], v[212:215], v[22:25]
	v_mfma_f32_16x16x32_bf16 v[18:21], v[188:191], v[212:215], v[18:21]
	v_mfma_f32_16x16x32_bf16 v[10:13], v[180:183], v[220:223], v[10:13]
	v_mfma_f32_16x16x32_bf16 v[6:9], v[188:191], v[220:223], v[6:9]
	v_mfma_f32_16x16x32_bf16 v[54:57], v[184:187], v[200:203], v[54:57]
	v_mfma_f32_16x16x32_bf16 v[46:49], v[192:195], v[200:203], v[46:49]
	v_mfma_f32_16x16x32_bf16 v[38:41], v[184:187], v[208:211], v[38:41]
	v_mfma_f32_16x16x32_bf16 v[26:29], v[192:195], v[208:211], v[26:29]
	v_mfma_f32_16x16x32_bf16 v[22:25], v[184:187], v[216:219], v[22:25]
	v_mfma_f32_16x16x32_bf16 v[18:21], v[192:195], v[216:219], v[18:21]
	v_mfma_f32_16x16x32_bf16 v[10:13], v[184:187], v[224:227], v[10:13]
	v_mfma_f32_16x16x32_bf16 v[6:9], v[192:195], v[224:227], v[6:9]
	s_setprio 0
	s_barrier
	s_add_i32 s87, s87, 2
	s_add_u32 s54, s54, 0x100
	s_addc_u32 s55, s55, 0
	s_cmp_gt_u32 s87, 29
	s_cbranch_scc0 .LBB0_1414
	s_and_b64 vcc, exec, s[44:45]
	s_cbranch_vccz .LBB0_1417
	s_barrier

; #define PG8_STAGE(bufoff, gbase, voff) do { _Pragma("unroll") for (int _i = 0; _i < 2; ++_i) \
;         __builtin_amdgcn_global_load_lds((const unsigned*)((const char*)(gbase) + (voff)[_i]), (PG8_LAS unsigned*)(lds + (bufoff) + ldsw + _i * 8192), 16, 0, 0); } while (0)
; #define PG8_LDA(dst, b, h) do { _Pragma("unroll") for (int m = 0; m < 4; ++m) _Pragma("unroll") for (int k = 0; k < 2; ++k) dst[m][k] = *(const PG8_LAS bf16x8*)(lds + PG8_SA(b, h) + aoff + m * 2048 + k * 1024); } while (0)
; #define PG8_LDB(dst, b, h) do { _Pragma("unroll") for (int n = 0; n < 2; ++n) _Pragma("unroll") for (int k = 0; k < 2; ++k) dst[n][k] = *(const PG8_LAS bf16x8*)(lds + PG8_SB(b, h) + boff + n * 2048 + k * 1024); } while (0)
; #define PG8_MMA(ai, bj, At, Bt) do { __builtin_amdgcn_s_setprio(1); _Pragma("unroll") for (int m = 0; m < 4; ++m) _Pragma("unroll") for (int n = 0; n < 2; ++n) _Pragma("unroll") for (int k = 0; k < 2; ++k) \
;         acc[ai][bj][m][n] = __builtin_amdgcn_mfma_f32_16x16x32_bf16(Bt[n][k], At[m][k], acc[ai][bj][m][n], 0, 0, 0); __builtin_amdgcn_s_setprio(0); } while (0)
; template <class Epi, class Sched, bool ALIGN_EPI = false>
; __device__ __forceinline__ void gemm_phase(PG8_LAS unsigned char* lds, const Gemm g, const Sched& S, const Epi& E) {
;     ...
;         for (int t = 0; t < nt; t += 2) {
;             const bool last = (t == nt - 2);
;             const char* a1 = cA + (size_t)(t + 1) * kstep;
;             const char* a2 = last ? nA : cA + (size_t)(t + 2) * kstep; const char* b2 = last ? nB : cB + (size_t)(t + 2) * kstep;
;             const char* a3 = a2 + kstep; const char* b3 = b2 + kstep;
;             unsigned w0[2], w1[2];
; #pragma unroll
;             for (int i = 0; i < 2; ++i) { w0[i] = (Sched::GATHER && last) ? vn0[i] : vc0[i]; w1[i] = (Sched::GATHER && last) ? vn1[i] : vc1[i]; }
;             if (last && has_next) S.a_ready(nxt);
;             PG8_LDB(B0, 0, 0); PG8_LDB(B1, 0, 1); PG8_SCHED; PG8_LDA(At, 0, 0); PG8_STAGE(PG8_SA(1, 1), a1 + hstepA, vc1);
;             PG8_WAIT_V(8); PG8_WAIT_L(0); PG8_BAR; PG8_MMA(0, 0, At, B0); PG8_MMA(0, 1, At, B1); PG8_BAR; PG8_SCHED;
;             PG8_LDA(At, 0, 1); PG8_STAGE(PG8_SB(0, 0), b2, voffB); PG8_STAGE(PG8_SB(0, 1), b2 + hstep, voffB); PG8_STAGE(PG8_SA(0, 0), a2, w0);
;             PG8_WAIT_V(8); PG8_WAIT_L(0); PG8_BAR; PG8_MMA(1, 0, At, B0); PG8_MMA(1, 1, At, B1); PG8_BAR; PG8_SCHED;
.LBB0_1480:
	ds_read_b128 v[172:175], v167
	ds_read_b128 v[176:179], v167 offset:1024
	ds_read_b128 v[180:183], v167 offset:2048
	ds_read_b128 v[184:187], v167 offset:3072
	ds_read_b128 v[188:191], v168
	ds_read_b128 v[192:195], v168 offset:1024
	ds_read_b128 v[196:199], v168 offset:2048
	ds_read_b128 v[200:203], v168 offset:3072
	s_add_u32 s16, s14, 0x3c800100
	s_addc_u32 s17, s15, 0
	s_add_u32 s56, s14, s43
	s_addc_u32 s57, s15, s44
	s_cmp_eq_u32 s45, 28
	s_cselect_b32 s19, s21, s17
	s_cselect_b32 s18, s20, s16
	s_cselect_b32 s17, s11, s57
	s_cselect_b32 s16, s10, s56
	s_mov_b32 m0, s46
	v_lshl_add_u64 v[236:237], s[14:15], 0, v[160:161]
	ds_read_b128 v[204:207], v169
	ds_read_b128 v[208:211], v169 offset:1024
	ds_read_b128 v[212:215], v169 offset:2048
	ds_read_b128 v[216:219], v169 offset:3072
	ds_read_b128 v[220:223], v169 offset:4096
	ds_read_b128 v[224:227], v169 offset:5120
	ds_read_b128 v[228:231], v169 offset:6144
	ds_read_b128 v[232:235], v169 offset:7168
	global_load_lds_dwordx4 v[236:237], off
	v_lshl_add_u64 v[236:237], s[14:15], 0, v[158:159]
	s_mov_b32 m0, s47
	s_nop 0
	global_load_lds_dwordx4 v[236:237], off
	s_waitcnt vmcnt(8)
	s_waitcnt lgkmcnt(0)
	s_barrier
	s_setprio 1
	v_mfma_f32_16x16x32_bf16 v[126:129], v[172:175], v[204:207], v[126:129]
	v_mfma_f32_16x16x32_bf16 v[122:125], v[180:183], v[204:207], v[122:125]
	v_mfma_f32_16x16x32_bf16 v[110:113], v[172:175], v[212:215], v[110:113]
	v_mfma_f32_16x16x32_bf16 v[106:109], v[180:183], v[212:215], v[106:109]
	v_mfma_f32_16x16x32_bf16 v[94:97], v[172:175], v[220:223], v[94:97]
	v_mfma_f32_16x16x32_bf16 v[90:93], v[180:183], v[220:223], v[90:93]
	v_mfma_f32_16x16x32_bf16 v[78:81], v[172:175], v[228:231], v[78:81]
	v_mfma_f32_16x16x32_bf16 v[74:77], v[180:183], v[228:231], v[74:77]
	v_mfma_f32_16x16x32_bf16 v[126:129], v[176:179], v[208:211], v[126:129]
	v_mfma_f32_16x16x32_bf16 v[122:125], v[184:187], v[208:211], v[122:125]
	v_mfma_f32_16x16x32_bf16 v[110:113], v[176:179], v[216:219], v[110:113]
	v_mfma_f32_16x16x32_bf16 v[106:109], v[184:187], v[216:219], v[106:109]
	v_mfma_f32_16x16x32_bf16 v[94:97], v[176:179], v[224:227], v[94:97]
	v_mfma_f32_16x16x32_bf16 v[90:93], v[184:187], v[224:227], v[90:93]
	v_mfma_f32_16x16x32_bf16 v[78:81], v[176:179], v[232:235], v[78:81]
	v_mfma_f32_16x16x32_bf16 v[74:77], v[184:187], v[232:235], v[74:77]
	v_mfma_f32_16x16x32_bf16 v[118:121], v[188:191], v[204:207], v[118:121]
	v_mfma_f32_16x16x32_bf16 v[114:117], v[196:199], v[204:207], v[114:117]
	v_mfma_f32_16x16x32_bf16 v[102:105], v[188:191], v[212:215], v[102:105]
	v_mfma_f32_16x16x32_bf16 v[98:101], v[196:199], v[212:215], v[98:101]
	v_mfma_f32_16x16x32_bf16 v[86:89], v[188:191], v[220:223], v[86:89]
	v_mfma_f32_16x16x32_bf16 v[82:85], v[196:199], v[220:223], v[82:85]
	v_mfma_f32_16x16x32_bf16 v[70:73], v[188:191], v[228:231], v[70:73]
	v_mfma_f32_16x16x32_bf16 v[66:69], v[196:199], v[228:231], v[66:69]
	v_mfma_f32_16x16x32_bf16 v[118:121], v[192:195], v[208:211], v[118:121]
	v_mfma_f32_16x16x32_bf16 v[114:117], v[200:203], v[208:211], v[114:117]
	v_mfma_f32_16x16x32_bf16 v[102:105], v[192:195], v[216:219], v[102:105]
	v_mfma_f32_16x16x32_bf16 v[98:101], v[200:203], v[216:219], v[98:101]
	v_mfma_f32_16x16x32_bf16 v[86:89], v[192:195], v[224:227], v[86:89]
	v_mfma_f32_16x16x32_bf16 v[82:85], v[200:203], v[224:227], v[82:85]
	v_mfma_f32_16x16x32_bf16 v[70:73], v[192:195], v[232:235], v[70:73]
	v_mfma_f32_16x16x32_bf16 v[66:69], v[200:203], v[232:235], v[66:69]
	s_setprio 0
	s_barrier
	s_mov_b32 m0, s48
	v_lshl_add_u64 v[236:237], s[16:17], 0, v[146:147]
	s_add_u32 s56, s16, 0x80000
	ds_read_b128 v[204:207], v169 offset:16384
	ds_read_b128 v[208:211], v169 offset:17408
	ds_read_b128 v[212:215], v169 offset:18432
	ds_read_b128 v[216:219], v169 offset:19456
	ds_read_b128 v[220:223], v169 offset:20480
	ds_read_b128 v[224:227], v169 offset:21504
	ds_read_b128 v[228:231], v169 offset:22528
	ds_read_b128 v[232:235], v169 offset:23552
	global_load_lds_dwordx4 v[236:237], off
	v_lshl_add_u64 v[238:239], s[16:17], 0, v[144:145]
	s_mov_b32 m0, s49
	s_addc_u32 s57, s17, 0
	global_load_lds_dwordx4 v[238:239], off
	v_lshl_add_u64 v[240:241], s[56:57], 0, v[146:147]
	s_mov_b32 m0, s50
	v_lshl_add_u64 v[242:243], s[18:19], 0, v[150:151]
	global_load_lds_dwordx4 v[240:241], off
	v_lshl_add_u64 v[240:241], s[56:57], 0, v[144:145]
	s_mov_b32 m0, s51
	s_nop 0
	global_load_lds_dwordx4 v[240:241], off
	v_lshl_add_u64 v[240:241], s[18:19], 0, v[148:149]
	s_mov_b32 m0, s25
	s_nop 0
	global_load_lds_dwordx4 v[240:241], off
	s_mov_b32 m0, s26
	s_nop 0
	global_load_lds_dwordx4 v[242:243], off
	s_waitcnt vmcnt(8)
	s_waitcnt lgkmcnt(0)
	s_barrier
; #define PG8_STAGE(bufoff, gbase, voff) do { _Pragma("unroll") for (int _i = 0; _i < 2; ++_i) \
;         __builtin_amdgcn_global_load_lds((const unsigned*)((const char*)(gbase) + (voff)[_i]), (PG8_LAS unsigned*)(lds + (bufoff) + ldsw + _i * 8192), 16, 0, 0); } while (0)
; #define PG8_LDA(dst, b, h) do { _Pragma("unroll") for (int m = 0; m < 4; ++m) _Pragma("unroll") for (int k = 0; k < 2; ++k) dst[m][k] = *(const PG8_LAS bf16x8*)(lds + PG8_SA(b, h) + aoff + m * 2048 + k * 1024); } while (0)
; #define PG8_LDB(dst, b, h) do { _Pragma("unroll") for (int n = 0; n < 2; ++n) _Pragma("unroll") for (int k = 0; k < 2; ++k) dst[n][k] = *(const PG8_LAS bf16x8*)(lds + PG8_SB(b, h) + boff + n * 2048 + k * 1024); } while (0)
; #define PG8_MMA(ai, bj, At, Bt) do { __builtin_amdgcn_s_setprio(1); _Pragma("unroll") for (int m = 0; m < 4; ++m) _Pragma("unroll") for (int n = 0; n < 2; ++n) _Pragma("unroll") for (int k = 0; k < 2; ++k) \
;         acc[ai][bj][m][n] = __builtin_amdgcn_mfma_f32_16x16x32_bf16(Bt[n][k], At[m][k], acc[ai][bj][m][n], 0, 0, 0); __builtin_amdgcn_s_setprio(0); } while (0)
; #define PG8_WAIT_V(n) asm volatile("s_waitcnt vmcnt(" #n ")" ::: "memory")
; #define PG8_WAIT_L(n) asm volatile("s_waitcnt lgkmcnt(" #n ")" ::: "memory")
; #define PG8_BAR __builtin_amdgcn_s_barrier()
; #define PG8_SCHED __builtin_amdgcn_sched_barrier(0)
; template <class Epi, class Sched, bool ALIGN_EPI = false>
; __device__ __forceinline__ void gemm_phase(PG8_LAS unsigned char* lds, const Gemm g, const Sched& S, const Epi& E) {
;     ...
;             PG8_WAIT_V(8); PG8_WAIT_L(0); PG8_BAR; PG8_MMA(1, 0, At, B0); PG8_MMA(1, 1, At, B1); PG8_BAR; PG8_SCHED;
;             PG8_LDB(B0, 1, 0); PG8_LDB(B1, 1, 1); PG8_SCHED; PG8_LDA(At, 1, 0); PG8_STAGE(PG8_SA(0, 1), a2 + hstepA, w1);
;             PG8_WAIT_V(8); PG8_WAIT_L(0); PG8_BAR; PG8_MMA(0, 0, At, B0); PG8_MMA(0, 1, At, B1); PG8_BAR; PG8_SCHED;
	s_setprio 1
	v_mfma_f32_16x16x32_bf16 v[62:65], v[172:175], v[204:207], v[62:65]
	v_mfma_f32_16x16x32_bf16 v[58:61], v[180:183], v[204:207], v[58:61]
	v_mfma_f32_16x16x32_bf16 v[50:53], v[172:175], v[212:215], v[50:53]
	v_mfma_f32_16x16x32_bf16 v[42:45], v[180:183], v[212:215], v[42:45]
	v_mfma_f32_16x16x32_bf16 v[34:37], v[172:175], v[220:223], v[34:37]
	v_mfma_f32_16x16x32_bf16 v[26:29], v[180:183], v[220:223], v[26:29]
	v_mfma_f32_16x16x32_bf16 v[14:17], v[172:175], v[228:231], v[14:17]
	v_mfma_f32_16x16x32_bf16 v[2:5], v[180:183], v[228:231], v[2:5]
	v_mfma_f32_16x16x32_bf16 v[62:65], v[176:179], v[208:211], v[62:65]
	v_mfma_f32_16x16x32_bf16 v[58:61], v[184:187], v[208:211], v[58:61]
	v_mfma_f32_16x16x32_bf16 v[50:53], v[176:179], v[216:219], v[50:53]
	v_mfma_f32_16x16x32_bf16 v[42:45], v[184:187], v[216:219], v[42:45]
	v_mfma_f32_16x16x32_bf16 v[34:37], v[176:179], v[224:227], v[34:37]
	v_mfma_f32_16x16x32_bf16 v[26:29], v[184:187], v[224:227], v[26:29]
	v_mfma_f32_16x16x32_bf16 v[14:17], v[176:179], v[232:235], v[14:17]
	v_mfma_f32_16x16x32_bf16 v[2:5], v[184:187], v[232:235], v[2:5]
	v_mfma_f32_16x16x32_bf16 v[54:57], v[188:191], v[204:207], v[54:57]
	v_mfma_f32_16x16x32_bf16 v[46:49], v[196:199], v[204:207], v[46:49]
	v_mfma_f32_16x16x32_bf16 v[38:41], v[188:191], v[212:215], v[38:41]
	v_mfma_f32_16x16x32_bf16 v[30:33], v[196:199], v[212:215], v[30:33]
	v_mfma_f32_16x16x32_bf16 v[22:25], v[188:191], v[220:223], v[22:25]
	v_mfma_f32_16x16x32_bf16 v[18:21], v[196:199], v[220:223], v[18:21]
	v_mfma_f32_16x16x32_bf16 v[10:13], v[188:191], v[228:231], v[10:13]
	v_mfma_f32_16x16x32_bf16 v[6:9], v[196:199], v[228:231], v[6:9]
	v_mfma_f32_16x16x32_bf16 v[54:57], v[192:195], v[208:211], v[54:57]
	v_mfma_f32_16x16x32_bf16 v[46:49], v[200:203], v[208:211], v[46:49]
	v_mfma_f32_16x16x32_bf16 v[38:41], v[192:195], v[216:219], v[38:41]
	v_mfma_f32_16x16x32_bf16 v[30:33], v[200:203], v[216:219], v[30:33]
	v_mfma_f32_16x16x32_bf16 v[22:25], v[192:195], v[224:227], v[22:25]
	v_mfma_f32_16x16x32_bf16 v[18:21], v[200:203], v[224:227], v[18:21]
	v_mfma_f32_16x16x32_bf16 v[10:13], v[192:195], v[232:235], v[10:13]
	v_mfma_f32_16x16x32_bf16 v[6:9], v[200:203], v[232:235], v[6:9]
	s_setprio 0
	s_barrier
	ds_read_b128 v[172:175], v170
	ds_read_b128 v[176:179], v170 offset:1024
	ds_read_b128 v[180:183], v170 offset:2048
	ds_read_b128 v[184:187], v170 offset:3072
	ds_read_b128 v[188:191], v171
	ds_read_b128 v[192:195], v171 offset:1024
	ds_read_b128 v[196:199], v171 offset:2048
	ds_read_b128 v[200:203], v171 offset:3072
	s_mov_b32 m0, s27
	v_lshl_add_u64 v[244:245], s[18:19], 0, v[152:153]
	ds_read_b128 v[204:207], v169 offset:32768
	ds_read_b128 v[208:211], v169 offset:33792
	ds_read_b128 v[212:215], v169 offset:34816
	ds_read_b128 v[216:219], v169 offset:35840
	ds_read_b128 v[220:223], v169 offset:36864
	ds_read_b128 v[224:227], v169 offset:37888
	ds_read_b128 v[228:231], v169 offset:38912
	ds_read_b128 v[232:235], v169 offset:39936
	global_load_lds_dwordx4 v[244:245], off
	v_lshl_add_u64 v[244:245], s[18:19], 0, v[154:155]
	s_mov_b32 m0, s35
	s_nop 0
	global_load_lds_dwordx4 v[244:245], off
	s_waitcnt vmcnt(8)
	s_waitcnt lgkmcnt(0)
	s_barrier
	s_setprio 1
	v_mfma_f32_16x16x32_bf16 v[126:129], v[172:175], v[204:207], v[126:129]
	v_mfma_f32_16x16x32_bf16 v[122:125], v[180:183], v[204:207], v[122:125]
	v_mfma_f32_16x16x32_bf16 v[110:113], v[172:175], v[212:215], v[110:113]
	v_mfma_f32_16x16x32_bf16 v[106:109], v[180:183], v[212:215], v[106:109]
	v_mfma_f32_16x16x32_bf16 v[94:97], v[172:175], v[220:223], v[94:97]
	v_mfma_f32_16x16x32_bf16 v[90:93], v[180:183], v[220:223], v[90:93]
	v_mfma_f32_16x16x32_bf16 v[78:81], v[172:175], v[228:231], v[78:81]
	v_mfma_f32_16x16x32_bf16 v[74:77], v[180:183], v[228:231], v[74:77]
	v_mfma_f32_16x16x32_bf16 v[126:129], v[176:179], v[208:211], v[126:129]
	v_mfma_f32_16x16x32_bf16 v[122:125], v[184:187], v[208:211], v[122:125]
	v_mfma_f32_16x16x32_bf16 v[110:113], v[176:179], v[216:219], v[110:113]
	v_mfma_f32_16x16x32_bf16 v[106:109], v[184:187], v[216:219], v[106:109]
	v_mfma_f32_16x16x32_bf16 v[94:97], v[176:179], v[224:227], v[94:97]
	v_mfma_f32_16x16x32_bf16 v[90:93], v[184:187], v[224:227], v[90:93]
	v_mfma_f32_16x16x32_bf16 v[78:81], v[176:179], v[232:235], v[78:81]
	v_mfma_f32_16x16x32_bf16 v[74:77], v[184:187], v[232:235], v[74:77]
	v_mfma_f32_16x16x32_bf16 v[118:121], v[188:191], v[204:207], v[118:121]
	v_mfma_f32_16x16x32_bf16 v[114:117], v[196:199], v[204:207], v[114:117]
	v_mfma_f32_16x16x32_bf16 v[102:105], v[188:191], v[212:215], v[102:105]
	v_mfma_f32_16x16x32_bf16 v[98:101], v[196:199], v[212:215], v[98:101]
	v_mfma_f32_16x16x32_bf16 v[86:89], v[188:191], v[220:223], v[86:89]
	v_mfma_f32_16x16x32_bf16 v[82:85], v[196:199], v[220:223], v[82:85]
	v_mfma_f32_16x16x32_bf16 v[70:73], v[188:191], v[228:231], v[70:73]
	v_mfma_f32_16x16x32_bf16 v[66:69], v[196:199], v[228:231], v[66:69]
	v_mfma_f32_16x16x32_bf16 v[118:121], v[192:195], v[208:211], v[118:121]
	v_mfma_f32_16x16x32_bf16 v[114:117], v[200:203], v[208:211], v[114:117]
	v_mfma_f32_16x16x32_bf16 v[102:105], v[192:195], v[216:219], v[102:105]
	v_mfma_f32_16x16x32_bf16 v[98:101], v[200:203], v[216:219], v[98:101]
	v_mfma_f32_16x16x32_bf16 v[86:89], v[192:195], v[224:227], v[86:89]
	v_mfma_f32_16x16x32_bf16 v[82:85], v[200:203], v[224:227], v[82:85]
	v_mfma_f32_16x16x32_bf16 v[70:73], v[192:195], v[232:235], v[70:73]
	v_mfma_f32_16x16x32_bf16 v[66:69], v[200:203], v[232:235], v[66:69]
	s_setprio 0
	s_barrier
; #define PG8_STAGE(bufoff, gbase, voff) do { _Pragma("unroll") for (int _i = 0; _i < 2; ++_i) \
;         __builtin_amdgcn_global_load_lds((const unsigned*)((const char*)(gbase) + (voff)[_i]), (PG8_LAS unsigned*)(lds + (bufoff) + ldsw + _i * 8192), 16, 0, 0); } while (0)
; #define PG8_LDA(dst, b, h) do { _Pragma("unroll") for (int m = 0; m < 4; ++m) _Pragma("unroll") for (int k = 0; k < 2; ++k) dst[m][k] = *(const PG8_LAS bf16x8*)(lds + PG8_SA(b, h) + aoff + m * 2048 + k * 1024); } while (0)
; #define PG8_MMA(ai, bj, At, Bt) do { __builtin_amdgcn_s_setprio(1); _Pragma("unroll") for (int m = 0; m < 4; ++m) _Pragma("unroll") for (int n = 0; n < 2; ++n) _Pragma("unroll") for (int k = 0; k < 2; ++k) \
;         acc[ai][bj][m][n] = __builtin_amdgcn_mfma_f32_16x16x32_bf16(Bt[n][k], At[m][k], acc[ai][bj][m][n], 0, 0, 0); __builtin_amdgcn_s_setprio(0); } while (0)
; #define PG8_WAIT_V(n) asm volatile("s_waitcnt vmcnt(" #n ")" ::: "memory")
; #define PG8_WAIT_L(n) asm volatile("s_waitcnt lgkmcnt(" #n ")" ::: "memory")
; #define PG8_BAR __builtin_amdgcn_s_barrier()
; #define PG8_SCHED __builtin_amdgcn_sched_barrier(0)
; template <class Epi, class Sched, bool ALIGN_EPI = false>
; __device__ __forceinline__ void gemm_phase(PG8_LAS unsigned char* lds, const Gemm g, const Sched& S, const Epi& E) {
;     ...
;             PG8_LDA(At, 1, 1); PG8_STAGE(PG8_SB(1, 0), b3, voffB); PG8_STAGE(PG8_SB(1, 1), b3 + hstep, voffB); PG8_STAGE(PG8_SA(1, 0), a3, w0);
;             PG8_WAIT_V(8); PG8_WAIT_L(0); PG8_BAR; PG8_MMA(1, 0, At, B0); PG8_MMA(1, 1, At, B1); PG8_BAR; PG8_SCHED;
;             if constexpr (Epi::KSCALE) { if (((t + 2) & 7) == 0 && t + 2 < nt) { E.kscale(acc, pf, ((t + 2) >> 3) - 1, wr, fr); PG8_SCHED; } }
;         }
;         if constexpr (ALIGN_EPI) { if (wr == 0) PG8_BAR; }
	s_mov_b32 m0, s52
	v_lshl_add_u64 v[236:237], v[236:237], 0, s[12:13]
	s_add_u32 s16, s16, 0x80080
	ds_read_b128 v[204:207], v169 offset:49152
	ds_read_b128 v[208:211], v169 offset:50176
	ds_read_b128 v[212:215], v169 offset:51200
	ds_read_b128 v[216:219], v169 offset:52224
	ds_read_b128 v[220:223], v169 offset:53248
	ds_read_b128 v[224:227], v169 offset:54272
	ds_read_b128 v[228:231], v169 offset:55296
	ds_read_b128 v[232:235], v169 offset:56320
	global_load_lds_dwordx4 v[236:237], off
	v_lshl_add_u64 v[236:237], v[238:239], 0, s[12:13]
	s_mov_b32 m0, s53
	s_addc_u32 s17, s17, 0
	global_load_lds_dwordx4 v[236:237], off
	v_lshl_add_u64 v[236:237], s[16:17], 0, v[146:147]
	s_mov_b32 m0, s54
	s_nop 0
	global_load_lds_dwordx4 v[236:237], off
	v_lshl_add_u64 v[236:237], s[16:17], 0, v[144:145]
	s_mov_b32 m0, s55
	s_nop 0
	global_load_lds_dwordx4 v[236:237], off
	v_lshl_add_u64 v[236:237], v[240:241], 0, s[12:13]
	s_mov_b32 m0, s41
	s_nop 0
	global_load_lds_dwordx4 v[236:237], off
	v_lshl_add_u64 v[236:237], v[242:243], 0, s[12:13]
	s_mov_b32 m0, s42
	s_nop 0
	global_load_lds_dwordx4 v[236:237], off
	s_waitcnt vmcnt(8)
	s_waitcnt lgkmcnt(0)
	s_barrier
	s_setprio 1
	v_mfma_f32_16x16x32_bf16 v[62:65], v[172:175], v[204:207], v[62:65]
	v_mfma_f32_16x16x32_bf16 v[58:61], v[180:183], v[204:207], v[58:61]
	v_mfma_f32_16x16x32_bf16 v[50:53], v[172:175], v[212:215], v[50:53]
	v_mfma_f32_16x16x32_bf16 v[42:45], v[180:183], v[212:215], v[42:45]
	v_mfma_f32_16x16x32_bf16 v[34:37], v[172:175], v[220:223], v[34:37]
	v_mfma_f32_16x16x32_bf16 v[26:29], v[180:183], v[220:223], v[26:29]
	v_mfma_f32_16x16x32_bf16 v[14:17], v[172:175], v[228:231], v[14:17]
	v_mfma_f32_16x16x32_bf16 v[2:5], v[180:183], v[228:231], v[2:5]
	v_mfma_f32_16x16x32_bf16 v[62:65], v[176:179], v[208:211], v[62:65]
	v_mfma_f32_16x16x32_bf16 v[58:61], v[184:187], v[208:211], v[58:61]
	v_mfma_f32_16x16x32_bf16 v[50:53], v[176:179], v[216:219], v[50:53]
	v_mfma_f32_16x16x32_bf16 v[42:45], v[184:187], v[216:219], v[42:45]
	v_mfma_f32_16x16x32_bf16 v[34:37], v[176:179], v[224:227], v[34:37]
	v_mfma_f32_16x16x32_bf16 v[26:29], v[184:187], v[224:227], v[26:29]
	v_mfma_f32_16x16x32_bf16 v[14:17], v[176:179], v[232:235], v[14:17]
	v_mfma_f32_16x16x32_bf16 v[2:5], v[184:187], v[232:235], v[2:5]
	v_mfma_f32_16x16x32_bf16 v[54:57], v[188:191], v[204:207], v[54:57]
	v_mfma_f32_16x16x32_bf16 v[46:49], v[196:199], v[204:207], v[46:49]
	v_mfma_f32_16x16x32_bf16 v[38:41], v[188:191], v[212:215], v[38:41]
	v_mfma_f32_16x16x32_bf16 v[30:33], v[196:199], v[212:215], v[30:33]
	v_mfma_f32_16x16x32_bf16 v[22:25], v[188:191], v[220:223], v[22:25]
	v_mfma_f32_16x16x32_bf16 v[18:21], v[196:199], v[220:223], v[18:21]
	v_mfma_f32_16x16x32_bf16 v[10:13], v[188:191], v[228:231], v[10:13]
	v_mfma_f32_16x16x32_bf16 v[6:9], v[196:199], v[228:231], v[6:9]
	v_mfma_f32_16x16x32_bf16 v[54:57], v[192:195], v[208:211], v[54:57]
	v_mfma_f32_16x16x32_bf16 v[46:49], v[200:203], v[208:211], v[46:49]
	v_mfma_f32_16x16x32_bf16 v[38:41], v[192:195], v[216:219], v[38:41]
	v_mfma_f32_16x16x32_bf16 v[30:33], v[200:203], v[216:219], v[30:33]
	v_mfma_f32_16x16x32_bf16 v[22:25], v[192:195], v[224:227], v[22:25]
	v_mfma_f32_16x16x32_bf16 v[18:21], v[200:203], v[224:227], v[18:21]
	v_mfma_f32_16x16x32_bf16 v[10:13], v[192:195], v[232:235], v[10:13]
	v_mfma_f32_16x16x32_bf16 v[6:9], v[200:203], v[232:235], v[6:9]
	s_setprio 0
	s_barrier
	s_add_i32 s45, s45, 2
	s_add_u32 s14, s14, 0x100
	s_addc_u32 s15, s15, 0
	s_cmp_gt_u32 s45, 29
	s_cbranch_scc0 .LBB0_1480
	s_cmpk_lt_u32 s22, 0x100
	s_cbranch_scc0 .LBB0_1483
	s_barrier

; #define PG8_STAGE(bufoff, gbase, voff) do { _Pragma("unroll") for (int _i = 0; _i < 2; ++_i) \
;         __builtin_amdgcn_global_load_lds((const unsigned*)((const char*)(gbase) + (voff)[_i]), (PG8_LAS unsigned*)(lds + (bufoff) + ldsw + _i * 8192), 16, 0, 0); } while (0)
; #define PG8_LDA(dst, b, h) do { _Pragma("unroll") for (int m = 0; m < 4; ++m) _Pragma("unroll") for (int k = 0; k < 2; ++k) dst[m][k] = *(const PG8_LAS bf16x8*)(lds + PG8_SA(b, h) + aoff + m * 2048 + k * 1024); } while (0)
; #define PG8_LDB(dst, b, h) do { _Pragma("unroll") for (int n = 0; n < 2; ++n) _Pragma("unroll") for (int k = 0; k < 2; ++k) dst[n][k] = *(const PG8_LAS bf16x8*)(lds + PG8_SB(b, h) + boff + n * 2048 + k * 1024); } while (0)
; #define PG8_MMA(ai, bj, At, Bt) do { __builtin_amdgcn_s_setprio(1); _Pragma("unroll") for (int m = 0; m < 4; ++m) _Pragma("unroll") for (int n = 0; n < 2; ++n) _Pragma("unroll") for (int k = 0; k < 2; ++k) \
;         acc[ai][bj][m][n] = __builtin_amdgcn_mfma_f32_16x16x32_bf16(Bt[n][k], At[m][k], acc[ai][bj][m][n], 0, 0, 0); __builtin_amdgcn_s_setprio(0); } while (0)
; template <class Epi, class Sched, bool ALIGN_EPI = false>
; __device__ __forceinline__ void gemm_phase(PG8_LAS unsigned char* lds, const Gemm g, const Sched& S, const Epi& E) {
;     ...
;         for (int t = 0; t < nt; t += 2) {
;             const bool last = (t == nt - 2);
;             const char* a1 = cA + (size_t)(t + 1) * kstep;
;             const char* a2 = last ? nA : cA + (size_t)(t + 2) * kstep; const char* b2 = last ? nB : cB + (size_t)(t + 2) * kstep;
;             const char* a3 = a2 + kstep; const char* b3 = b2 + kstep;
;             unsigned w0[2], w1[2];
; #pragma unroll
;             for (int i = 0; i < 2; ++i) { w0[i] = (Sched::GATHER && last) ? vn0[i] : vc0[i]; w1[i] = (Sched::GATHER && last) ? vn1[i] : vc1[i]; }
;             if (last && has_next) S.a_ready(nxt);
;             PG8_LDB(B0, 0, 0); PG8_LDB(B1, 0, 1); PG8_SCHED; PG8_LDA(At, 0, 0); PG8_STAGE(PG8_SA(1, 1), a1 + hstepA, vc1);
;             PG8_WAIT_V(8); PG8_WAIT_L(0); PG8_BAR; PG8_MMA(0, 0, At, B0); PG8_MMA(0, 1, At, B1); PG8_BAR; PG8_SCHED;
;             PG8_LDA(At, 0, 1); PG8_STAGE(PG8_SB(0, 0), b2, voffB); PG8_STAGE(PG8_SB(0, 1), b2 + hstep, voffB); PG8_STAGE(PG8_SA(0, 0), a2, w0);
;             PG8_WAIT_V(8); PG8_WAIT_L(0); PG8_BAR; PG8_MMA(1, 0, At, B0); PG8_MMA(1, 1, At, B1); PG8_BAR; PG8_SCHED;
.LBB0_1498:
	ds_read_b128 v[142:145], v1
	ds_read_b128 v[158:161], v1 offset:1024
	ds_read_b128 v[162:165], v1 offset:2048
	ds_read_b128 v[166:169], v1 offset:3072
	ds_read_b128 v[170:173], v156
	ds_read_b128 v[174:177], v156 offset:1024
	ds_read_b128 v[178:181], v156 offset:2048
	ds_read_b128 v[182:185], v156 offset:3072
	s_add_u32 s58, s56, 0xfffe0080
	s_addc_u32 s59, s57, -1
	s_cmp_eq_u32 s87, 4
	s_cselect_b32 s61, s41, s59
	s_cselect_b32 s60, s53, s58
	s_cselect_b32 s59, s43, s86
	s_cselect_b32 s58, s84, s85
	v_lshl_add_u64 v[218:219], s[56:57], 0, v[140:141]
	s_add_i32 m0, s55, 0xc000
	ds_read_b128 v[186:189], v157
	ds_read_b128 v[190:193], v157 offset:1024
	ds_read_b128 v[194:197], v157 offset:2048
	ds_read_b128 v[198:201], v157 offset:3072
	ds_read_b128 v[202:205], v157 offset:4096
	ds_read_b128 v[206:209], v157 offset:5120
	ds_read_b128 v[210:213], v157 offset:6144
	ds_read_b128 v[214:217], v157 offset:7168
	global_load_lds_dwordx4 v[218:219], off
	v_lshl_add_u64 v[218:219], s[56:57], 0, v[138:139]
	s_add_i32 m0, s55, 0xe000
	s_nop 0
	global_load_lds_dwordx4 v[218:219], off
	s_waitcnt vmcnt(8)
	s_waitcnt lgkmcnt(0)
	s_barrier
	s_setprio 1
	v_mfma_f32_16x16x32_bf16 v[126:129], v[142:145], v[186:189], v[126:129]
	v_mfma_f32_16x16x32_bf16 v[122:125], v[162:165], v[186:189], v[122:125]
	v_mfma_f32_16x16x32_bf16 v[114:117], v[142:145], v[194:197], v[114:117]
	v_mfma_f32_16x16x32_bf16 v[106:109], v[162:165], v[194:197], v[106:109]
	v_mfma_f32_16x16x32_bf16 v[98:101], v[142:145], v[202:205], v[98:101]
	v_mfma_f32_16x16x32_bf16 v[90:93], v[162:165], v[202:205], v[90:93]
	v_mfma_f32_16x16x32_bf16 v[82:85], v[142:145], v[210:213], v[82:85]
	v_mfma_f32_16x16x32_bf16 v[74:77], v[162:165], v[210:213], v[74:77]
	v_mfma_f32_16x16x32_bf16 v[126:129], v[158:161], v[190:193], v[126:129]
	v_mfma_f32_16x16x32_bf16 v[122:125], v[166:169], v[190:193], v[122:125]
	v_mfma_f32_16x16x32_bf16 v[114:117], v[158:161], v[198:201], v[114:117]
	v_mfma_f32_16x16x32_bf16 v[106:109], v[166:169], v[198:201], v[106:109]
	v_mfma_f32_16x16x32_bf16 v[98:101], v[158:161], v[206:209], v[98:101]
	v_mfma_f32_16x16x32_bf16 v[90:93], v[166:169], v[206:209], v[90:93]
	v_mfma_f32_16x16x32_bf16 v[82:85], v[158:161], v[214:217], v[82:85]
	v_mfma_f32_16x16x32_bf16 v[74:77], v[166:169], v[214:217], v[74:77]
	v_mfma_f32_16x16x32_bf16 v[118:121], v[170:173], v[186:189], v[118:121]
	v_mfma_f32_16x16x32_bf16 v[110:113], v[178:181], v[186:189], v[110:113]
	v_mfma_f32_16x16x32_bf16 v[102:105], v[170:173], v[194:197], v[102:105]
	v_mfma_f32_16x16x32_bf16 v[94:97], v[178:181], v[194:197], v[94:97]
	v_mfma_f32_16x16x32_bf16 v[86:89], v[170:173], v[202:205], v[86:89]
	v_mfma_f32_16x16x32_bf16 v[78:81], v[178:181], v[202:205], v[78:81]
	v_mfma_f32_16x16x32_bf16 v[62:65], v[170:173], v[210:213], v[62:65]
	v_mfma_f32_16x16x32_bf16 v[58:61], v[178:181], v[210:213], v[58:61]
	v_mfma_f32_16x16x32_bf16 v[118:121], v[174:177], v[190:193], v[118:121]
	v_mfma_f32_16x16x32_bf16 v[110:113], v[182:185], v[190:193], v[110:113]
	v_mfma_f32_16x16x32_bf16 v[102:105], v[174:177], v[198:201], v[102:105]
	v_mfma_f32_16x16x32_bf16 v[94:97], v[182:185], v[198:201], v[94:97]
	v_mfma_f32_16x16x32_bf16 v[86:89], v[174:177], v[206:209], v[86:89]
	v_mfma_f32_16x16x32_bf16 v[78:81], v[182:185], v[206:209], v[78:81]
	v_mfma_f32_16x16x32_bf16 v[62:65], v[174:177], v[214:217], v[62:65]
	v_mfma_f32_16x16x32_bf16 v[58:61], v[182:185], v[214:217], v[58:61]
	s_setprio 0
	s_barrier
	s_add_i32 s88, s74, s62
	v_lshl_add_u64 v[218:219], s[58:59], 0, v[132:133]
	s_mov_b32 m0, s88
	ds_read_b128 v[186:189], v157 offset:16384
	ds_read_b128 v[190:193], v157 offset:17408
	ds_read_b128 v[194:197], v157 offset:18432
	ds_read_b128 v[198:201], v157 offset:19456
	ds_read_b128 v[202:205], v157 offset:20480
	ds_read_b128 v[206:209], v157 offset:21504
	ds_read_b128 v[210:213], v157 offset:22528
	ds_read_b128 v[214:217], v157 offset:23552
	global_load_lds_dwordx4 v[218:219], off
	s_add_i32 m0, s88, 0x2000
	s_add_u32 s88, s58, 0x20000
	v_lshl_add_u64 v[220:221], s[58:59], 0, v[136:137]
	s_addc_u32 s89, s59, 0
	s_add_i32 s90, s75, s62
	global_load_lds_dwordx4 v[220:221], off
	v_lshl_add_u64 v[222:223], s[88:89], 0, v[132:133]
	s_mov_b32 m0, s90
	v_lshl_add_u64 v[224:225], s[60:61], 0, v[134:135]
	global_load_lds_dwordx4 v[222:223], off
	v_lshl_add_u64 v[222:223], s[88:89], 0, v[136:137]
	s_add_i32 m0, s90, 0x2000
	s_nop 0
	global_load_lds_dwordx4 v[222:223], off
	v_lshl_add_u64 v[222:223], s[60:61], 0, v[130:131]
	s_mov_b32 m0, s55
	s_nop 0
	global_load_lds_dwordx4 v[222:223], off
	s_mov_b32 m0, s63
	s_nop 0
	global_load_lds_dwordx4 v[224:225], off
	s_waitcnt vmcnt(8)
	s_waitcnt lgkmcnt(0)
	s_barrier
; #define PG8_STAGE(bufoff, gbase, voff) do { _Pragma("unroll") for (int _i = 0; _i < 2; ++_i) \
;         __builtin_amdgcn_global_load_lds((const unsigned*)((const char*)(gbase) + (voff)[_i]), (PG8_LAS unsigned*)(lds + (bufoff) + ldsw + _i * 8192), 16, 0, 0); } while (0)
; #define PG8_LDA(dst, b, h) do { _Pragma("unroll") for (int m = 0; m < 4; ++m) _Pragma("unroll") for (int k = 0; k < 2; ++k) dst[m][k] = *(const PG8_LAS bf16x8*)(lds + PG8_SA(b, h) + aoff + m * 2048 + k * 1024); } while (0)
; #define PG8_LDB(dst, b, h) do { _Pragma("unroll") for (int n = 0; n < 2; ++n) _Pragma("unroll") for (int k = 0; k < 2; ++k) dst[n][k] = *(const PG8_LAS bf16x8*)(lds + PG8_SB(b, h) + boff + n * 2048 + k * 1024); } while (0)
; #define PG8_MMA(ai, bj, At, Bt) do { __builtin_amdgcn_s_setprio(1); _Pragma("unroll") for (int m = 0; m < 4; ++m) _Pragma("unroll") for (int n = 0; n < 2; ++n) _Pragma("unroll") for (int k = 0; k < 2; ++k) \
;         acc[ai][bj][m][n] = __builtin_amdgcn_mfma_f32_16x16x32_bf16(Bt[n][k], At[m][k], acc[ai][bj][m][n], 0, 0, 0); __builtin_amdgcn_s_setprio(0); } while (0)
; #define PG8_WAIT_V(n) asm volatile("s_waitcnt vmcnt(" #n ")" ::: "memory")
; #define PG8_WAIT_L(n) asm volatile("s_waitcnt lgkmcnt(" #n ")" ::: "memory")
; #define PG8_BAR __builtin_amdgcn_s_barrier()
; #define PG8_SCHED __builtin_amdgcn_sched_barrier(0)
; template <class Epi, class Sched, bool ALIGN_EPI = false>
; __device__ __forceinline__ void gemm_phase(PG8_LAS unsigned char* lds, const Gemm g, const Sched& S, const Epi& E) {
;     ...
;             PG8_WAIT_V(8); PG8_WAIT_L(0); PG8_BAR; PG8_MMA(1, 0, At, B0); PG8_MMA(1, 1, At, B1); PG8_BAR; PG8_SCHED;
;             PG8_LDB(B0, 1, 0); PG8_LDB(B1, 1, 1); PG8_SCHED; PG8_LDA(At, 1, 0); PG8_STAGE(PG8_SA(0, 1), a2 + hstepA, w1);
;             PG8_WAIT_V(8); PG8_WAIT_L(0); PG8_BAR; PG8_MMA(0, 0, At, B0); PG8_MMA(0, 1, At, B1); PG8_BAR; PG8_SCHED;
	s_setprio 1
	v_mfma_f32_16x16x32_bf16 v[54:57], v[142:145], v[186:189], v[54:57]
	v_mfma_f32_16x16x32_bf16 v[42:45], v[162:165], v[186:189], v[42:45]
	v_mfma_f32_16x16x32_bf16 v[30:33], v[142:145], v[194:197], v[30:33]
	v_mfma_f32_16x16x32_bf16 v[26:29], v[162:165], v[194:197], v[26:29]
	v_mfma_f32_16x16x32_bf16 v[14:17], v[142:145], v[202:205], v[14:17]
	v_mfma_f32_16x16x32_bf16 v[10:13], v[162:165], v[202:205], v[10:13]
	v_mfma_f32_16x16x32_bf16 v[6:9], v[142:145], v[210:213], v[6:9]
	v_mfma_f32_16x16x32_bf16 v[2:5], v[162:165], v[210:213], v[2:5]
	v_mfma_f32_16x16x32_bf16 v[54:57], v[158:161], v[190:193], v[54:57]
	v_mfma_f32_16x16x32_bf16 v[42:45], v[166:169], v[190:193], v[42:45]
	v_mfma_f32_16x16x32_bf16 v[30:33], v[158:161], v[198:201], v[30:33]
	v_mfma_f32_16x16x32_bf16 v[26:29], v[166:169], v[198:201], v[26:29]
	v_mfma_f32_16x16x32_bf16 v[14:17], v[158:161], v[206:209], v[14:17]
	v_mfma_f32_16x16x32_bf16 v[10:13], v[166:169], v[206:209], v[10:13]
	v_mfma_f32_16x16x32_bf16 v[6:9], v[158:161], v[214:217], v[6:9]
	v_mfma_f32_16x16x32_bf16 v[2:5], v[166:169], v[214:217], v[2:5]
	v_mfma_f32_16x16x32_bf16 v[70:73], v[170:173], v[186:189], v[70:73]
	v_mfma_f32_16x16x32_bf16 v[66:69], v[178:181], v[186:189], v[66:69]
	v_mfma_f32_16x16x32_bf16 v[50:53], v[170:173], v[194:197], v[50:53]
	v_mfma_f32_16x16x32_bf16 v[46:49], v[178:181], v[194:197], v[46:49]
	v_mfma_f32_16x16x32_bf16 v[38:41], v[170:173], v[202:205], v[38:41]
	v_mfma_f32_16x16x32_bf16 v[34:37], v[178:181], v[202:205], v[34:37]
	v_mfma_f32_16x16x32_bf16 v[22:25], v[170:173], v[210:213], v[22:25]
	v_mfma_f32_16x16x32_bf16 v[18:21], v[178:181], v[210:213], v[18:21]
	v_mfma_f32_16x16x32_bf16 v[70:73], v[174:177], v[190:193], v[70:73]
	v_mfma_f32_16x16x32_bf16 v[66:69], v[182:185], v[190:193], v[66:69]
	v_mfma_f32_16x16x32_bf16 v[50:53], v[174:177], v[198:201], v[50:53]
	v_mfma_f32_16x16x32_bf16 v[46:49], v[182:185], v[198:201], v[46:49]
	v_mfma_f32_16x16x32_bf16 v[38:41], v[174:177], v[206:209], v[38:41]
	v_mfma_f32_16x16x32_bf16 v[34:37], v[182:185], v[206:209], v[34:37]
	v_mfma_f32_16x16x32_bf16 v[22:25], v[174:177], v[214:217], v[22:25]
	v_mfma_f32_16x16x32_bf16 v[18:21], v[182:185], v[214:217], v[18:21]
	s_setprio 0
	s_barrier
	s_add_i32 s88, 0, 0x18000
	s_add_i32 s89, 0, 0x1c000
	v_add_u32_e32 v166, s88, v147
	v_add_u32_e32 v182, s89, v147
	ds_read_b128 v[142:145], v166
	ds_read_b128 v[158:161], v166 offset:1024
	ds_read_b128 v[162:165], v166 offset:2048
	ds_read_b128 v[166:169], v166 offset:3072
	ds_read_b128 v[170:173], v182
	ds_read_b128 v[174:177], v182 offset:1024
	ds_read_b128 v[178:181], v182 offset:2048
	ds_read_b128 v[182:185], v182 offset:3072
	s_add_u32 s60, s60, 0x20000
	s_addc_u32 s61, s61, 0
	s_mov_b32 m0, s64
	v_lshl_add_u64 v[226:227], s[60:61], 0, v[130:131]
	ds_read_b128 v[186:189], v157 offset:32768
	ds_read_b128 v[190:193], v157 offset:33792
	ds_read_b128 v[194:197], v157 offset:34816
	ds_read_b128 v[198:201], v157 offset:35840
	ds_read_b128 v[202:205], v157 offset:36864
	ds_read_b128 v[206:209], v157 offset:37888
	ds_read_b128 v[210:213], v157 offset:38912
	ds_read_b128 v[214:217], v157 offset:39936
	global_load_lds_dwordx4 v[226:227], off
	v_lshl_add_u64 v[226:227], s[60:61], 0, v[134:135]
	s_mov_b32 m0, s65
	s_nop 0
	global_load_lds_dwordx4 v[226:227], off
	s_waitcnt vmcnt(8)
	s_waitcnt lgkmcnt(0)
	s_barrier
	s_setprio 1
	v_mfma_f32_16x16x32_bf16 v[126:129], v[142:145], v[186:189], v[126:129]
	v_mfma_f32_16x16x32_bf16 v[122:125], v[162:165], v[186:189], v[122:125]
	v_mfma_f32_16x16x32_bf16 v[114:117], v[142:145], v[194:197], v[114:117]
	v_mfma_f32_16x16x32_bf16 v[106:109], v[162:165], v[194:197], v[106:109]
	v_mfma_f32_16x16x32_bf16 v[98:101], v[142:145], v[202:205], v[98:101]
	v_mfma_f32_16x16x32_bf16 v[90:93], v[162:165], v[202:205], v[90:93]
	v_mfma_f32_16x16x32_bf16 v[82:85], v[142:145], v[210:213], v[82:85]
	v_mfma_f32_16x16x32_bf16 v[74:77], v[162:165], v[210:213], v[74:77]
	v_mfma_f32_16x16x32_bf16 v[126:129], v[158:161], v[190:193], v[126:129]
	v_mfma_f32_16x16x32_bf16 v[122:125], v[166:169], v[190:193], v[122:125]
	v_mfma_f32_16x16x32_bf16 v[114:117], v[158:161], v[198:201], v[114:117]
	v_mfma_f32_16x16x32_bf16 v[106:109], v[166:169], v[198:201], v[106:109]
	v_mfma_f32_16x16x32_bf16 v[98:101], v[158:161], v[206:209], v[98:101]
	v_mfma_f32_16x16x32_bf16 v[90:93], v[166:169], v[206:209], v[90:93]
	v_mfma_f32_16x16x32_bf16 v[82:85], v[158:161], v[214:217], v[82:85]
	v_mfma_f32_16x16x32_bf16 v[74:77], v[166:169], v[214:217], v[74:77]
	v_mfma_f32_16x16x32_bf16 v[118:121], v[170:173], v[186:189], v[118:121]
	v_mfma_f32_16x16x32_bf16 v[110:113], v[178:181], v[186:189], v[110:113]
	v_mfma_f32_16x16x32_bf16 v[102:105], v[170:173], v[194:197], v[102:105]
	v_mfma_f32_16x16x32_bf16 v[94:97], v[178:181], v[194:197], v[94:97]
	v_mfma_f32_16x16x32_bf16 v[86:89], v[170:173], v[202:205], v[86:89]
	v_mfma_f32_16x16x32_bf16 v[78:81], v[178:181], v[202:205], v[78:81]
	v_mfma_f32_16x16x32_bf16 v[62:65], v[170:173], v[210:213], v[62:65]
	v_mfma_f32_16x16x32_bf16 v[58:61], v[178:181], v[210:213], v[58:61]
	v_mfma_f32_16x16x32_bf16 v[118:121], v[174:177], v[190:193], v[118:121]
	v_mfma_f32_16x16x32_bf16 v[110:113], v[182:185], v[190:193], v[110:113]
	v_mfma_f32_16x16x32_bf16 v[102:105], v[174:177], v[198:201], v[102:105]
	v_mfma_f32_16x16x32_bf16 v[94:97], v[182:185], v[198:201], v[94:97]
	v_mfma_f32_16x16x32_bf16 v[86:89], v[174:177], v[206:209], v[86:89]
	v_mfma_f32_16x16x32_bf16 v[78:81], v[182:185], v[206:209], v[78:81]
	v_mfma_f32_16x16x32_bf16 v[62:65], v[174:177], v[214:217], v[62:65]
	v_mfma_f32_16x16x32_bf16 v[58:61], v[182:185], v[214:217], v[58:61]
	s_setprio 0
	s_barrier
; #define PG8_STAGE(bufoff, gbase, voff) do { _Pragma("unroll") for (int _i = 0; _i < 2; ++_i) \
;         __builtin_amdgcn_global_load_lds((const unsigned*)((const char*)(gbase) + (voff)[_i]), (PG8_LAS unsigned*)(lds + (bufoff) + ldsw + _i * 8192), 16, 0, 0); } while (0)
; #define PG8_LDA(dst, b, h) do { _Pragma("unroll") for (int m = 0; m < 4; ++m) _Pragma("unroll") for (int k = 0; k < 2; ++k) dst[m][k] = *(const PG8_LAS bf16x8*)(lds + PG8_SA(b, h) + aoff + m * 2048 + k * 1024); } while (0)
; #define PG8_MMA(ai, bj, At, Bt) do { __builtin_amdgcn_s_setprio(1); _Pragma("unroll") for (int m = 0; m < 4; ++m) _Pragma("unroll") for (int n = 0; n < 2; ++n) _Pragma("unroll") for (int k = 0; k < 2; ++k) \
;         acc[ai][bj][m][n] = __builtin_amdgcn_mfma_f32_16x16x32_bf16(Bt[n][k], At[m][k], acc[ai][bj][m][n], 0, 0, 0); __builtin_amdgcn_s_setprio(0); } while (0)
; #define PG8_WAIT_V(n) asm volatile("s_waitcnt vmcnt(" #n ")" ::: "memory")
; #define PG8_WAIT_L(n) asm volatile("s_waitcnt lgkmcnt(" #n ")" ::: "memory")
; #define PG8_BAR __builtin_amdgcn_s_barrier()
; #define PG8_SCHED __builtin_amdgcn_sched_barrier(0)
; template <class Epi, class Sched, bool ALIGN_EPI = false>
; __device__ __forceinline__ void gemm_phase(PG8_LAS unsigned char* lds, const Gemm g, const Sched& S, const Epi& E) {
;     ...
;             PG8_LDA(At, 1, 1); PG8_STAGE(PG8_SB(1, 0), b3, voffB); PG8_STAGE(PG8_SB(1, 1), b3 + hstep, voffB); PG8_STAGE(PG8_SA(1, 0), a3, w0);
;             PG8_WAIT_V(8); PG8_WAIT_L(0); PG8_BAR; PG8_MMA(1, 0, At, B0); PG8_MMA(1, 1, At, B1); PG8_BAR; PG8_SCHED;
;             if constexpr (Epi::KSCALE) { if (((t + 2) & 7) == 0 && t + 2 < nt) { E.kscale(acc, pf, ((t + 2) >> 3) - 1, wr, fr); PG8_SCHED; } }
;         }
;         if constexpr (ALIGN_EPI) { if (wr == 0) PG8_BAR; }
	s_add_i32 s60, s88, s62
	v_lshl_add_u64 v[218:219], v[218:219], 0, s[16:17]
	s_mov_b32 m0, s60
	ds_read_b128 v[186:189], v157 offset:49152
	ds_read_b128 v[190:193], v157 offset:50176
	ds_read_b128 v[194:197], v157 offset:51200
	ds_read_b128 v[198:201], v157 offset:52224
	ds_read_b128 v[202:205], v157 offset:53248
	ds_read_b128 v[206:209], v157 offset:54272
	ds_read_b128 v[210:213], v157 offset:55296
	ds_read_b128 v[214:217], v157 offset:56320
	global_load_lds_dwordx4 v[218:219], off
	s_add_i32 m0, s60, 0x2000
	s_add_u32 s58, s58, 0x20080
	v_lshl_add_u64 v[218:219], v[220:221], 0, s[16:17]
	s_addc_u32 s59, s59, 0
	s_add_i32 s60, s89, s62
	global_load_lds_dwordx4 v[218:219], off
	v_lshl_add_u64 v[218:219], s[58:59], 0, v[132:133]
	s_mov_b32 m0, s60
	s_nop 0
	global_load_lds_dwordx4 v[218:219], off
	v_lshl_add_u64 v[218:219], s[58:59], 0, v[136:137]
	s_add_i32 m0, s60, 0x2000
	s_nop 0
	global_load_lds_dwordx4 v[218:219], off
	v_lshl_add_u64 v[218:219], v[222:223], 0, s[16:17]
	s_mov_b32 m0, s67
	s_nop 0
	global_load_lds_dwordx4 v[218:219], off
	v_lshl_add_u64 v[218:219], v[224:225], 0, s[16:17]
	s_mov_b32 m0, s68
	s_nop 0
	global_load_lds_dwordx4 v[218:219], off
	s_waitcnt vmcnt(8)
	s_waitcnt lgkmcnt(0)
	s_barrier
	s_setprio 1
	v_mfma_f32_16x16x32_bf16 v[54:57], v[142:145], v[186:189], v[54:57]
	v_mfma_f32_16x16x32_bf16 v[42:45], v[162:165], v[186:189], v[42:45]
	v_mfma_f32_16x16x32_bf16 v[30:33], v[142:145], v[194:197], v[30:33]
	v_mfma_f32_16x16x32_bf16 v[26:29], v[162:165], v[194:197], v[26:29]
	v_mfma_f32_16x16x32_bf16 v[14:17], v[142:145], v[202:205], v[14:17]
	v_mfma_f32_16x16x32_bf16 v[10:13], v[162:165], v[202:205], v[10:13]
	v_mfma_f32_16x16x32_bf16 v[6:9], v[142:145], v[210:213], v[6:9]
	v_mfma_f32_16x16x32_bf16 v[2:5], v[162:165], v[210:213], v[2:5]
	v_mfma_f32_16x16x32_bf16 v[54:57], v[158:161], v[190:193], v[54:57]
	v_mfma_f32_16x16x32_bf16 v[42:45], v[166:169], v[190:193], v[42:45]
	v_mfma_f32_16x16x32_bf16 v[30:33], v[158:161], v[198:201], v[30:33]
	v_mfma_f32_16x16x32_bf16 v[26:29], v[166:169], v[198:201], v[26:29]
	v_mfma_f32_16x16x32_bf16 v[14:17], v[158:161], v[206:209], v[14:17]
	v_mfma_f32_16x16x32_bf16 v[10:13], v[166:169], v[206:209], v[10:13]
	v_mfma_f32_16x16x32_bf16 v[6:9], v[158:161], v[214:217], v[6:9]
	v_mfma_f32_16x16x32_bf16 v[2:5], v[166:169], v[214:217], v[2:5]
	v_mfma_f32_16x16x32_bf16 v[70:73], v[170:173], v[186:189], v[70:73]
	v_mfma_f32_16x16x32_bf16 v[66:69], v[178:181], v[186:189], v[66:69]
	v_mfma_f32_16x16x32_bf16 v[50:53], v[170:173], v[194:197], v[50:53]
	v_mfma_f32_16x16x32_bf16 v[46:49], v[178:181], v[194:197], v[46:49]
	v_mfma_f32_16x16x32_bf16 v[38:41], v[170:173], v[202:205], v[38:41]
	v_mfma_f32_16x16x32_bf16 v[34:37], v[178:181], v[202:205], v[34:37]
	v_mfma_f32_16x16x32_bf16 v[22:25], v[170:173], v[210:213], v[22:25]
	v_mfma_f32_16x16x32_bf16 v[18:21], v[178:181], v[210:213], v[18:21]
	v_mfma_f32_16x16x32_bf16 v[70:73], v[174:177], v[190:193], v[70:73]
	v_mfma_f32_16x16x32_bf16 v[66:69], v[182:185], v[190:193], v[66:69]
	v_mfma_f32_16x16x32_bf16 v[50:53], v[174:177], v[198:201], v[50:53]
	v_mfma_f32_16x16x32_bf16 v[46:49], v[182:185], v[198:201], v[46:49]
	v_mfma_f32_16x16x32_bf16 v[38:41], v[174:177], v[206:209], v[38:41]
	v_mfma_f32_16x16x32_bf16 v[34:37], v[182:185], v[206:209], v[34:37]
	v_mfma_f32_16x16x32_bf16 v[22:25], v[174:177], v[214:217], v[22:25]
	v_mfma_f32_16x16x32_bf16 v[18:21], v[182:185], v[214:217], v[18:21]
	s_setprio 0
	s_barrier
	s_add_i32 s87, s87, 2
	s_add_u32 s85, s85, 0x100
	s_addc_u32 s86, s86, 0
	s_add_u32 s56, s56, 0x100
	s_addc_u32 s57, s57, 0
	s_cmp_gt_u32 s87, 5
	s_cbranch_scc0 .LBB0_1498
	s_and_b64 vcc, exec, s[18:19]
	s_cbranch_vccz .LBB0_1501
	s_barrier

; #define PG8_STAGE(bufoff, gbase, voff) do { _Pragma("unroll") for (int _i = 0; _i < 2; ++_i) \
;         __builtin_amdgcn_global_load_lds((const unsigned*)((const char*)(gbase) + (voff)[_i]), (PG8_LAS unsigned*)(lds + (bufoff) + ldsw + _i * 8192), 16, 0, 0); } while (0)
; #define PG8_LDA(dst, b, h) do { _Pragma("unroll") for (int m = 0; m < 4; ++m) _Pragma("unroll") for (int k = 0; k < 2; ++k) dst[m][k] = *(const PG8_LAS bf16x8*)(lds + PG8_SA(b, h) + aoff + m * 2048 + k * 1024); } while (0)
; #define PG8_LDB(dst, b, h) do { _Pragma("unroll") for (int n = 0; n < 2; ++n) _Pragma("unroll") for (int k = 0; k < 2; ++k) dst[n][k] = *(const PG8_LAS bf16x8*)(lds + PG8_SB(b, h) + boff + n * 2048 + k * 1024); } while (0)
; #define PG8_MMA(ai, bj, At, Bt) do { __builtin_amdgcn_s_setprio(1); _Pragma("unroll") for (int m = 0; m < 4; ++m) _Pragma("unroll") for (int n = 0; n < 2; ++n) _Pragma("unroll") for (int k = 0; k < 2; ++k) \
;         acc[ai][bj][m][n] = __builtin_amdgcn_mfma_f32_16x16x32_bf16(Bt[n][k], At[m][k], acc[ai][bj][m][n], 0, 0, 0); __builtin_amdgcn_s_setprio(0); } while (0)
; template <class Epi, class Sched, bool ALIGN_EPI = false>
; __device__ __forceinline__ void gemm_phase(PG8_LAS unsigned char* lds, const Gemm g, const Sched& S, const Epi& E) {
;     ...
;         for (int t = 0; t < nt; t += 2) {
;             const bool last = (t == nt - 2);
;             const char* a1 = cA + (size_t)(t + 1) * kstep;
;             const char* a2 = last ? nA : cA + (size_t)(t + 2) * kstep; const char* b2 = last ? nB : cB + (size_t)(t + 2) * kstep;
;             const char* a3 = a2 + kstep; const char* b3 = b2 + kstep;
;             unsigned w0[2], w1[2];
; #pragma unroll
;             for (int i = 0; i < 2; ++i) { w0[i] = (Sched::GATHER && last) ? vn0[i] : vc0[i]; w1[i] = (Sched::GATHER && last) ? vn1[i] : vc1[i]; }
;             if (last && has_next) S.a_ready(nxt);
;             PG8_LDB(B0, 0, 0); PG8_LDB(B1, 0, 1); PG8_SCHED; PG8_LDA(At, 0, 0); PG8_STAGE(PG8_SA(1, 1), a1 + hstepA, vc1);
;             PG8_WAIT_V(8); PG8_WAIT_L(0); PG8_BAR; PG8_MMA(0, 0, At, B0); PG8_MMA(0, 1, At, B1); PG8_BAR; PG8_SCHED;
;             PG8_LDA(At, 0, 1); PG8_STAGE(PG8_SB(0, 0), b2, voffB); PG8_STAGE(PG8_SB(0, 1), b2 + hstep, voffB); PG8_STAGE(PG8_SA(0, 0), a2, w0);
;             PG8_WAIT_V(8); PG8_WAIT_L(0); PG8_BAR; PG8_MMA(1, 0, At, B0); PG8_MMA(1, 1, At, B1); PG8_BAR; PG8_SCHED;
.LBB0_1601:
	ds_read_b128 v[144:147], v157
	ds_read_b128 v[160:163], v157 offset:1024
	ds_read_b128 v[164:167], v157 offset:2048
	ds_read_b128 v[168:171], v157 offset:3072
	ds_read_b128 v[172:175], v158
	ds_read_b128 v[176:179], v158 offset:1024
	ds_read_b128 v[180:183], v158 offset:2048
	ds_read_b128 v[184:187], v158 offset:3072
	s_add_u32 s54, s52, 0xfffe0080
	s_addc_u32 s55, s53, -1
	s_cmp_eq_u32 s87, 4
	s_cselect_b32 s57, s25, s55
	s_cselect_b32 s56, s43, s54
	s_cselect_b32 s55, s27, s86
	s_cselect_b32 s54, s84, s85
	v_lshl_add_u64 v[220:221], s[52:53], 0, v[142:143]
	s_add_i32 m0, s45, 0xc000
	ds_read_b128 v[188:191], v159
	ds_read_b128 v[192:195], v159 offset:1024
	ds_read_b128 v[196:199], v159 offset:2048
	ds_read_b128 v[200:203], v159 offset:3072
	ds_read_b128 v[204:207], v159 offset:4096
	ds_read_b128 v[208:211], v159 offset:5120
	ds_read_b128 v[212:215], v159 offset:6144
	ds_read_b128 v[216:219], v159 offset:7168
	global_load_lds_dwordx4 v[220:221], off
	v_lshl_add_u64 v[220:221], s[52:53], 0, v[140:141]
	s_add_i32 m0, s45, 0xe000
	s_nop 0
	global_load_lds_dwordx4 v[220:221], off
	s_waitcnt vmcnt(8)
	s_waitcnt lgkmcnt(0)
	s_barrier
	s_setprio 1
	v_mfma_f32_16x16x32_bf16 v[126:129], v[144:147], v[188:191], v[126:129]
	v_mfma_f32_16x16x32_bf16 v[122:125], v[164:167], v[188:191], v[122:125]
	v_mfma_f32_16x16x32_bf16 v[114:117], v[144:147], v[196:199], v[114:117]
	v_mfma_f32_16x16x32_bf16 v[106:109], v[164:167], v[196:199], v[106:109]
	v_mfma_f32_16x16x32_bf16 v[98:101], v[144:147], v[204:207], v[98:101]
	v_mfma_f32_16x16x32_bf16 v[90:93], v[164:167], v[204:207], v[90:93]
	v_mfma_f32_16x16x32_bf16 v[82:85], v[144:147], v[212:215], v[82:85]
	v_mfma_f32_16x16x32_bf16 v[74:77], v[164:167], v[212:215], v[74:77]
	v_mfma_f32_16x16x32_bf16 v[126:129], v[160:163], v[192:195], v[126:129]
	v_mfma_f32_16x16x32_bf16 v[122:125], v[168:171], v[192:195], v[122:125]
	v_mfma_f32_16x16x32_bf16 v[114:117], v[160:163], v[200:203], v[114:117]
	v_mfma_f32_16x16x32_bf16 v[106:109], v[168:171], v[200:203], v[106:109]
	v_mfma_f32_16x16x32_bf16 v[98:101], v[160:163], v[208:211], v[98:101]
	v_mfma_f32_16x16x32_bf16 v[90:93], v[168:171], v[208:211], v[90:93]
	v_mfma_f32_16x16x32_bf16 v[82:85], v[160:163], v[216:219], v[82:85]
	v_mfma_f32_16x16x32_bf16 v[74:77], v[168:171], v[216:219], v[74:77]
	v_mfma_f32_16x16x32_bf16 v[118:121], v[172:175], v[188:191], v[118:121]
	v_mfma_f32_16x16x32_bf16 v[110:113], v[180:183], v[188:191], v[110:113]
	v_mfma_f32_16x16x32_bf16 v[102:105], v[172:175], v[196:199], v[102:105]
	v_mfma_f32_16x16x32_bf16 v[94:97], v[180:183], v[196:199], v[94:97]
	v_mfma_f32_16x16x32_bf16 v[86:89], v[172:175], v[204:207], v[86:89]
	v_mfma_f32_16x16x32_bf16 v[78:81], v[180:183], v[204:207], v[78:81]
	v_mfma_f32_16x16x32_bf16 v[62:65], v[172:175], v[212:215], v[62:65]
	v_mfma_f32_16x16x32_bf16 v[58:61], v[180:183], v[212:215], v[58:61]
	v_mfma_f32_16x16x32_bf16 v[118:121], v[176:179], v[192:195], v[118:121]
	v_mfma_f32_16x16x32_bf16 v[110:113], v[184:187], v[192:195], v[110:113]
	v_mfma_f32_16x16x32_bf16 v[102:105], v[176:179], v[200:203], v[102:105]
	v_mfma_f32_16x16x32_bf16 v[94:97], v[184:187], v[200:203], v[94:97]
	v_mfma_f32_16x16x32_bf16 v[86:89], v[176:179], v[208:211], v[86:89]
	v_mfma_f32_16x16x32_bf16 v[78:81], v[184:187], v[208:211], v[78:81]
	v_mfma_f32_16x16x32_bf16 v[62:65], v[176:179], v[216:219], v[62:65]
	v_mfma_f32_16x16x32_bf16 v[58:61], v[184:187], v[216:219], v[58:61]
	s_setprio 0
	s_barrier
	s_add_i32 s88, s74, s62
	v_lshl_add_u64 v[220:221], s[54:55], 0, v[134:135]
	s_mov_b32 m0, s88
	ds_read_b128 v[188:191], v159 offset:16384
	ds_read_b128 v[192:195], v159 offset:17408
	ds_read_b128 v[196:199], v159 offset:18432
	ds_read_b128 v[200:203], v159 offset:19456
	ds_read_b128 v[204:207], v159 offset:20480
	ds_read_b128 v[208:211], v159 offset:21504
	ds_read_b128 v[212:215], v159 offset:22528
	ds_read_b128 v[216:219], v159 offset:23552
	global_load_lds_dwordx4 v[220:221], off
	s_add_i32 m0, s88, 0x2000
	s_add_u32 s88, s54, 0x20000
	v_lshl_add_u64 v[222:223], s[54:55], 0, v[138:139]
	s_addc_u32 s89, s55, 0
	s_add_i32 s90, s75, s62
	global_load_lds_dwordx4 v[222:223], off
	v_lshl_add_u64 v[224:225], s[88:89], 0, v[134:135]
	s_mov_b32 m0, s90
	v_lshl_add_u64 v[226:227], s[56:57], 0, v[136:137]
	global_load_lds_dwordx4 v[224:225], off
	v_lshl_add_u64 v[224:225], s[88:89], 0, v[138:139]
	s_add_i32 m0, s90, 0x2000
	s_nop 0
	global_load_lds_dwordx4 v[224:225], off
	v_lshl_add_u64 v[224:225], s[56:57], 0, v[132:133]
	s_mov_b32 m0, s45
	s_nop 0
	global_load_lds_dwordx4 v[224:225], off
	s_mov_b32 m0, s63
	s_nop 0
	global_load_lds_dwordx4 v[226:227], off
	s_waitcnt vmcnt(8)
	s_waitcnt lgkmcnt(0)
	s_barrier
; #define PG8_STAGE(bufoff, gbase, voff) do { _Pragma("unroll") for (int _i = 0; _i < 2; ++_i) \
;         __builtin_amdgcn_global_load_lds((const unsigned*)((const char*)(gbase) + (voff)[_i]), (PG8_LAS unsigned*)(lds + (bufoff) + ldsw + _i * 8192), 16, 0, 0); } while (0)
; #define PG8_LDA(dst, b, h) do { _Pragma("unroll") for (int m = 0; m < 4; ++m) _Pragma("unroll") for (int k = 0; k < 2; ++k) dst[m][k] = *(const PG8_LAS bf16x8*)(lds + PG8_SA(b, h) + aoff + m * 2048 + k * 1024); } while (0)
; #define PG8_LDB(dst, b, h) do { _Pragma("unroll") for (int n = 0; n < 2; ++n) _Pragma("unroll") for (int k = 0; k < 2; ++k) dst[n][k] = *(const PG8_LAS bf16x8*)(lds + PG8_SB(b, h) + boff + n * 2048 + k * 1024); } while (0)
; #define PG8_MMA(ai, bj, At, Bt) do { __builtin_amdgcn_s_setprio(1); _Pragma("unroll") for (int m = 0; m < 4; ++m) _Pragma("unroll") for (int n = 0; n < 2; ++n) _Pragma("unroll") for (int k = 0; k < 2; ++k) \
;         acc[ai][bj][m][n] = __builtin_amdgcn_mfma_f32_16x16x32_bf16(Bt[n][k], At[m][k], acc[ai][bj][m][n], 0, 0, 0); __builtin_amdgcn_s_setprio(0); } while (0)
; #define PG8_WAIT_V(n) asm volatile("s_waitcnt vmcnt(" #n ")" ::: "memory")
; #define PG8_WAIT_L(n) asm volatile("s_waitcnt lgkmcnt(" #n ")" ::: "memory")
; #define PG8_BAR __builtin_amdgcn_s_barrier()
; #define PG8_SCHED __builtin_amdgcn_sched_barrier(0)
; template <class Epi, class Sched, bool ALIGN_EPI = false>
; __device__ __forceinline__ void gemm_phase(PG8_LAS unsigned char* lds, const Gemm g, const Sched& S, const Epi& E) {
;     ...
;             PG8_WAIT_V(8); PG8_WAIT_L(0); PG8_BAR; PG8_MMA(1, 0, At, B0); PG8_MMA(1, 1, At, B1); PG8_BAR; PG8_SCHED;
;             PG8_LDB(B0, 1, 0); PG8_LDB(B1, 1, 1); PG8_SCHED; PG8_LDA(At, 1, 0); PG8_STAGE(PG8_SA(0, 1), a2 + hstepA, w1);
;             PG8_WAIT_V(8); PG8_WAIT_L(0); PG8_BAR; PG8_MMA(0, 0, At, B0); PG8_MMA(0, 1, At, B1); PG8_BAR; PG8_SCHED;
	s_setprio 1
	v_mfma_f32_16x16x32_bf16 v[54:57], v[144:147], v[188:191], v[54:57]
	v_mfma_f32_16x16x32_bf16 v[42:45], v[164:167], v[188:191], v[42:45]
	v_mfma_f32_16x16x32_bf16 v[30:33], v[144:147], v[196:199], v[30:33]
	v_mfma_f32_16x16x32_bf16 v[26:29], v[164:167], v[196:199], v[26:29]
	v_mfma_f32_16x16x32_bf16 v[14:17], v[144:147], v[204:207], v[14:17]
	v_mfma_f32_16x16x32_bf16 v[10:13], v[164:167], v[204:207], v[10:13]
	v_mfma_f32_16x16x32_bf16 v[6:9], v[144:147], v[212:215], v[6:9]
	v_mfma_f32_16x16x32_bf16 v[2:5], v[164:167], v[212:215], v[2:5]
	v_mfma_f32_16x16x32_bf16 v[54:57], v[160:163], v[192:195], v[54:57]
	v_mfma_f32_16x16x32_bf16 v[42:45], v[168:171], v[192:195], v[42:45]
	v_mfma_f32_16x16x32_bf16 v[30:33], v[160:163], v[200:203], v[30:33]
	v_mfma_f32_16x16x32_bf16 v[26:29], v[168:171], v[200:203], v[26:29]
	v_mfma_f32_16x16x32_bf16 v[14:17], v[160:163], v[208:211], v[14:17]
	v_mfma_f32_16x16x32_bf16 v[10:13], v[168:171], v[208:211], v[10:13]
	v_mfma_f32_16x16x32_bf16 v[6:9], v[160:163], v[216:219], v[6:9]
	v_mfma_f32_16x16x32_bf16 v[2:5], v[168:171], v[216:219], v[2:5]
	v_mfma_f32_16x16x32_bf16 v[70:73], v[172:175], v[188:191], v[70:73]
	v_mfma_f32_16x16x32_bf16 v[66:69], v[180:183], v[188:191], v[66:69]
	v_mfma_f32_16x16x32_bf16 v[50:53], v[172:175], v[196:199], v[50:53]
	v_mfma_f32_16x16x32_bf16 v[46:49], v[180:183], v[196:199], v[46:49]
	v_mfma_f32_16x16x32_bf16 v[38:41], v[172:175], v[204:207], v[38:41]
	v_mfma_f32_16x16x32_bf16 v[34:37], v[180:183], v[204:207], v[34:37]
	v_mfma_f32_16x16x32_bf16 v[22:25], v[172:175], v[212:215], v[22:25]
	v_mfma_f32_16x16x32_bf16 v[18:21], v[180:183], v[212:215], v[18:21]
	v_mfma_f32_16x16x32_bf16 v[70:73], v[176:179], v[192:195], v[70:73]
	v_mfma_f32_16x16x32_bf16 v[66:69], v[184:187], v[192:195], v[66:69]
	v_mfma_f32_16x16x32_bf16 v[50:53], v[176:179], v[200:203], v[50:53]
	v_mfma_f32_16x16x32_bf16 v[46:49], v[184:187], v[200:203], v[46:49]
	v_mfma_f32_16x16x32_bf16 v[38:41], v[176:179], v[208:211], v[38:41]
	v_mfma_f32_16x16x32_bf16 v[34:37], v[184:187], v[208:211], v[34:37]
	v_mfma_f32_16x16x32_bf16 v[22:25], v[176:179], v[216:219], v[22:25]
	v_mfma_f32_16x16x32_bf16 v[18:21], v[184:187], v[216:219], v[18:21]
	s_setprio 0
	s_barrier
	s_add_i32 s88, 0, 0x18000
	s_add_i32 s89, 0, 0x1c000
	v_add_u32_e32 v168, s88, v148
	v_add_u32_e32 v184, s89, v148
	ds_read_b128 v[144:147], v168
	ds_read_b128 v[160:163], v168 offset:1024
	ds_read_b128 v[164:167], v168 offset:2048
	ds_read_b128 v[168:171], v168 offset:3072
	ds_read_b128 v[172:175], v184
	ds_read_b128 v[176:179], v184 offset:1024
	ds_read_b128 v[180:183], v184 offset:2048
	ds_read_b128 v[184:187], v184 offset:3072
	s_add_u32 s56, s56, 0x20000
	s_addc_u32 s57, s57, 0
	s_mov_b32 m0, s64
	v_lshl_add_u64 v[228:229], s[56:57], 0, v[132:133]
	ds_read_b128 v[188:191], v159 offset:32768
	ds_read_b128 v[192:195], v159 offset:33792
	ds_read_b128 v[196:199], v159 offset:34816
	ds_read_b128 v[200:203], v159 offset:35840
	ds_read_b128 v[204:207], v159 offset:36864
	ds_read_b128 v[208:211], v159 offset:37888
	ds_read_b128 v[212:215], v159 offset:38912
	ds_read_b128 v[216:219], v159 offset:39936
	global_load_lds_dwordx4 v[228:229], off
	v_lshl_add_u64 v[228:229], s[56:57], 0, v[136:137]
	s_mov_b32 m0, s65
	s_nop 0
	global_load_lds_dwordx4 v[228:229], off
	s_waitcnt vmcnt(8)
	s_waitcnt lgkmcnt(0)
	s_barrier
	s_setprio 1
	v_mfma_f32_16x16x32_bf16 v[126:129], v[144:147], v[188:191], v[126:129]
	v_mfma_f32_16x16x32_bf16 v[122:125], v[164:167], v[188:191], v[122:125]
	v_mfma_f32_16x16x32_bf16 v[114:117], v[144:147], v[196:199], v[114:117]
	v_mfma_f32_16x16x32_bf16 v[106:109], v[164:167], v[196:199], v[106:109]
	v_mfma_f32_16x16x32_bf16 v[98:101], v[144:147], v[204:207], v[98:101]
	v_mfma_f32_16x16x32_bf16 v[90:93], v[164:167], v[204:207], v[90:93]
	v_mfma_f32_16x16x32_bf16 v[82:85], v[144:147], v[212:215], v[82:85]
	v_mfma_f32_16x16x32_bf16 v[74:77], v[164:167], v[212:215], v[74:77]
	v_mfma_f32_16x16x32_bf16 v[126:129], v[160:163], v[192:195], v[126:129]
	v_mfma_f32_16x16x32_bf16 v[122:125], v[168:171], v[192:195], v[122:125]
	v_mfma_f32_16x16x32_bf16 v[114:117], v[160:163], v[200:203], v[114:117]
	v_mfma_f32_16x16x32_bf16 v[106:109], v[168:171], v[200:203], v[106:109]
	v_mfma_f32_16x16x32_bf16 v[98:101], v[160:163], v[208:211], v[98:101]
	v_mfma_f32_16x16x32_bf16 v[90:93], v[168:171], v[208:211], v[90:93]
	v_mfma_f32_16x16x32_bf16 v[82:85], v[160:163], v[216:219], v[82:85]
	v_mfma_f32_16x16x32_bf16 v[74:77], v[168:171], v[216:219], v[74:77]
	v_mfma_f32_16x16x32_bf16 v[118:121], v[172:175], v[188:191], v[118:121]
	v_mfma_f32_16x16x32_bf16 v[110:113], v[180:183], v[188:191], v[110:113]
	v_mfma_f32_16x16x32_bf16 v[102:105], v[172:175], v[196:199], v[102:105]
	v_mfma_f32_16x16x32_bf16 v[94:97], v[180:183], v[196:199], v[94:97]
	v_mfma_f32_16x16x32_bf16 v[86:89], v[172:175], v[204:207], v[86:89]
	v_mfma_f32_16x16x32_bf16 v[78:81], v[180:183], v[204:207], v[78:81]
	v_mfma_f32_16x16x32_bf16 v[62:65], v[172:175], v[212:215], v[62:65]
	v_mfma_f32_16x16x32_bf16 v[58:61], v[180:183], v[212:215], v[58:61]
	v_mfma_f32_16x16x32_bf16 v[118:121], v[176:179], v[192:195], v[118:121]
	v_mfma_f32_16x16x32_bf16 v[110:113], v[184:187], v[192:195], v[110:113]
	v_mfma_f32_16x16x32_bf16 v[102:105], v[176:179], v[200:203], v[102:105]
	v_mfma_f32_16x16x32_bf16 v[94:97], v[184:187], v[200:203], v[94:97]
	v_mfma_f32_16x16x32_bf16 v[86:89], v[176:179], v[208:211], v[86:89]
	v_mfma_f32_16x16x32_bf16 v[78:81], v[184:187], v[208:211], v[78:81]
	v_mfma_f32_16x16x32_bf16 v[62:65], v[176:179], v[216:219], v[62:65]
	v_mfma_f32_16x16x32_bf16 v[58:61], v[184:187], v[216:219], v[58:61]
	s_setprio 0
	s_barrier
; #define PG8_STAGE(bufoff, gbase, voff) do { _Pragma("unroll") for (int _i = 0; _i < 2; ++_i) \
;         __builtin_amdgcn_global_load_lds((const unsigned*)((const char*)(gbase) + (voff)[_i]), (PG8_LAS unsigned*)(lds + (bufoff) + ldsw + _i * 8192), 16, 0, 0); } while (0)
; #define PG8_LDA(dst, b, h) do { _Pragma("unroll") for (int m = 0; m < 4; ++m) _Pragma("unroll") for (int k = 0; k < 2; ++k) dst[m][k] = *(const PG8_LAS bf16x8*)(lds + PG8_SA(b, h) + aoff + m * 2048 + k * 1024); } while (0)
; #define PG8_MMA(ai, bj, At, Bt) do { __builtin_amdgcn_s_setprio(1); _Pragma("unroll") for (int m = 0; m < 4; ++m) _Pragma("unroll") for (int n = 0; n < 2; ++n) _Pragma("unroll") for (int k = 0; k < 2; ++k) \
;         acc[ai][bj][m][n] = __builtin_amdgcn_mfma_f32_16x16x32_bf16(Bt[n][k], At[m][k], acc[ai][bj][m][n], 0, 0, 0); __builtin_amdgcn_s_setprio(0); } while (0)
; #define PG8_WAIT_V(n) asm volatile("s_waitcnt vmcnt(" #n ")" ::: "memory")
; #define PG8_WAIT_L(n) asm volatile("s_waitcnt lgkmcnt(" #n ")" ::: "memory")
; #define PG8_BAR __builtin_amdgcn_s_barrier()
; #define PG8_SCHED __builtin_amdgcn_sched_barrier(0)
; template <class Epi, class Sched, bool ALIGN_EPI = false>
; __device__ __forceinline__ void gemm_phase(PG8_LAS unsigned char* lds, const Gemm g, const Sched& S, const Epi& E) {
;     ...
;             PG8_LDA(At, 1, 1); PG8_STAGE(PG8_SB(1, 0), b3, voffB); PG8_STAGE(PG8_SB(1, 1), b3 + hstep, voffB); PG8_STAGE(PG8_SA(1, 0), a3, w0);
;             PG8_WAIT_V(8); PG8_WAIT_L(0); PG8_BAR; PG8_MMA(1, 0, At, B0); PG8_MMA(1, 1, At, B1); PG8_BAR; PG8_SCHED;
;             if constexpr (Epi::KSCALE) { if (((t + 2) & 7) == 0 && t + 2 < nt) { E.kscale(acc, pf, ((t + 2) >> 3) - 1, wr, fr); PG8_SCHED; } }
;         }
;         if constexpr (ALIGN_EPI) { if (wr == 0) PG8_BAR; }
	s_add_i32 s56, s88, s62
	v_lshl_add_u64 v[220:221], v[220:221], 0, s[12:13]
	s_mov_b32 m0, s56
	ds_read_b128 v[188:191], v159 offset:49152
	ds_read_b128 v[192:195], v159 offset:50176
	ds_read_b128 v[196:199], v159 offset:51200
	ds_read_b128 v[200:203], v159 offset:52224
	ds_read_b128 v[204:207], v159 offset:53248
	ds_read_b128 v[208:211], v159 offset:54272
	ds_read_b128 v[212:215], v159 offset:55296
	ds_read_b128 v[216:219], v159 offset:56320
	global_load_lds_dwordx4 v[220:221], off
	s_add_i32 m0, s56, 0x2000
	s_add_u32 s54, s54, 0x20080
	v_lshl_add_u64 v[220:221], v[222:223], 0, s[12:13]
	s_addc_u32 s55, s55, 0
	s_add_i32 s56, s89, s62
	global_load_lds_dwordx4 v[220:221], off
	v_lshl_add_u64 v[220:221], s[54:55], 0, v[134:135]
	s_mov_b32 m0, s56
	s_nop 0
	global_load_lds_dwordx4 v[220:221], off
	v_lshl_add_u64 v[220:221], s[54:55], 0, v[138:139]
	s_add_i32 m0, s56, 0x2000
	s_nop 0
	global_load_lds_dwordx4 v[220:221], off
	v_lshl_add_u64 v[220:221], v[224:225], 0, s[12:13]
	s_mov_b32 m0, s68
	s_nop 0
	global_load_lds_dwordx4 v[220:221], off
	v_lshl_add_u64 v[220:221], v[226:227], 0, s[12:13]
	s_mov_b32 m0, s69
	s_nop 0
	global_load_lds_dwordx4 v[220:221], off
	s_waitcnt vmcnt(8)
	s_waitcnt lgkmcnt(0)
	s_barrier
	s_setprio 1
	v_mfma_f32_16x16x32_bf16 v[54:57], v[144:147], v[188:191], v[54:57]
	v_mfma_f32_16x16x32_bf16 v[42:45], v[164:167], v[188:191], v[42:45]
	v_mfma_f32_16x16x32_bf16 v[30:33], v[144:147], v[196:199], v[30:33]
	v_mfma_f32_16x16x32_bf16 v[26:29], v[164:167], v[196:199], v[26:29]
	v_mfma_f32_16x16x32_bf16 v[14:17], v[144:147], v[204:207], v[14:17]
	v_mfma_f32_16x16x32_bf16 v[10:13], v[164:167], v[204:207], v[10:13]
	v_mfma_f32_16x16x32_bf16 v[6:9], v[144:147], v[212:215], v[6:9]
	v_mfma_f32_16x16x32_bf16 v[2:5], v[164:167], v[212:215], v[2:5]
	v_mfma_f32_16x16x32_bf16 v[54:57], v[160:163], v[192:195], v[54:57]
	v_mfma_f32_16x16x32_bf16 v[42:45], v[168:171], v[192:195], v[42:45]
	v_mfma_f32_16x16x32_bf16 v[30:33], v[160:163], v[200:203], v[30:33]
	v_mfma_f32_16x16x32_bf16 v[26:29], v[168:171], v[200:203], v[26:29]
	v_mfma_f32_16x16x32_bf16 v[14:17], v[160:163], v[208:211], v[14:17]
	v_mfma_f32_16x16x32_bf16 v[10:13], v[168:171], v[208:211], v[10:13]
	v_mfma_f32_16x16x32_bf16 v[6:9], v[160:163], v[216:219], v[6:9]
	v_mfma_f32_16x16x32_bf16 v[2:5], v[168:171], v[216:219], v[2:5]
	v_mfma_f32_16x16x32_bf16 v[70:73], v[172:175], v[188:191], v[70:73]
	v_mfma_f32_16x16x32_bf16 v[66:69], v[180:183], v[188:191], v[66:69]
	v_mfma_f32_16x16x32_bf16 v[50:53], v[172:175], v[196:199], v[50:53]
	v_mfma_f32_16x16x32_bf16 v[46:49], v[180:183], v[196:199], v[46:49]
	v_mfma_f32_16x16x32_bf16 v[38:41], v[172:175], v[204:207], v[38:41]
	v_mfma_f32_16x16x32_bf16 v[34:37], v[180:183], v[204:207], v[34:37]
	v_mfma_f32_16x16x32_bf16 v[22:25], v[172:175], v[212:215], v[22:25]
	v_mfma_f32_16x16x32_bf16 v[18:21], v[180:183], v[212:215], v[18:21]
	v_mfma_f32_16x16x32_bf16 v[70:73], v[176:179], v[192:195], v[70:73]
	v_mfma_f32_16x16x32_bf16 v[66:69], v[184:187], v[192:195], v[66:69]
	v_mfma_f32_16x16x32_bf16 v[50:53], v[176:179], v[200:203], v[50:53]
	v_mfma_f32_16x16x32_bf16 v[46:49], v[184:187], v[200:203], v[46:49]
	v_mfma_f32_16x16x32_bf16 v[38:41], v[176:179], v[208:211], v[38:41]
	v_mfma_f32_16x16x32_bf16 v[34:37], v[184:187], v[208:211], v[34:37]
	v_mfma_f32_16x16x32_bf16 v[22:25], v[176:179], v[216:219], v[22:25]
	v_mfma_f32_16x16x32_bf16 v[18:21], v[184:187], v[216:219], v[18:21]
	s_setprio 0
	s_barrier
	s_add_i32 s87, s87, 2
	s_add_u32 s85, s85, 0x100
	s_addc_u32 s86, s86, 0
	s_add_u32 s52, s52, 0x100
	s_addc_u32 s53, s53, 0
	s_cmp_gt_u32 s87, 5
	s_cbranch_scc0 .LBB0_1601
	s_and_b64 vcc, exec, s[14:15]
	s_cbranch_vccz .LBB0_1604
	s_barrier
